# gdn_prep: forward-substitution FMAs paired into packed f32 FMAs; next conv blocks' activation lines touched early
# baseline (speedup 1.0000x reference)
.LBB0_264:
	v_mov_b32_e32 v1, s31
	ds_read_b64 v[4:5], v1
	v_ashrrev_i32_e32 v1, 3, v20
	v_add_u32_e32 v32, s18, v1
	v_lshlrev_b32_e32 v2, 4, v20
	v_cmp_lt_i32_e32 vcc, 2, v32
	v_and_b32_e32 v23, 0x70, v2
	v_add_u32_e32 v36, s14, v1
	v_cndmask_b32_e64 v2, 0, -3, vcc
	s_waitcnt lgkmcnt(0)
	v_lshl_add_u64 v[30:31], v[4:5], 0, s[10:11]
	v_add_u32_e32 v2, v2, v36
	v_mov_b64_e32 v[4:5], s[0:1]
	s_movk_i32 s18, 0x7200
	v_mad_i64_i32 v[6:7], s[0:1], v2, s18, v[4:5]
	v_cmp_lt_i32_e64 s[0:1], 1, v32
	s_lshl_b32 s35, s17, 7
	s_mov_b64 s[38:39], 0x1c00
	v_cndmask_b32_e64 v2, 0, -2, s[0:1]
	v_add_u32_e32 v2, v2, v36
	v_or_b32_e32 v21, s35, v23
	v_lshl_add_u64 v[24:25], v[6:7], 0, s[38:39]
	v_mad_i64_i32 v[6:7], s[4:5], v2, s18, v[4:5]
	v_lshlrev_b32_e32 v2, 2, v21
	v_lshl_add_u64 v[42:43], v[30:31], 0, v[2:3]
	s_movk_i32 s21, 0x1000
	v_add_co_u32_e64 v8, s[4:5], s21, v42
	s_movk_i32 s19, 0x3000
	s_nop 0
	v_addc_co_u32_e64 v9, s[4:5], 0, v43, s[4:5]
	v_add_co_u32_e64 v44, s[4:5], s19, v42
	s_movk_i32 s17, 0x4000
	s_nop 0
	v_addc_co_u32_e64 v45, s[4:5], 0, v43, s[4:5]
	v_add_co_u32_e64 v10, s[4:5], s17, v42
	v_lshl_add_u64 v[28:29], v[6:7], 0, s[38:39]
	s_nop 0
	v_addc_co_u32_e64 v11, s[4:5], 0, v43, s[4:5]
	v_cmp_lt_i32_e64 s[4:5], 0, v32
	global_load_dwordx4 v[46:49], v[42:43], off
	global_load_dwordx4 v[50:53], v[8:9], off offset:2048
	v_cndmask_b32_e64 v26, 0, 1.0, s[4:5]
	v_subbrev_co_u32_e64 v2, s[4:5], 0, v36, s[4:5]
	v_mad_i64_i32 v[6:7], s[4:5], v2, s18, v[4:5]
	v_lshlrev_b32_e32 v2, 1, v21
	global_load_dwordx4 v[54:57], v[42:43], off offset:16
	global_load_dwordx4 v[58:61], v[44:45], off
	global_load_dwordx4 v[62:65], v[10:11], off offset:2048
	global_load_dwordx4 v[66:69], v[8:9], off offset:2064
	global_load_dwordx4 v[70:73], v[44:45], off offset:16
	global_load_dwordx4 v[74:77], v[10:11], off offset:2064
	global_load_dwordx4 v[78:81], v[42:43], off offset:32
	global_load_dwordx4 v[82:85], v[8:9], off offset:2080
	global_load_dwordx4 v[86:89], v[44:45], off offset:32
	global_load_dwordx4 v[90:93], v[10:11], off offset:2080
	global_load_dwordx4 v[94:97], v[42:43], off offset:48
	v_lshl_add_u64 v[34:35], v[6:7], 0, s[38:39]
	global_load_dwordx4 v[98:101], v[8:9], off offset:2096
	global_load_dwordx4 v[102:105], v[44:45], off offset:48
	v_lshl_add_u64 v[110:111], v[24:25], 0, v[2:3]
	global_load_dwordx4 v[106:109], v[10:11], off offset:2096
	global_load_dwordx4 v[16:19], v[110:111], off offset:16
	v_lshl_add_u64 v[114:115], v[28:29], 0, v[2:3]
	v_mad_i64_i32 v[4:5], s[4:5], v36, s18, v[4:5]
	global_load_dwordx4 v[12:15], v[114:115], off offset:16
	v_lshl_add_u64 v[118:119], v[34:35], 0, v[2:3]
	v_lshl_add_u64 v[40:41], v[4:5], 0, s[38:39]
	global_load_dwordx4 v[8:11], v[118:119], off offset:16
	v_lshl_add_u64 v[122:123], v[40:41], 0, v[2:3]
	global_load_dwordx4 v[4:7], v[122:123], off offset:16
	global_load_dword v206, v[110:111], off offset:1024
	global_load_dword v206, v[114:115], off offset:1024
	global_load_dword v206, v[118:119], off offset:1024
	global_load_dword v206, v[122:123], off offset:1024
	global_load_dword v207, v[110:111], off offset:2048
	global_load_dword v207, v[114:115], off offset:2048
	global_load_dword v207, v[118:119], off offset:2048
	global_load_dword v207, v[122:123], off offset:2048
	s_nop 0
	global_load_dwordx4 v[110:113], v[110:111], off
	s_nop 0
	global_load_dwordx4 v[114:117], v[114:115], off
	s_nop 0
	global_load_dwordx4 v[118:121], v[118:119], off
	s_nop 0
	global_load_dwordx4 v[122:125], v[122:123], off
	v_cndmask_b32_e64 v38, 0, 1.0, vcc
	v_cndmask_b32_e64 v36, 0, 1.0, s[0:1]
	v_cmp_lt_i32_e64 s[4:5], -1, v32
	s_mov_b32 s0, 0x800000
	s_movk_i32 s1, 0x2000
	v_cndmask_b32_e64 v32, 0, 1.0, s[4:5]
	v_or_b32_e32 v2, 0x400, v2
	s_movk_i32 s45, 0x7200
	s_mov_b32 s43, 0x800000
	s_waitcnt vmcnt(0) lgkmcnt(0)
	v_pk_mul_f32 v[128:129], v[38:39], v[46:47] op_sel_hi:[0,1]
	v_pk_mul_f32 v[134:135], v[36:37], v[52:53] op_sel_hi:[0,1]
	v_pk_mul_f32 v[136:137], v[36:37], v[50:51] op_sel_hi:[0,1]
	v_pk_mul_f32 v[126:127], v[38:39], v[48:49] op_sel_hi:[0,1]
	v_pk_mul_f32 v[130:131], v[38:39], v[56:57] op_sel_hi:[0,1]
	v_pk_mul_f32 v[132:133], v[38:39], v[54:55] op_sel_hi:[0,1]
	v_pk_mul_f32 v[68:69], v[36:37], v[68:69] op_sel_hi:[0,1]
	v_pk_mul_f32 v[66:67], v[36:37], v[66:67] op_sel_hi:[0,1]
	v_pk_mul_f32 v[52:53], v[38:39], v[80:81] op_sel_hi:[0,1]
	v_pk_mul_f32 v[56:57], v[36:37], v[82:83] op_sel_hi:[0,1]
	v_pk_mul_f32 v[80:81], v[38:39], v[96:97] op_sel_hi:[0,1]
	v_pk_mul_f32 v[82:83], v[38:39], v[94:95] op_sel_hi:[0,1]
	v_pk_mul_f32 v[54:55], v[26:27], v[86:87] op_sel_hi:[0,1]
	v_pk_mul_f32 v[86:87], v[36:37], v[98:99] op_sel_hi:[0,1]
	v_pk_mul_f32 v[46:47], v[32:33], v[92:93] op_sel_hi:[0,1]
	v_and_b32_e32 v97, 0xffff0000, v18
	v_lshlrev_b32_e32 v96, 16, v18
	v_pk_fma_f32 v[82:83], v[82:83], v[96:97], 0 op_sel_hi:[1,1,0]
	v_pk_mul_f32 v[92:93], v[26:27], v[102:103] op_sel_hi:[0,1]
	v_and_b32_e32 v97, 0xffff0000, v14
	v_lshlrev_b32_e32 v96, 16, v14
	v_pk_fma_f32 v[82:83], v[86:87], v[96:97], v[82:83]
	v_and_b32_e32 v87, 0xffff0000, v10
	v_lshlrev_b32_e32 v86, 16, v10
	v_pk_mul_f32 v[94:95], v[32:33], v[106:107] op_sel_hi:[0,1]
	v_pk_fma_f32 v[82:83], v[92:93], v[86:87], v[82:83]
	v_and_b32_e32 v87, 0xffff0000, v6
	v_lshlrev_b32_e32 v86, 16, v6
	v_pk_fma_f32 v[82:83], v[94:95], v[86:87], v[82:83]
	v_and_b32_e32 v93, 0xffff0000, v19
	v_mul_f32_e32 v10, 0xbfb8aa3b, v83
	v_exp_f32_e32 v10, v10
	v_lshlrev_b32_e32 v92, 16, v19
	v_pk_mul_f32 v[50:51], v[36:37], v[84:85] op_sel_hi:[0,1]
	v_pk_mul_f32 v[84:85], v[36:37], v[100:101] op_sel_hi:[0,1]
	v_mul_f32_e32 v6, 0xbfb8aa3b, v82
	v_pk_fma_f32 v[18:19], v[80:81], v[92:93], 0 op_sel_hi:[1,1,0]
	v_and_b32_e32 v81, 0xffff0000, v15
	v_lshlrev_b32_e32 v80, 16, v15
	v_pk_mul_f32 v[48:49], v[26:27], v[88:89] op_sel_hi:[0,1]
	v_pk_mul_f32 v[88:89], v[26:27], v[104:105] op_sel_hi:[0,1]
	v_exp_f32_e32 v6, v6
	v_pk_fma_f32 v[14:15], v[84:85], v[80:81], v[18:19]
	v_and_b32_e32 v19, 0xffff0000, v11
	v_lshlrev_b32_e32 v18, 16, v11
	v_pk_mul_f32 v[86:87], v[32:33], v[108:109] op_sel_hi:[0,1]
	v_add_f32_e32 v37, 1.0, v10
	v_pk_fma_f32 v[10:11], v[88:89], v[18:19], v[14:15]
	v_and_b32_e32 v15, 0xffff0000, v7
	v_lshlrev_b32_e32 v14, 16, v7
	v_pk_fma_f32 v[10:11], v[86:87], v[14:15], v[10:11]
	v_add_f32_e32 v6, 1.0, v6
	v_mul_f32_e32 v7, 0xbfb8aa3b, v10
	v_exp_f32_e32 v14, v7
	v_mul_f32_e32 v7, 0xbfb8aa3b, v11
	v_rcp_f32_e32 v6, v6
	v_exp_f32_e32 v15, v7
	v_rcp_f32_e32 v7, v37
	v_lshlrev_b32_e32 v84, 16, v114
	v_and_b32_e32 v85, 0xffff0000, v114
	v_pk_mul_f32 v[58:59], v[26:27], v[58:59] op_sel_hi:[0,1]
	v_pk_mul_f32 v[6:7], v[82:83], v[6:7]
	v_lshlrev_b32_e32 v82, 16, v110
	v_and_b32_e32 v83, 0xffff0000, v110
	v_pk_fma_f32 v[82:83], v[128:129], v[82:83], 0 op_sel_hi:[1,1,0]
	v_pk_mul_f32 v[62:63], v[32:33], v[62:63] op_sel_hi:[0,1]
	v_pk_fma_f32 v[82:83], v[136:137], v[84:85], v[82:83]
	v_lshlrev_b32_e32 v84, 16, v118
	v_and_b32_e32 v85, 0xffff0000, v118
	v_pk_mul_f32 v[78:79], v[38:39], v[78:79] op_sel_hi:[0,1]
	v_xor_b32_e32 v37, 1, v27
	v_add_u32_e32 v39, 64, v33
	v_pk_fma_f32 v[58:59], v[58:59], v[84:85], v[82:83]
	v_lshlrev_b32_e32 v82, 16, v122
	v_and_b32_e32 v83, 0xffff0000, v122
	v_cmp_lt_i32_e32 vcc, v37, v39
	v_pk_fma_f32 v[58:59], v[62:63], v[82:83], v[58:59]
	v_pk_mul_f32 v[64:65], v[32:33], v[64:65] op_sel_hi:[0,1]
	v_pk_mul_f32 v[76:77], v[32:33], v[76:77] op_sel_hi:[0,1]
	v_pk_mul_f32 v[74:75], v[32:33], v[74:75] op_sel_hi:[0,1]
	v_pk_mul_f32 v[18:19], v[32:33], v[90:91] op_sel_hi:[0,1]
	v_cndmask_b32_e32 v33, v27, v37, vcc
	v_mul_f32_e32 v37, 0xbfb8aa3b, v58
	v_exp_f32_e32 v37, v37
	v_mul_f32_e32 v62, 0xbfb8aa3b, v59
	v_exp_f32_e32 v63, v62
	v_lshlrev_b32_e32 v82, 16, v111
	v_and_b32_e32 v83, 0xffff0000, v111
	v_pk_fma_f32 v[82:83], v[126:127], v[82:83], 0 op_sel_hi:[1,1,0]
	v_lshlrev_b32_e32 v84, 16, v115
	v_and_b32_e32 v85, 0xffff0000, v115
	v_pk_mul_f32 v[60:61], v[26:27], v[60:61] op_sel_hi:[0,1]
	v_pk_fma_f32 v[82:83], v[134:135], v[84:85], v[82:83]
	v_lshlrev_b32_e32 v84, 16, v119
	v_and_b32_e32 v85, 0xffff0000, v119
	v_add_f32_e32 v37, 1.0, v37
	v_pk_fma_f32 v[60:61], v[60:61], v[84:85], v[82:83]
	v_lshlrev_b32_e32 v82, 16, v123
	v_and_b32_e32 v83, 0xffff0000, v123
	v_rcp_f32_e32 v62, v37
	v_add_f32_e32 v37, 1.0, v63
	v_pk_fma_f32 v[60:61], v[64:65], v[82:83], v[60:61]
	v_rcp_f32_e32 v63, v37
	v_mul_f32_e32 v37, 0xbfb8aa3b, v60
	v_exp_f32_e32 v37, v37
	v_mul_f32_e32 v64, 0xbfb8aa3b, v61
	v_exp_f32_e32 v64, v64
	v_pk_mul_f32 v[58:59], v[58:59], v[62:63]
	v_add_f32_e32 v37, 1.0, v37
	v_rcp_f32_e32 v62, v37
	v_add_f32_e32 v37, 1.0, v64
	v_lshlrev_b32_e32 v64, 16, v112
	v_and_b32_e32 v65, 0xffff0000, v112
	v_pk_fma_f32 v[64:65], v[132:133], v[64:65], 0 op_sel_hi:[1,1,0]
	v_lshlrev_b32_e32 v82, 16, v116
	v_and_b32_e32 v83, 0xffff0000, v116
	v_pk_mul_f32 v[70:71], v[26:27], v[70:71] op_sel_hi:[0,1]
	v_pk_fma_f32 v[64:65], v[66:67], v[82:83], v[64:65]
	v_lshlrev_b32_e32 v66, 16, v120
	v_and_b32_e32 v67, 0xffff0000, v120
	v_pk_fma_f32 v[64:65], v[70:71], v[66:67], v[64:65]
	v_lshlrev_b32_e32 v66, 16, v124
	v_and_b32_e32 v67, 0xffff0000, v124
	v_pk_fma_f32 v[64:65], v[74:75], v[66:67], v[64:65]
	v_lshlrev_b32_e32 v74, 16, v117
	v_mul_f32_e32 v63, 0xbfb8aa3b, v64
	v_exp_f32_e32 v66, v63
	v_mul_f32_e32 v63, 0xbfb8aa3b, v65
	v_exp_f32_e32 v67, v63
	v_rcp_f32_e32 v63, v37
	v_add_f32_e32 v37, 1.0, v66
	v_rcp_f32_e32 v66, v37
	v_add_f32_e32 v37, 1.0, v67
	v_rcp_f32_e32 v67, v37
	v_and_b32_e32 v75, 0xffff0000, v117
	v_pk_mul_f32 v[72:73], v[26:27], v[72:73] op_sel_hi:[0,1]
	v_pk_mul_f32 v[70:71], v[58:59], v[58:59]
	v_pk_mul_f32 v[64:65], v[64:65], v[66:67]
	v_lshlrev_b32_e32 v66, 16, v113
	v_and_b32_e32 v67, 0xffff0000, v113
	v_pk_fma_f32 v[66:67], v[130:131], v[66:67], 0 op_sel_hi:[1,1,0]
	v_pk_mul_f32 v[60:61], v[60:61], v[62:63]
	v_pk_fma_f32 v[66:67], v[68:69], v[74:75], v[66:67]
	v_lshlrev_b32_e32 v68, 16, v121
	v_and_b32_e32 v69, 0xffff0000, v121
	v_pk_fma_f32 v[66:67], v[72:73], v[68:69], v[66:67]
	v_lshlrev_b32_e32 v68, 16, v125
	v_and_b32_e32 v69, 0xffff0000, v125
	v_lshlrev_b32_e32 v74, 16, v16
	v_and_b32_e32 v75, 0xffff0000, v16
	v_pk_fma_f32 v[66:67], v[76:77], v[68:69], v[66:67]
	v_pk_fma_f32 v[74:75], v[78:79], v[74:75], 0 op_sel_hi:[1,1,0]
	v_lshlrev_b32_e32 v76, 16, v12
	v_and_b32_e32 v77, 0xffff0000, v12
	v_pk_fma_f32 v[56:57], v[56:57], v[76:77], v[74:75]
	v_lshlrev_b32_e32 v74, 16, v8
	v_and_b32_e32 v75, 0xffff0000, v8
	v_mul_f32_e32 v37, 0xbfb8aa3b, v66
	v_pk_fma_f32 v[54:55], v[54:55], v[74:75], v[56:57]
	v_lshlrev_b32_e32 v56, 16, v4
	v_and_b32_e32 v57, 0xffff0000, v4
	v_exp_f32_e32 v37, v37
	v_mul_f32_e32 v68, 0xbfb8aa3b, v67
	v_pk_fma_f32 v[18:19], v[18:19], v[56:57], v[54:55]
	v_exp_f32_e32 v73, v68
	v_mul_f32_e32 v8, 0xbfb8aa3b, v19
	v_exp_f32_e32 v8, v8
	v_add_f32_e32 v37, 1.0, v37
	v_lshlrev_b32_e32 v16, 16, v17
	v_and_b32_e32 v17, 0xffff0000, v17
	v_rcp_f32_e32 v72, v37
	v_add_f32_e32 v37, 1.0, v73
	v_pk_fma_f32 v[16:17], v[52:53], v[16:17], 0 op_sel_hi:[1,1,0]
	v_lshlrev_b32_e32 v12, 16, v13
	v_and_b32_e32 v13, 0xffff0000, v13
	v_rcp_f32_e32 v73, v37
	v_add_f32_e32 v37, 1.0, v8
	v_pk_fma_f32 v[12:13], v[50:51], v[12:13], v[16:17]
	v_lshlrev_b32_e32 v8, 16, v9
	v_and_b32_e32 v9, 0xffff0000, v9
	v_pk_fma_f32 v[8:9], v[48:49], v[8:9], v[12:13]
	v_lshlrev_b32_e32 v12, 16, v5
	v_and_b32_e32 v13, 0xffff0000, v5
	v_mul_f32_e32 v4, 0xbfb8aa3b, v18
	v_pk_fma_f32 v[8:9], v[46:47], v[12:13], v[8:9]
	v_exp_f32_e32 v4, v4
	v_mul_f32_e32 v5, 0xbfb8aa3b, v8
	v_exp_f32_e32 v12, v5
	v_mul_f32_e32 v5, 0xbfb8aa3b, v9
	v_exp_f32_e32 v13, v5
	v_pk_mul_f32 v[62:63], v[60:61], v[60:61]
	v_add_f32_e32 v4, 1.0, v4
	v_rcp_f32_e32 v5, v37
	v_add_f32_e32 v37, v70, v71
	v_rcp_f32_e32 v4, v4
	v_add_f32_e32 v37, v62, v37
	v_pk_mul_f32 v[68:69], v[64:65], v[64:65]
	v_add_f32_e32 v12, 1.0, v12
	v_add_f32_e32 v13, 1.0, v13
	v_add_f32_e32 v37, v63, v37
	v_pk_mul_f32 v[54:55], v[66:67], v[72:73]
	v_rcp_f32_e32 v12, v12
	v_rcp_f32_e32 v13, v13
	v_add_f32_e32 v37, v37, v68
	v_pk_mul_f32 v[16:17], v[54:55], v[54:55]
	v_add_f32_e32 v37, v69, v37
	v_pk_mul_f32 v[4:5], v[18:19], v[4:5]
	v_add_f32_e32 v16, v16, v37
	v_add_f32_e32 v14, 1.0, v14
	v_add_f32_e32 v15, 1.0, v15
	v_pk_mul_f32 v[18:19], v[4:5], v[4:5]
	v_add_f32_e32 v16, v17, v16
	v_rcp_f32_e32 v14, v14
	v_rcp_f32_e32 v15, v15
	v_pk_mul_f32 v[8:9], v[8:9], v[12:13]
	v_add_f32_e32 v16, v16, v18
	v_pk_mul_f32 v[12:13], v[8:9], v[8:9]
	v_add_f32_e32 v16, v19, v16
	v_add_f32_e32 v12, v12, v16
	v_pk_mul_f32 v[80:81], v[6:7], v[6:7]
	v_add_f32_e32 v12, v13, v12
	v_pk_mul_f32 v[10:11], v[10:11], v[14:15]
	v_add_f32_e32 v12, v80, v12
	v_pk_mul_f32 v[14:15], v[10:11], v[10:11]
	v_add_f32_e32 v12, v81, v12
	v_add_f32_e32 v12, v14, v12
	v_lshlrev_b32_e32 v33, 2, v33
	v_add_f32_e32 v12, v15, v12
	ds_bpermute_b32 v13, v33, v12
	v_xor_b32_e32 v14, 2, v27
	v_cmp_lt_i32_e32 vcc, v14, v39
	v_lshlrev_b32_e32 v136, 1, v23
	v_lshl_add_u64 v[110:111], v[34:35], 0, v[2:3]
	v_cndmask_b32_e32 v14, v27, v14, vcc
	v_lshlrev_b32_e32 v37, 2, v14
	s_waitcnt lgkmcnt(0)
	v_add_f32_e32 v12, v12, v13
	ds_bpermute_b32 v13, v37, v12
	v_xor_b32_e32 v14, 4, v27
	v_cmp_lt_i32_e32 vcc, v14, v39
	v_mul_lo_u32 v39, v1, s20
	v_lshl_add_u64 v[112:113], v[40:41], 0, v[2:3]
	v_cndmask_b32_e32 v14, v27, v14, vcc
	v_lshlrev_b32_e32 v27, 2, v14
	s_waitcnt lgkmcnt(0)
	v_add_f32_e32 v12, v12, v13
	ds_bpermute_b32 v13, v27, v12
	s_waitcnt lgkmcnt(0)
	v_add_f32_e32 v12, v12, v13
	v_add_f32_e32 v12, 0x358637bd, v12
	v_mul_f32_e32 v13, 0x4b800000, v12
	v_cmp_gt_f32_e32 vcc, s0, v12
	s_nop 1
	v_cndmask_b32_e32 v12, v12, v13, vcc
	v_rsq_f32_e32 v12, v12
	s_nop 0
	v_mul_f32_e32 v13, 0x45800000, v12
	v_cndmask_b32_e32 v12, v12, v13, vcc
	v_mul_f32_e32 v12, 0x3db504f3, v12
	v_pk_mul_f32 v[14:15], v[58:59], v[12:13] op_sel_hi:[1,0]
	v_pk_mul_f32 v[16:17], v[60:61], v[12:13] op_sel_hi:[1,0]
	v_pk_mul_f32 v[4:5], v[4:5], v[12:13] op_sel_hi:[1,0]
	v_pk_mul_f32 v[8:9], v[8:9], v[12:13] op_sel_hi:[1,0]
	v_pk_mul_f32 v[18:19], v[64:65], v[12:13] op_sel_hi:[1,0]
	v_pk_mul_f32 v[46:47], v[54:55], v[12:13] op_sel_hi:[1,0]
	v_pk_mul_f32 v[6:7], v[6:7], v[12:13] op_sel_hi:[1,0]
	v_pk_mul_f32 v[10:11], v[10:11], v[12:13] op_sel_hi:[1,0]
	v_add3_u32 v12, s25, v39, v136
	v_cvt_pk_bf16_f32 v13, v14, v15
	v_cvt_pk_bf16_f32 v14, v16, v17
	v_cvt_pk_bf16_f32 v4, v4, v5
	v_cvt_pk_bf16_f32 v5, v8, v9
	ds_write2_b32 v12, v13, v14 offset1:1
	v_cvt_pk_bf16_f32 v13, v18, v19
	v_cvt_pk_bf16_f32 v14, v46, v47
	ds_write2_b32 v12, v4, v5 offset0:4 offset1:5
	v_cvt_pk_bf16_f32 v4, v6, v7
	v_cvt_pk_bf16_f32 v5, v10, v11
	v_add_co_u32_e32 v82, vcc, s1, v42
	ds_write2_b32 v12, v13, v14 offset0:2 offset1:3
	ds_write2_b32 v12, v4, v5 offset0:6 offset1:7
	v_addc_co_u32_e32 v83, vcc, 0, v43, vcc
	global_load_dwordx4 v[4:7], v[42:43], off offset:2048
	global_load_dwordx4 v[8:11], v[82:83], off
	global_load_dwordx4 v[12:15], v[44:45], off offset:2048
	s_movk_i32 s1, 0x5000
	v_add_co_u32_e32 v106, vcc, s1, v42
	s_waitcnt vmcnt(0) lgkmcnt(0)
	v_pk_mul_f32 v[118:119], v[36:37], v[10:11] op_sel_hi:[0,1]
	v_addc_co_u32_e32 v107, vcc, 0, v43, vcc
	global_load_dwordx4 v[16:19], v[106:107], off
	global_load_dwordx4 v[46:49], v[42:43], off offset:2064
	global_load_dwordx4 v[50:53], v[82:83], off offset:16
	global_load_dwordx4 v[54:57], v[44:45], off offset:2064
	global_load_dwordx4 v[58:61], v[106:107], off offset:16
	global_load_dwordx4 v[62:65], v[42:43], off offset:2080
	global_load_dwordx4 v[66:69], v[82:83], off offset:32
	global_load_dwordx4 v[70:73], v[44:45], off offset:2080
	global_load_dwordx4 v[74:77], v[106:107], off offset:32
	global_load_dwordx4 v[78:81], v[42:43], off offset:2096
	s_nop 0
	global_load_dwordx4 v[82:85], v[82:83], off offset:48
	v_lshl_add_u64 v[42:43], v[24:25], 0, v[2:3]
	global_load_dwordx4 v[86:89], v[44:45], off offset:2096
	global_load_dwordx4 v[90:93], v[42:43], off
	v_lshl_add_u64 v[44:45], v[28:29], 0, v[2:3]
	global_load_dwordx4 v[94:97], v[44:45], off
	global_load_dwordx4 v[98:101], v[110:111], off
	global_load_dwordx4 v[102:105], v[112:113], off
	s_nop 0
	global_load_dwordx4 v[106:109], v[106:107], off offset:48
	v_pk_mul_f32 v[122:123], v[26:27], v[14:15] op_sel_hi:[0,1]
	v_pk_mul_f32 v[124:125], v[26:27], v[12:13] op_sel_hi:[0,1]
	global_load_dwordx4 v[12:15], v[44:45], off offset:16
	v_pk_mul_f32 v[120:121], v[36:37], v[8:9] op_sel_hi:[0,1]
	global_load_dwordx4 v[8:11], v[110:111], off offset:16
	v_pk_mul_f32 v[114:115], v[38:39], v[6:7] op_sel_hi:[0,1]
	v_pk_mul_f32 v[116:117], v[38:39], v[4:5] op_sel_hi:[0,1]
	global_load_dwordx4 v[4:7], v[112:113], off offset:16
	s_waitcnt vmcnt(0) lgkmcnt(0)
	v_pk_mul_f32 v[126:127], v[32:33], v[18:19] op_sel_hi:[0,1]
	v_pk_mul_f32 v[128:129], v[32:33], v[16:17] op_sel_hi:[0,1]
	global_load_dwordx4 v[16:19], v[42:43], off offset:16
	v_pk_mul_f32 v[130:131], v[38:39], v[48:49] op_sel_hi:[0,1]
	v_pk_mul_f32 v[134:135], v[36:37], v[50:51] op_sel_hi:[0,1]
	v_pk_mul_f32 v[132:133], v[38:39], v[46:47] op_sel_hi:[0,1]
	v_pk_mul_f32 v[54:55], v[26:27], v[54:55] op_sel_hi:[0,1]
	v_pk_mul_f32 v[58:59], v[32:33], v[58:59] op_sel_hi:[0,1]
	v_pk_mul_f32 v[52:53], v[36:37], v[52:53] op_sel_hi:[0,1]
	v_pk_mul_f32 v[46:47], v[38:39], v[80:81] op_sel_hi:[0,1]
	v_pk_mul_f32 v[80:81], v[36:37], v[82:83] op_sel_hi:[0,1]
	v_pk_mul_f32 v[56:57], v[26:27], v[56:57] op_sel_hi:[0,1]
	v_pk_mul_f32 v[82:83], v[26:27], v[86:87] op_sel_hi:[0,1]
	v_lshlrev_b32_e32 v48, 16, v90
	v_and_b32_e32 v49, 0xffff0000, v90
	v_pk_fma_f32 v[48:49], v[116:117], v[48:49], 0 op_sel_hi:[1,1,0]
	v_lshlrev_b32_e32 v50, 16, v94
	v_and_b32_e32 v51, 0xffff0000, v94
	v_pk_fma_f32 v[48:49], v[120:121], v[50:51], v[48:49]
	v_lshlrev_b32_e32 v50, 16, v98
	v_and_b32_e32 v51, 0xffff0000, v98
	v_pk_fma_f32 v[48:49], v[124:125], v[50:51], v[48:49]
	v_lshlrev_b32_e32 v50, 16, v102
	v_and_b32_e32 v51, 0xffff0000, v102
	v_pk_fma_f32 v[48:49], v[128:129], v[50:51], v[48:49]
	v_lshlrev_b32_e32 v86, 16, v91
	v_mul_f32_e32 v2, 0xbfb8aa3b, v48
	v_exp_f32_e32 v2, v2
	v_mul_f32_e32 v50, 0xbfb8aa3b, v49
	v_and_b32_e32 v87, 0xffff0000, v91
	v_pk_mul_f32 v[42:43], v[26:27], v[88:89] op_sel_hi:[0,1]
	v_exp_f32_e32 v51, v50
	v_pk_fma_f32 v[86:87], v[114:115], v[86:87], 0 op_sel_hi:[1,1,0]
	v_lshlrev_b32_e32 v88, 16, v95
	v_and_b32_e32 v89, 0xffff0000, v95
	v_pk_fma_f32 v[86:87], v[118:119], v[88:89], v[86:87]
	v_lshlrev_b32_e32 v88, 16, v99
	v_and_b32_e32 v89, 0xffff0000, v99
	v_pk_fma_f32 v[86:87], v[122:123], v[88:89], v[86:87]
	v_lshlrev_b32_e32 v88, 16, v103
	v_and_b32_e32 v89, 0xffff0000, v103
	v_add_f32_e32 v2, 1.0, v2
	v_pk_fma_f32 v[86:87], v[126:127], v[88:89], v[86:87]
	v_rcp_f32_e32 v50, v2
	v_add_f32_e32 v2, 1.0, v51
	v_mul_f32_e32 v51, 0xbfb8aa3b, v86
	v_exp_f32_e32 v88, v51
	v_mul_f32_e32 v51, 0xbfb8aa3b, v87
	v_exp_f32_e32 v89, v51
	v_rcp_f32_e32 v51, v2
	v_add_f32_e32 v2, 1.0, v88
	v_rcp_f32_e32 v88, v2
	v_add_f32_e32 v2, 1.0, v89
	v_rcp_f32_e32 v89, v2
	v_pk_mul_f32 v[48:49], v[48:49], v[50:51]
	v_pk_mul_f32 v[60:61], v[32:33], v[60:61] op_sel_hi:[0,1]
	v_pk_mul_f32 v[62:63], v[38:39], v[62:63] op_sel_hi:[0,1]
	v_pk_mul_f32 v[50:51], v[86:87], v[88:89]
	v_lshlrev_b32_e32 v86, 16, v92
	v_and_b32_e32 v87, 0xffff0000, v92
	v_pk_fma_f32 v[86:87], v[132:133], v[86:87], 0 op_sel_hi:[1,1,0]
	v_lshlrev_b32_e32 v88, 16, v96
	v_and_b32_e32 v89, 0xffff0000, v96
	v_pk_fma_f32 v[86:87], v[134:135], v[88:89], v[86:87]
	v_lshlrev_b32_e32 v88, 16, v100
	v_and_b32_e32 v89, 0xffff0000, v100
	v_pk_fma_f32 v[54:55], v[54:55], v[88:89], v[86:87]
	v_lshlrev_b32_e32 v86, 16, v104
	v_and_b32_e32 v87, 0xffff0000, v104
	v_pk_fma_f32 v[54:55], v[58:59], v[86:87], v[54:55]
	v_lshlrev_b32_e32 v88, 16, v93
	v_mul_f32_e32 v2, 0xbfb8aa3b, v54
	v_and_b32_e32 v89, 0xffff0000, v93
	v_exp_f32_e32 v2, v2
	v_mul_f32_e32 v58, 0xbfb8aa3b, v55
	v_pk_fma_f32 v[88:89], v[130:131], v[88:89], 0 op_sel_hi:[1,1,0]
	v_lshlrev_b32_e32 v92, 16, v97
	v_and_b32_e32 v93, 0xffff0000, v97
	v_exp_f32_e32 v87, v58
	v_pk_fma_f32 v[52:53], v[52:53], v[92:93], v[88:89]
	v_lshlrev_b32_e32 v88, 16, v101
	v_and_b32_e32 v89, 0xffff0000, v101
	v_pk_fma_f32 v[52:53], v[56:57], v[88:89], v[52:53]
	v_lshlrev_b32_e32 v56, 16, v105
	v_and_b32_e32 v57, 0xffff0000, v105
	v_pk_fma_f32 v[52:53], v[60:61], v[56:57], v[52:53]
	s_waitcnt vmcnt(0) lgkmcnt(0)
	v_lshlrev_b32_e32 v60, 16, v16
	v_and_b32_e32 v61, 0xffff0000, v16
	v_pk_mul_f32 v[66:67], v[36:37], v[66:67] op_sel_hi:[0,1]
	v_add_f32_e32 v2, 1.0, v2
	v_pk_fma_f32 v[60:61], v[62:63], v[60:61], 0 op_sel_hi:[1,1,0]
	v_lshlrev_b32_e32 v62, 16, v12
	v_and_b32_e32 v63, 0xffff0000, v12
	v_pk_mul_f32 v[70:71], v[26:27], v[70:71] op_sel_hi:[0,1]
	v_rcp_f32_e32 v86, v2
	v_add_f32_e32 v2, 1.0, v87
	v_pk_fma_f32 v[60:61], v[66:67], v[62:63], v[60:61]
	v_lshlrev_b32_e32 v62, 16, v8
	v_and_b32_e32 v63, 0xffff0000, v8
	v_pk_mul_f32 v[74:75], v[32:33], v[74:75] op_sel_hi:[0,1]
	v_rcp_f32_e32 v87, v2
	v_mul_f32_e32 v2, 0xbfb8aa3b, v52
	v_pk_fma_f32 v[60:61], v[70:71], v[62:63], v[60:61]
	v_lshlrev_b32_e32 v62, 16, v4
	v_and_b32_e32 v63, 0xffff0000, v4
	v_exp_f32_e32 v2, v2
	v_mul_f32_e32 v56, 0xbfb8aa3b, v53
	v_pk_fma_f32 v[60:61], v[74:75], v[62:63], v[60:61]
	v_exp_f32_e32 v57, v56
	v_mul_f32_e32 v4, 0xbfb8aa3b, v60
	v_exp_f32_e32 v4, v4
	v_mul_f32_e32 v8, 0xbfb8aa3b, v61
	v_exp_f32_e32 v8, v8
	v_add_f32_e32 v2, 1.0, v2
	v_pk_mul_f32 v[64:65], v[38:39], v[64:65] op_sel_hi:[0,1]
	v_rcp_f32_e32 v56, v2
	v_add_f32_e32 v2, 1.0, v57
	v_lshlrev_b32_e32 v16, 16, v17
	v_and_b32_e32 v17, 0xffff0000, v17
	v_pk_mul_f32 v[68:69], v[36:37], v[68:69] op_sel_hi:[0,1]
	v_rcp_f32_e32 v57, v2
	v_add_f32_e32 v2, 1.0, v4
	v_pk_fma_f32 v[16:17], v[64:65], v[16:17], 0 op_sel_hi:[1,1,0]
	v_lshlrev_b32_e32 v12, 16, v13
	v_and_b32_e32 v13, 0xffff0000, v13
	v_pk_mul_f32 v[72:73], v[26:27], v[72:73] op_sel_hi:[0,1]
	v_rcp_f32_e32 v62, v2
	v_add_f32_e32 v2, 1.0, v8
	v_pk_fma_f32 v[12:13], v[68:69], v[12:13], v[16:17]
	v_lshlrev_b32_e32 v8, 16, v9
	v_and_b32_e32 v9, 0xffff0000, v9
	v_pk_mul_f32 v[76:77], v[32:33], v[76:77] op_sel_hi:[0,1]
	v_pk_fma_f32 v[8:9], v[72:73], v[8:9], v[12:13]
	v_lshlrev_b32_e32 v4, 16, v5
	v_and_b32_e32 v5, 0xffff0000, v5
	v_rcp_f32_e32 v63, v2
	v_pk_fma_f32 v[4:5], v[76:77], v[4:5], v[8:9]
	v_pk_mul_f32 v[78:79], v[38:39], v[78:79] op_sel_hi:[0,1]
	v_mul_f32_e32 v2, 0xbfb8aa3b, v4
	v_exp_f32_e32 v2, v2
	v_mul_f32_e32 v8, 0xbfb8aa3b, v5
	v_exp_f32_e32 v13, v8
	v_lshlrev_b32_e32 v16, 16, v18
	v_and_b32_e32 v17, 0xffff0000, v18
	v_pk_mul_f32 v[60:61], v[60:61], v[62:63]
	v_pk_fma_f32 v[16:17], v[78:79], v[16:17], 0 op_sel_hi:[1,1,0]
	v_lshlrev_b32_e32 v62, 16, v14
	v_and_b32_e32 v63, 0xffff0000, v14
	v_pk_fma_f32 v[16:17], v[80:81], v[62:63], v[16:17]
	v_lshlrev_b32_e32 v62, 16, v10
	v_and_b32_e32 v63, 0xffff0000, v10
	v_pk_mul_f32 v[90:91], v[32:33], v[106:107] op_sel_hi:[0,1]
	v_add_f32_e32 v2, 1.0, v2
	v_pk_fma_f32 v[16:17], v[82:83], v[62:63], v[16:17]
	v_lshlrev_b32_e32 v62, 16, v6
	v_and_b32_e32 v63, 0xffff0000, v6
	v_rcp_f32_e32 v12, v2
	v_add_f32_e32 v2, 1.0, v13
	v_pk_fma_f32 v[16:17], v[90:91], v[62:63], v[16:17]
	v_rcp_f32_e32 v13, v2
	v_mul_f32_e32 v2, 0xbfb8aa3b, v16
	v_exp_f32_e32 v2, v2
	v_mul_f32_e32 v6, 0xbfb8aa3b, v17
	v_exp_f32_e32 v10, v6
	v_pk_mul_f32 v[4:5], v[4:5], v[12:13]
	v_lshlrev_b32_e32 v12, 16, v19
	v_and_b32_e32 v13, 0xffff0000, v19
	v_pk_mul_f32 v[44:45], v[36:37], v[84:85] op_sel_hi:[0,1]
	v_add_f32_e32 v2, 1.0, v2
	v_pk_fma_f32 v[12:13], v[46:47], v[12:13], 0 op_sel_hi:[1,1,0]
	v_lshlrev_b32_e32 v14, 16, v15
	v_and_b32_e32 v15, 0xffff0000, v15
	v_rcp_f32_e32 v6, v2
	v_add_f32_e32 v2, 1.0, v10
	v_pk_fma_f32 v[12:13], v[44:45], v[14:15], v[12:13]
	v_lshlrev_b32_e32 v10, 16, v11
	v_and_b32_e32 v11, 0xffff0000, v11
	v_pk_mul_f32 v[84:85], v[32:33], v[108:109] op_sel_hi:[0,1]
	v_pk_fma_f32 v[10:11], v[42:43], v[10:11], v[12:13]
	v_lshlrev_b32_e32 v12, 16, v7
	v_and_b32_e32 v13, 0xffff0000, v7
	v_pk_fma_f32 v[10:11], v[84:85], v[12:13], v[10:11]
	v_pk_mul_f32 v[94:95], v[48:49], v[48:49]
	v_mul_f32_e32 v7, 0xbfb8aa3b, v10
	v_exp_f32_e32 v12, v7
	v_mul_f32_e32 v7, 0xbfb8aa3b, v11
	v_exp_f32_e32 v13, v7
	v_rcp_f32_e32 v7, v2
	v_add_f32_e32 v2, 1.0, v12
	v_rcp_f32_e32 v12, v2
	v_add_f32_e32 v2, 1.0, v13
	v_pk_mul_f32 v[58:59], v[50:51], v[50:51]
	v_rcp_f32_e32 v13, v2
	v_add_f32_e32 v2, v94, v95
	v_pk_mul_f32 v[54:55], v[54:55], v[86:87]
	v_add_f32_e32 v2, v58, v2
	v_pk_mul_f32 v[66:67], v[54:55], v[54:55]
	v_add_f32_e32 v2, v59, v2
	v_pk_mul_f32 v[52:53], v[52:53], v[56:57]
	v_add_f32_e32 v2, v2, v66
	v_pk_mul_f32 v[56:57], v[52:53], v[52:53]
	v_add_f32_e32 v2, v67, v2
	v_add_f32_e32 v2, v56, v2
	v_pk_mul_f32 v[8:9], v[60:61], v[60:61]
	v_add_f32_e32 v2, v57, v2
	v_add_f32_e32 v2, v2, v8
	v_pk_mul_f32 v[14:15], v[4:5], v[4:5]
	v_add_f32_e32 v2, v9, v2
	v_pk_mul_f32 v[6:7], v[16:17], v[6:7]
	v_add_f32_e32 v2, v14, v2
	v_pk_mul_f32 v[16:17], v[6:7], v[6:7]
	v_add_f32_e32 v2, v15, v2
	v_pk_mul_f32 v[10:11], v[10:11], v[12:13]
	v_add_f32_e32 v2, v16, v2
	v_pk_mul_f32 v[12:13], v[10:11], v[10:11]
	v_add_f32_e32 v2, v17, v2
	v_add_f32_e32 v2, v12, v2
	v_add_f32_e32 v2, v13, v2
	ds_bpermute_b32 v8, v33, v2
	v_lshl_add_u32 v46, v23, 2, s33
	s_waitcnt lgkmcnt(0)
	v_add_f32_e32 v2, v2, v8
	ds_bpermute_b32 v8, v37, v2
	s_waitcnt lgkmcnt(0)
	v_add_f32_e32 v2, v2, v8
	ds_bpermute_b32 v8, v27, v2
	s_waitcnt lgkmcnt(0)
	v_add_f32_e32 v2, v2, v8
	v_add_f32_e32 v2, 0x358637bd, v2
	v_mul_f32_e32 v8, 0x4b800000, v2
	v_cmp_gt_f32_e32 vcc, s0, v2
	s_movk_i32 s0, 0x204
	s_nop 0
	v_cndmask_b32_e32 v2, v2, v8, vcc
	v_rsq_f32_e32 v2, v2
	v_mad_u64_u32 v[8:9], s[0:1], v1, s0, v[46:47]
	v_add3_u32 v9, s24, v39, v136
	v_mul_f32_e32 v12, 0x45800000, v2
	v_cndmask_b32_e32 v2, v2, v12, vcc
	v_pk_mul_f32 v[12:13], v[48:49], v[2:3] op_sel_hi:[1,0]
	v_pk_mul_f32 v[14:15], v[50:51], v[2:3] op_sel_hi:[1,0]
	v_pk_mul_f32 v[16:17], v[54:55], v[2:3] op_sel_hi:[1,0]
	v_pk_mul_f32 v[18:19], v[52:53], v[2:3] op_sel_hi:[1,0]
	v_pk_mul_f32 v[42:43], v[60:61], v[2:3] op_sel_hi:[1,0]
	v_pk_mul_f32 v[4:5], v[4:5], v[2:3] op_sel_hi:[1,0]
	v_pk_mul_f32 v[6:7], v[6:7], v[2:3] op_sel_hi:[1,0]
	v_pk_mul_f32 v[10:11], v[10:11], v[2:3] op_sel_hi:[1,0]
	v_cvt_pk_bf16_f32 v2, v12, v13
	v_cvt_pk_bf16_f32 v23, v14, v15
	ds_write2_b32 v9, v2, v23 offset1:1
	v_cvt_pk_bf16_f32 v2, v16, v17
	v_cvt_pk_bf16_f32 v23, v18, v19
	ds_write2_b32 v9, v2, v23 offset0:2 offset1:3
	v_cvt_pk_bf16_f32 v2, v42, v43
	v_cvt_pk_bf16_f32 v23, v4, v5
	ds_write2_b32 v9, v2, v23 offset0:4 offset1:5
	v_cvt_pk_bf16_f32 v2, v6, v7
	v_cvt_pk_bf16_f32 v23, v10, v11
	ds_write2_b32 v9, v2, v23 offset0:6 offset1:7
	ds_write2_b32 v8, v12, v13 offset1:1
	ds_write2_b32 v8, v14, v15 offset0:2 offset1:3
	ds_write2_b32 v8, v16, v17 offset0:4 offset1:5
	ds_write2_b32 v8, v18, v19 offset0:6 offset1:7
	ds_write2_b32 v8, v42, v43 offset0:8 offset1:9
	ds_write2_b32 v8, v4, v5 offset0:10 offset1:11
	ds_write2_b32 v8, v6, v7 offset0:12 offset1:13
	ds_write2_b32 v8, v10, v11 offset0:14 offset1:15
	v_or_b32_e32 v12, 0x400, v21
	v_lshlrev_b32_e32 v2, 2, v12
	v_lshl_add_u64 v[4:5], v[30:31], 0, v[2:3]
	v_add_co_u32_e32 v6, vcc, s21, v4
	v_lshlrev_b32_e32 v2, 1, v12
	s_nop 0
	v_addc_co_u32_e32 v7, vcc, 0, v5, vcc
	v_add_co_u32_e32 v8, vcc, s19, v4
	global_load_dwordx4 v[42:45], v[4:5], off offset:48
	global_load_dwordx4 v[48:51], v[6:7], off offset:2096
	v_addc_co_u32_e32 v9, vcc, 0, v5, vcc
	v_add_co_u32_e32 v10, vcc, s17, v4
	global_load_dwordx4 v[52:55], v[8:9], off offset:48
	s_nop 0
	v_addc_co_u32_e32 v11, vcc, 0, v5, vcc
	global_load_dwordx4 v[56:59], v[10:11], off offset:2096
	global_load_dwordx4 v[60:63], v[4:5], off offset:32
	global_load_dwordx4 v[64:67], v[6:7], off offset:2080
	global_load_dwordx4 v[68:71], v[8:9], off offset:32
	global_load_dwordx4 v[72:75], v[10:11], off offset:2080
	global_load_dwordx4 v[76:79], v[4:5], off offset:16
	global_load_dwordx4 v[80:83], v[6:7], off offset:2064
	global_load_dwordx4 v[84:87], v[8:9], off offset:16
	global_load_dwordx4 v[88:91], v[10:11], off offset:2064
	global_load_dwordx4 v[92:95], v[4:5], off
	global_load_dwordx4 v[96:99], v[6:7], off offset:2048
	global_load_dwordx4 v[100:103], v[8:9], off
	v_lshl_add_u64 v[4:5], v[24:25], 0, v[2:3]
	global_load_dwordx4 v[104:107], v[10:11], off offset:2048
	global_load_dwordx4 v[108:111], v[4:5], off
	v_lshl_add_u64 v[6:7], v[28:29], 0, v[2:3]
	global_load_dwordx4 v[112:115], v[6:7], off
	v_lshl_add_u64 v[8:9], v[34:35], 0, v[2:3]
	global_load_dwordx4 v[116:119], v[8:9], off
	v_lshl_add_u64 v[24:25], v[40:41], 0, v[2:3]
	global_load_dwordx4 v[120:123], v[24:25], off
	global_load_dwordx4 v[16:19], v[4:5], off offset:16
	global_load_dwordx4 v[12:15], v[6:7], off offset:16
	s_nop 0
	global_load_dwordx4 v[8:11], v[8:9], off offset:16
	s_nop 0
	global_load_dwordx4 v[4:7], v[24:25], off offset:16
	v_lshl_add_u32 v1, v1, 9, v46
	v_add_u32_e32 v23, 0x8100, v1
	s_ashr_i32 s0, s15, 6
	s_cmp_gt_u32 s0, 3
	s_cselect_b64 s[18:19], -1, 0
	s_lshl_b32 s1, s0, 4
	v_and_b32_e32 v2, 31, v20
	s_and_b32 s4, s1, 32
	s_lshl_b32 s1, s0, 5
	v_lshrrev_b32_e32 v21, 5, v22
	s_cmp_lt_u32 s0, 4
	s_cselect_b32 s0, s24, s25
	s_ashr_i32 s17, s16, 31
	s_mov_b64 s[20:21], -1
	s_waitcnt vmcnt(0) lgkmcnt(0)
	v_pk_mul_f32 v[40:41], v[32:33], v[56:57] op_sel_hi:[0,1]
	v_pk_mul_f32 v[34:35], v[38:39], v[44:45] op_sel_hi:[0,1]
	v_pk_mul_f32 v[46:47], v[38:39], v[42:43] op_sel_hi:[0,1]
	v_pk_mul_f32 v[30:31], v[36:37], v[50:51] op_sel_hi:[0,1]
	v_pk_mul_f32 v[44:45], v[36:37], v[48:49] op_sel_hi:[0,1]
	v_pk_mul_f32 v[48:49], v[38:39], v[62:63] op_sel_hi:[0,1]
	v_pk_mul_f32 v[50:51], v[38:39], v[60:61] op_sel_hi:[0,1]
	v_pk_mul_f32 v[28:29], v[26:27], v[54:55] op_sel_hi:[0,1]
	v_pk_mul_f32 v[42:43], v[26:27], v[52:53] op_sel_hi:[0,1]
	v_pk_mul_f32 v[52:53], v[36:37], v[66:67] op_sel_hi:[0,1]
	v_pk_mul_f32 v[54:55], v[36:37], v[64:65] op_sel_hi:[0,1]
	v_pk_mul_f32 v[56:57], v[26:27], v[70:71] op_sel_hi:[0,1]
	v_pk_mul_f32 v[64:65], v[38:39], v[78:79] op_sel_hi:[0,1]
	v_pk_mul_f32 v[66:67], v[38:39], v[76:77] op_sel_hi:[0,1]
	v_pk_mul_f32 v[70:71], v[36:37], v[80:81] op_sel_hi:[0,1]
	v_pk_mul_f32 v[78:79], v[32:33], v[88:89] op_sel_hi:[0,1]
	v_pk_mul_f32 v[80:81], v[38:39], v[94:95] op_sel_hi:[0,1]
	v_pk_mul_f32 v[38:39], v[38:39], v[92:93] op_sel_hi:[0,1]
	v_lshlrev_b32_e32 v88, 16, v108
	v_and_b32_e32 v89, 0xffff0000, v108
	v_pk_mul_f32 v[24:25], v[32:33], v[58:59] op_sel_hi:[0,1]
	v_pk_mul_f32 v[58:59], v[26:27], v[68:69] op_sel_hi:[0,1]
	v_pk_mul_f32 v[68:69], v[36:37], v[82:83] op_sel_hi:[0,1]
	v_pk_mul_f32 v[82:83], v[36:37], v[98:99] op_sel_hi:[0,1]
	v_pk_mul_f32 v[36:37], v[36:37], v[96:97] op_sel_hi:[0,1]
	v_pk_fma_f32 v[38:39], v[38:39], v[88:89], 0 op_sel_hi:[1,1,0]
	v_lshlrev_b32_e32 v88, 16, v112
	v_and_b32_e32 v89, 0xffff0000, v112
	v_pk_mul_f32 v[60:61], v[32:33], v[74:75] op_sel_hi:[0,1]
	v_pk_mul_f32 v[62:63], v[32:33], v[72:73] op_sel_hi:[0,1]
	v_pk_mul_f32 v[72:73], v[26:27], v[86:87] op_sel_hi:[0,1]
	v_pk_mul_f32 v[74:75], v[26:27], v[84:85] op_sel_hi:[0,1]
	v_pk_mul_f32 v[84:85], v[26:27], v[102:103] op_sel_hi:[0,1]
	v_pk_mul_f32 v[26:27], v[26:27], v[100:101] op_sel_hi:[0,1]
	v_pk_fma_f32 v[36:37], v[36:37], v[88:89], v[38:39]
	v_lshlrev_b32_e32 v38, 16, v116
	v_and_b32_e32 v39, 0xffff0000, v116
	v_pk_mul_f32 v[86:87], v[32:33], v[104:105] op_sel_hi:[0,1]
	v_pk_fma_f32 v[26:27], v[26:27], v[38:39], v[36:37]
	v_lshlrev_b32_e32 v36, 16, v120
	v_and_b32_e32 v37, 0xffff0000, v120
	v_pk_fma_f32 v[26:27], v[86:87], v[36:37], v[26:27]
	v_pk_mul_f32 v[76:77], v[32:33], v[90:91] op_sel_hi:[0,1]
	v_mul_f32_e32 v33, 0xbfb8aa3b, v27
	v_exp_f32_e32 v36, v33
	v_mul_f32_e32 v33, 0xbfb8aa3b, v26
	v_exp_f32_e32 v38, v33
	v_and_b32_e32 v39, 0xffff0000, v109
	v_add_f32_e32 v36, 1.0, v36
	v_rcp_f32_e32 v37, v36
	v_add_f32_e32 v36, 1.0, v38
	v_lshlrev_b32_e32 v38, 16, v109
	v_pk_fma_f32 v[38:39], v[80:81], v[38:39], 0 op_sel_hi:[1,1,0]
	v_lshlrev_b32_e32 v80, 16, v113
	v_and_b32_e32 v81, 0xffff0000, v113
	v_pk_fma_f32 v[38:39], v[82:83], v[80:81], v[38:39]
	v_lshlrev_b32_e32 v80, 16, v117
	v_and_b32_e32 v81, 0xffff0000, v117
	v_pk_mul_f32 v[32:33], v[32:33], v[106:107] op_sel_hi:[0,1]
	v_pk_fma_f32 v[38:39], v[84:85], v[80:81], v[38:39]
	v_lshlrev_b32_e32 v80, 16, v121
	v_and_b32_e32 v81, 0xffff0000, v121
	v_pk_fma_f32 v[32:33], v[32:33], v[80:81], v[38:39]
	v_rcp_f32_e32 v36, v36
	v_mul_f32_e32 v38, 0xbfb8aa3b, v33
	v_exp_f32_e32 v38, v38
	v_mul_f32_e32 v39, 0xbfb8aa3b, v32
	v_exp_f32_e32 v80, v39
	v_pk_mul_f32 v[26:27], v[26:27], v[36:37]
	v_add_f32_e32 v38, 1.0, v38
	v_rcp_f32_e32 v39, v38
	v_add_f32_e32 v38, 1.0, v80
	v_rcp_f32_e32 v38, v38
	ds_write2_b32 v23, v26, v27 offset1:1
	v_add_u32_e32 v23, 0x8108, v1
	v_lshlrev_b32_e32 v36, 16, v111
	v_pk_mul_f32 v[26:27], v[32:33], v[38:39]
	ds_write2_b32 v23, v26, v27 offset1:1
	v_lshlrev_b32_e32 v26, 16, v110
	v_and_b32_e32 v27, 0xffff0000, v110
	v_pk_fma_f32 v[26:27], v[66:67], v[26:27], 0 op_sel_hi:[1,1,0]
	v_lshlrev_b32_e32 v32, 16, v114
	v_and_b32_e32 v33, 0xffff0000, v114
	v_pk_fma_f32 v[26:27], v[70:71], v[32:33], v[26:27]
	v_lshlrev_b32_e32 v32, 16, v118
	v_and_b32_e32 v33, 0xffff0000, v118
	v_pk_fma_f32 v[26:27], v[74:75], v[32:33], v[26:27]
	v_lshlrev_b32_e32 v32, 16, v122
	v_and_b32_e32 v33, 0xffff0000, v122
	v_pk_fma_f32 v[26:27], v[78:79], v[32:33], v[26:27]
	v_and_b32_e32 v37, 0xffff0000, v111
	v_mul_f32_e32 v23, 0xbfb8aa3b, v27
	v_exp_f32_e32 v23, v23
	v_mul_f32_e32 v32, 0xbfb8aa3b, v26
	v_exp_f32_e32 v32, v32
	v_pk_fma_f32 v[36:37], v[64:65], v[36:37], 0 op_sel_hi:[1,1,0]
	v_lshlrev_b32_e32 v38, 16, v115
	v_and_b32_e32 v39, 0xffff0000, v115
	v_pk_fma_f32 v[36:37], v[68:69], v[38:39], v[36:37]
	v_lshlrev_b32_e32 v38, 16, v119
	v_and_b32_e32 v39, 0xffff0000, v119
	v_pk_fma_f32 v[36:37], v[72:73], v[38:39], v[36:37]
	v_lshlrev_b32_e32 v38, 16, v123
	v_and_b32_e32 v39, 0xffff0000, v123
	v_add_f32_e32 v23, 1.0, v23
	v_pk_fma_f32 v[36:37], v[76:77], v[38:39], v[36:37]
	v_rcp_f32_e32 v33, v23
	v_add_f32_e32 v23, 1.0, v32
	v_mul_f32_e32 v32, 0xbfb8aa3b, v37
	v_exp_f32_e32 v38, v32
	v_mul_f32_e32 v32, 0xbfb8aa3b, v36
	v_exp_f32_e32 v64, v32
	v_rcp_f32_e32 v32, v23
	v_add_f32_e32 v23, 1.0, v38
	v_rcp_f32_e32 v39, v23
	v_add_f32_e32 v23, 1.0, v64
	v_rcp_f32_e32 v38, v23
	v_add_u32_e32 v66, 0x8110, v1
	v_pk_mul_f32 v[26:27], v[26:27], v[32:33]
	ds_write2_b32 v66, v26, v27 offset1:1
	v_add_u32_e32 v23, 0x8118, v1
	v_pk_mul_f32 v[26:27], v[36:37], v[38:39]
	ds_write2_b32 v23, v26, v27 offset1:1
	v_lshlrev_b32_e32 v26, 16, v16
	v_and_b32_e32 v27, 0xffff0000, v16
	v_pk_fma_f32 v[26:27], v[50:51], v[26:27], 0 op_sel_hi:[1,1,0]
	v_lshlrev_b32_e32 v32, 16, v12
	v_and_b32_e32 v33, 0xffff0000, v12
	v_pk_fma_f32 v[26:27], v[54:55], v[32:33], v[26:27]
	v_lshlrev_b32_e32 v32, 16, v8
	v_and_b32_e32 v33, 0xffff0000, v8
	v_pk_fma_f32 v[26:27], v[58:59], v[32:33], v[26:27]
	v_lshlrev_b32_e32 v32, 16, v4
	v_and_b32_e32 v33, 0xffff0000, v4
	v_pk_fma_f32 v[26:27], v[62:63], v[32:33], v[26:27]
	v_lshlrev_b32_e32 v16, 16, v17
	v_mul_f32_e32 v4, 0xbfb8aa3b, v27
	v_mul_f32_e32 v8, 0xbfb8aa3b, v26
	v_exp_f32_e32 v4, v4
	v_exp_f32_e32 v8, v8
	v_and_b32_e32 v17, 0xffff0000, v17
	v_pk_fma_f32 v[16:17], v[48:49], v[16:17], 0 op_sel_hi:[1,1,0]
	v_lshlrev_b32_e32 v12, 16, v13
	v_and_b32_e32 v13, 0xffff0000, v13
	v_add_f32_e32 v4, 1.0, v4
	v_add_f32_e32 v32, 1.0, v8
	v_pk_fma_f32 v[12:13], v[52:53], v[12:13], v[16:17]
	v_lshlrev_b32_e32 v8, 16, v9
	v_and_b32_e32 v9, 0xffff0000, v9
	v_rcp_f32_e32 v33, v4
	v_pk_fma_f32 v[8:9], v[56:57], v[8:9], v[12:13]
	v_lshlrev_b32_e32 v4, 16, v5
	v_and_b32_e32 v5, 0xffff0000, v5
	v_pk_fma_f32 v[4:5], v[60:61], v[4:5], v[8:9]
	v_rcp_f32_e32 v32, v32
	v_mul_f32_e32 v8, 0xbfb8aa3b, v5
	v_exp_f32_e32 v8, v8
	v_mul_f32_e32 v9, 0xbfb8aa3b, v4
	v_exp_f32_e32 v12, v9
	v_add_u32_e32 v23, 0x8120, v1
	v_add_f32_e32 v8, 1.0, v8
	v_rcp_f32_e32 v9, v8
	v_add_f32_e32 v8, 1.0, v12
	v_rcp_f32_e32 v8, v8
	v_pk_mul_f32 v[12:13], v[26:27], v[32:33]
	ds_write2_b32 v23, v12, v13 offset1:1
	v_add_u32_e32 v12, 0x8128, v1
	v_pk_mul_f32 v[4:5], v[4:5], v[8:9]
	ds_write2_b32 v12, v4, v5 offset1:1
	v_lshlrev_b32_e32 v4, 16, v18
	v_and_b32_e32 v5, 0xffff0000, v18
	v_pk_fma_f32 v[4:5], v[46:47], v[4:5], 0 op_sel_hi:[1,1,0]
	v_lshlrev_b32_e32 v8, 16, v14
	v_and_b32_e32 v9, 0xffff0000, v14
	v_pk_fma_f32 v[4:5], v[44:45], v[8:9], v[4:5]
	v_lshlrev_b32_e32 v8, 16, v10
	v_and_b32_e32 v9, 0xffff0000, v10
	v_pk_fma_f32 v[4:5], v[42:43], v[8:9], v[4:5]
	v_lshlrev_b32_e32 v8, 16, v6
	v_and_b32_e32 v9, 0xffff0000, v6
	v_pk_fma_f32 v[4:5], v[40:41], v[8:9], v[4:5]
	v_lshlrev_b32_e32 v12, 16, v19
	v_mul_f32_e32 v6, 0xbfb8aa3b, v5
	v_exp_f32_e32 v6, v6
	v_and_b32_e32 v13, 0xffff0000, v19
	v_pk_fma_f32 v[12:13], v[34:35], v[12:13], 0 op_sel_hi:[1,1,0]
	v_lshlrev_b32_e32 v14, 16, v15
	v_and_b32_e32 v15, 0xffff0000, v15
	v_add_f32_e32 v6, 1.0, v6
	v_pk_fma_f32 v[12:13], v[30:31], v[14:15], v[12:13]
	v_lshlrev_b32_e32 v10, 16, v11
	v_and_b32_e32 v11, 0xffff0000, v11
	v_rcp_f32_e32 v9, v6
	v_pk_fma_f32 v[10:11], v[28:29], v[10:11], v[12:13]
	v_lshlrev_b32_e32 v6, 16, v7
	v_and_b32_e32 v7, 0xffff0000, v7
	v_pk_fma_f32 v[6:7], v[24:25], v[6:7], v[10:11]
	v_mul_f32_e32 v8, 0xbfb8aa3b, v4
	v_mul_f32_e32 v10, 0xbfb8aa3b, v7
	v_exp_f32_e32 v8, v8
	v_exp_f32_e32 v10, v10
	v_mul_f32_e32 v11, 0xbfb8aa3b, v6
	v_exp_f32_e32 v12, v11
	v_add_f32_e32 v8, 1.0, v8
	v_add_f32_e32 v10, 1.0, v10
	v_rcp_f32_e32 v8, v8
	v_rcp_f32_e32 v11, v10
	v_add_f32_e32 v10, 1.0, v12
	v_rcp_f32_e32 v10, v10
	v_add_u32_e32 v16, 0x8130, v1
	v_pk_mul_f32 v[4:5], v[4:5], v[8:9]
	ds_write2_b32 v16, v4, v5 offset1:1
	v_add_u32_e32 v1, 0x8138, v1
	v_pk_mul_f32 v[4:5], v[6:7], v[10:11]
	ds_write2_b32 v1, v4, v5 offset1:1
	v_or_b32_e32 v1, s4, v2
	v_mul_u32_u24_e32 v1, 0x110, v1
	v_lshlrev_b32_e32 v8, 4, v21
	v_add3_u32 v23, s0, v1, v8
	s_waitcnt lgkmcnt(0)
	s_barrier
	ds_read_b128 v[4:7], v23
	v_and_or_b32 v1, s1, 32, v2
	v_mul_u32_u24_e32 v2, 0x110, v1
	v_add3_u32 v2, s24, v2, v8
	ds_read_b128 v[8:11], v2
	ds_read_b128 v[24:27], v23 offset:32
	ds_read_b128 v[28:31], v2 offset:32
	s_waitcnt lgkmcnt(2)
	v_mfma_f32_32x32x16_bf16 v[4:19], v[4:7], v[8:11], 0
	v_lshl_or_b32 v21, v21, 2, s4
	s_lshl_b64 s[0:1], s[16:17], 13
	s_add_u32 s0, s12, s0
	s_addc_u32 s1, s13, s1
	s_add_u32 s4, s0, 0x46a00000
	s_addc_u32 s5, s1, 0
	s_and_b64 vcc, exec, s[18:19]
	s_waitcnt lgkmcnt(0)
	v_mfma_f32_32x32x16_bf16 v[4:19], v[24:27], v[28:31], v[4:19]
	ds_read_b128 v[24:27], v23 offset:64
	ds_read_b128 v[28:31], v2 offset:64
	ds_read_b128 v[32:35], v23 offset:96
	ds_read_b128 v[36:39], v2 offset:96
	v_cmp_ge_u32_e64 s[0:1], v21, v1
	s_waitcnt lgkmcnt(2)
	v_mfma_f32_32x32x16_bf16 v[4:19], v[24:27], v[28:31], v[4:19]
	s_waitcnt lgkmcnt(0)
	v_mfma_f32_32x32x16_bf16 v[4:19], v[32:35], v[36:39], v[4:19]
	ds_read_b128 v[24:27], v23 offset:128
	ds_read_b128 v[28:31], v2 offset:128
	ds_read_b128 v[32:35], v23 offset:160
	ds_read_b128 v[36:39], v2 offset:160
	s_waitcnt lgkmcnt(2)
	v_mfma_f32_32x32x16_bf16 v[4:19], v[24:27], v[28:31], v[4:19]
	s_waitcnt lgkmcnt(0)
	v_mfma_f32_32x32x16_bf16 v[4:19], v[32:35], v[36:39], v[4:19]
	ds_read_b128 v[24:27], v23 offset:192
	ds_read_b128 v[28:31], v2 offset:192
	ds_read_b128 v[32:35], v23 offset:224
	ds_read_b128 v[36:39], v2 offset:224
	v_lshl_add_u32 v2, v1, 2, s28
	v_lshl_add_u32 v23, v21, 2, s28
	s_waitcnt lgkmcnt(2)
	v_mfma_f32_32x32x16_bf16 v[4:19], v[24:27], v[28:31], v[4:19]
	ds_read_b32 v25, v2
	ds_read_b32 v2, v23
	v_lshlrev_b32_e32 v24, 1, v1
	s_waitcnt lgkmcnt(0)
	v_sub_f32_e32 v2, v2, v25
	v_min_f32_e32 v2, 0, v2
	v_mfma_f32_32x32x16_bf16 v[4:19], v[32:35], v[36:39], v[4:19]
	v_mul_f32_e32 v2, 0x3fb8aa3b, v2
	v_exp_f32_e32 v26, v2
	s_cbranch_vccz .LBB0_266
	s_nop 8
	v_mul_f32_e32 v2, v4, v26
	v_cvt_pk_bf16_f32 v2, v2, s0
	v_cndmask_b32_e64 v23, 0, v2, s[0:1]
	v_lshl_or_b32 v2, v21, 7, v24
	v_lshl_add_u64 v[28:29], s[4:5], 0, v[2:3]
	global_store_short v[28:29], v23, off
	s_mov_b64 s[20:21], 0

.LBB0_373:
	s_or_b64 exec, exec, s[4:5]
	v_mov_b32_e32 v1, v3
	s_nop 0
	v_lshl_add_u32 v21, v1, 2, s26
	ds_read_b128 v[70:73], v21
	ds_read_b128 v[74:77], v21 offset:16
	ds_read_b128 v[78:81], v21 offset:32
	ds_read_b128 v[82:85], v21 offset:48
	ds_read_b128 v[86:89], v21 offset:64
	ds_read_b128 v[90:93], v21 offset:80
	ds_read_b128 v[94:97], v21 offset:96
	ds_read_b128 v[98:101], v21 offset:112
	ds_read_b128 v[102:105], v21 offset:128
	ds_read_b128 v[106:109], v21 offset:144
	ds_read_b128 v[110:113], v21 offset:160
	ds_read_b128 v[114:117], v21 offset:176
	ds_read_b128 v[118:121], v21 offset:192
	ds_read_b128 v[122:125], v21 offset:208
	ds_read_b128 v[126:129], v21 offset:224
	ds_read_b128 v[130:133], v21 offset:240
	ds_read_b128 v[134:137], v21 offset:272
	ds_read_b128 v[138:141], v21 offset:288
	ds_read_b128 v[142:145], v21 offset:304
	ds_read_b128 v[146:149], v21 offset:320
	ds_read_b128 v[150:153], v21 offset:336
	ds_read_b128 v[154:157], v21 offset:352
	ds_read_b128 v[158:161], v21 offset:368
	ds_read_b128 v[162:165], v21 offset:384
	ds_read_b128 v[166:169], v21 offset:400
	ds_read_b128 v[170:173], v21 offset:416
	ds_read_b128 v[174:177], v21 offset:432
	ds_read_b128 v[178:181], v21 offset:448
	ds_read_b128 v[182:185], v21 offset:464
	ds_read_b128 v[186:189], v21 offset:480
	ds_read_b128 v[194:197], v21 offset:496
	ds_read_b128 v[198:201], v21 offset:512
	s_waitcnt lgkmcnt(0)
	v_fma_f32 v1, -v4, v70, v4
	v_fma_f32 v2, -v4, v71, v5
	v_fma_f32 v5, -v4, v72, v6
	v_fma_f32 v6, -v4, v73, v7
	v_fma_f32 v7, -v4, v74, v8
	v_fma_f32 v74, -v4, v75, v9
	v_fma_f32 v75, -v4, v76, v10
	v_fma_f32 v76, -v4, v77, v11
	v_fma_f32 v77, -v4, v78, v12
	v_fma_f32 v78, -v4, v79, v13
	v_fma_f32 v79, -v4, v80, v14
	v_fma_f32 v80, -v4, v81, v15
	v_fma_f32 v81, -v4, v82, v16
	v_fma_f32 v82, -v4, v83, v17
	v_fma_f32 v83, -v4, v84, v18
	v_fma_f32 v84, -v4, v85, v19
	v_fma_f32 v85, -v4, v86, v22
	v_fma_f32 v86, -v4, v87, v23
	v_fma_f32 v87, -v4, v88, v24
	v_fma_f32 v88, -v4, v89, v25
	v_fma_f32 v89, -v4, v90, v26
	v_fma_f32 v90, -v4, v91, v27
	v_fma_f32 v91, -v4, v92, v28
	v_fma_f32 v92, -v4, v93, v29
	v_fma_f32 v93, -v4, v94, v30
	v_fma_f32 v94, -v4, v95, v31
	v_fma_f32 v95, -v4, v96, v32
	v_fma_f32 v96, -v4, v97, v33
	v_fma_f32 v97, -v4, v98, v34
	v_fma_f32 v98, -v4, v99, v35
	v_fma_f32 v99, -v4, v100, v36
	v_fma_f32 v100, -v4, v101, v37
	v_fma_f32 v101, -v4, v102, v38
	v_fma_f32 v102, -v4, v103, v39
	v_fma_f32 v103, -v4, v104, v40
	v_fma_f32 v104, -v4, v105, v41
	v_fma_f32 v105, -v4, v106, v42
	v_fma_f32 v106, -v4, v107, v43
	v_fma_f32 v107, -v4, v108, v44
	v_fma_f32 v108, -v4, v109, v45
	v_fma_f32 v109, -v4, v110, v46
	v_fma_f32 v110, -v4, v111, v47
	v_fma_f32 v111, -v4, v112, v48
	v_fma_f32 v112, -v4, v113, v49
	v_fma_f32 v113, -v4, v114, v50
	v_fma_f32 v114, -v4, v115, v51
	v_fma_f32 v115, -v4, v116, v52
	v_fma_f32 v116, -v4, v117, v53
	v_fma_f32 v117, -v4, v118, v54
	v_fma_f32 v118, -v4, v119, v55
	v_fma_f32 v119, -v4, v120, v56
	v_fma_f32 v120, -v4, v121, v57
	v_fma_f32 v121, -v4, v122, v58
	v_fma_f32 v122, -v4, v123, v59
	v_fma_f32 v123, -v4, v124, v60
	v_fma_f32 v124, -v4, v125, v61
	v_fma_f32 v125, -v4, v126, v62
	v_fma_f32 v126, -v4, v127, v63
	v_fma_f32 v127, -v4, v128, v64
	v_fma_f32 v128, -v4, v129, v65
	v_fma_f32 v129, -v4, v130, v66
	v_fma_f32 v130, -v4, v131, v67
	v_fma_f32 v131, -v4, v132, v68
	v_fma_f32 v4, -v4, v133, v69
	ds_read_b128 v[8:11], v21 offset:544
	ds_read_b128 v[12:15], v21 offset:560
	ds_read_b128 v[16:19], v21 offset:576
	ds_read_b128 v[22:25], v21 offset:592
	ds_read_b128 v[26:29], v21 offset:608
	ds_read_b128 v[30:33], v21 offset:624
	ds_read_b128 v[34:37], v21 offset:640
	ds_read_b128 v[38:41], v21 offset:656
	ds_read_b128 v[42:45], v21 offset:672
	ds_read_b128 v[46:49], v21 offset:688
	ds_read_b128 v[50:53], v21 offset:704
	ds_read_b128 v[54:57], v21 offset:720
	ds_read_b128 v[58:61], v21 offset:736
	ds_read_b128 v[62:65], v21 offset:752
	ds_read_b128 v[66:69], v21 offset:768
	ds_read_b128 v[70:73], v21 offset:784
	v_fma_f32 v1, -v2, v134, v1
	v_fma_f32 v134, -v2, v135, v2
	v_fma_f32 v5, -v2, v136, v5
	v_fma_f32 v135, -v2, v137, v6
	v_fma_f32 v136, -v2, v138, v7
	v_fma_f32 v137, -v2, v139, v74
	v_fma_f32 v138, -v2, v140, v75
	v_fma_f32 v139, -v2, v141, v76
	v_fma_f32 v140, -v2, v142, v77
	v_fma_f32 v141, -v2, v143, v78
	v_fma_f32 v142, -v2, v144, v79
	v_fma_f32 v143, -v2, v145, v80
	v_fma_f32 v144, -v2, v146, v81
	v_fma_f32 v145, -v2, v147, v82
	v_fma_f32 v146, -v2, v148, v83
	v_fma_f32 v147, -v2, v149, v84
	v_fma_f32 v148, -v2, v150, v85
	v_fma_f32 v149, -v2, v151, v86
	v_fma_f32 v150, -v2, v152, v87
	v_fma_f32 v151, -v2, v153, v88
	v_fma_f32 v152, -v2, v154, v89
	v_fma_f32 v153, -v2, v155, v90
	v_fma_f32 v154, -v2, v156, v91
	v_fma_f32 v155, -v2, v157, v92
	v_fma_f32 v156, -v2, v158, v93
	v_fma_f32 v157, -v2, v159, v94
	v_fma_f32 v158, -v2, v160, v95
	v_fma_f32 v159, -v2, v161, v96
	v_fma_f32 v160, -v2, v162, v97
	v_fma_f32 v161, -v2, v163, v98
	v_fma_f32 v162, -v2, v164, v99
	v_fma_f32 v163, -v2, v165, v100
	v_fma_f32 v164, -v2, v166, v101
	v_fma_f32 v165, -v2, v167, v102
	v_fma_f32 v166, -v2, v168, v103
	v_fma_f32 v167, -v2, v169, v104
	v_fma_f32 v168, -v2, v170, v105
	v_fma_f32 v169, -v2, v171, v106
	v_fma_f32 v170, -v2, v172, v107
	v_fma_f32 v171, -v2, v173, v108
	v_fma_f32 v172, -v2, v174, v109
	v_fma_f32 v173, -v2, v175, v110
	v_fma_f32 v174, -v2, v176, v111
	v_fma_f32 v175, -v2, v177, v112
	v_fma_f32 v176, -v2, v178, v113
	v_fma_f32 v177, -v2, v179, v114
	v_fma_f32 v178, -v2, v180, v115
	v_fma_f32 v179, -v2, v181, v116
	v_fma_f32 v180, -v2, v182, v117
	v_fma_f32 v181, -v2, v183, v118
	v_fma_f32 v182, -v2, v184, v119
	v_fma_f32 v183, -v2, v185, v120
	v_fma_f32 v184, -v2, v186, v121
	v_fma_f32 v185, -v2, v187, v122
	v_fma_f32 v186, -v2, v188, v123
	v_fma_f32 v187, -v2, v189, v124
	v_fma_f32 v188, -v2, v194, v125
	v_fma_f32 v189, -v2, v195, v126
	v_fma_f32 v190, -v2, v196, v127
	v_fma_f32 v191, -v2, v197, v128
	v_fma_f32 v192, -v2, v198, v129
	v_fma_f32 v193, -v2, v199, v130
	v_fma_f32 v194, -v2, v200, v131
	v_fma_f32 v4, -v2, v201, v4
	ds_read_b128 v[74:77], v21 offset:832
	ds_read_b128 v[78:81], v21 offset:848
	ds_read_b128 v[82:85], v21 offset:864
	ds_read_b128 v[86:89], v21 offset:880
	ds_read_b128 v[90:93], v21 offset:896
	ds_read_b128 v[94:97], v21 offset:912
	ds_read_b128 v[98:101], v21 offset:928
	ds_read_b128 v[102:105], v21 offset:944
	ds_read_b128 v[106:109], v21 offset:960
	ds_read_b128 v[110:113], v21 offset:976
	ds_read_b128 v[114:117], v21 offset:992
	ds_read_b128 v[118:121], v21 offset:1008
	ds_read_b128 v[122:125], v21 offset:1024
	ds_read_b128 v[126:129], v21 offset:1040
	ds_read_b128 v[130:133], v21 offset:1056
	s_waitcnt lgkmcnt(0)
	v_fma_f32 v7, -v5, v8, v1
	v_fma_f32 v6, -v5, v9, v134
	v_fma_f32 v2, -v5, v10, v5
	v_fma_f32 v1, -v5, v11, v135
	v_mov_b32_e32 v202, v5
	v_pk_fma_f32 v[134:135], v[202:203], v[12:13], v[136:137] op_sel_hi:[0,1,1] neg_lo:[1,0,0] neg_hi:[1,0,0]
	v_pk_fma_f32 v[136:137], v[202:203], v[14:15], v[138:139] op_sel_hi:[0,1,1] neg_lo:[1,0,0] neg_hi:[1,0,0]
	v_pk_fma_f32 v[138:139], v[202:203], v[16:17], v[140:141] op_sel_hi:[0,1,1] neg_lo:[1,0,0] neg_hi:[1,0,0]
	v_pk_fma_f32 v[140:141], v[202:203], v[18:19], v[142:143] op_sel_hi:[0,1,1] neg_lo:[1,0,0] neg_hi:[1,0,0]
	v_pk_fma_f32 v[142:143], v[202:203], v[22:23], v[144:145] op_sel_hi:[0,1,1] neg_lo:[1,0,0] neg_hi:[1,0,0]
	v_pk_fma_f32 v[144:145], v[202:203], v[24:25], v[146:147] op_sel_hi:[0,1,1] neg_lo:[1,0,0] neg_hi:[1,0,0]
	v_pk_fma_f32 v[146:147], v[202:203], v[26:27], v[148:149] op_sel_hi:[0,1,1] neg_lo:[1,0,0] neg_hi:[1,0,0]
	v_pk_fma_f32 v[148:149], v[202:203], v[28:29], v[150:151] op_sel_hi:[0,1,1] neg_lo:[1,0,0] neg_hi:[1,0,0]
	v_pk_fma_f32 v[150:151], v[202:203], v[30:31], v[152:153] op_sel_hi:[0,1,1] neg_lo:[1,0,0] neg_hi:[1,0,0]
	v_pk_fma_f32 v[152:153], v[202:203], v[32:33], v[154:155] op_sel_hi:[0,1,1] neg_lo:[1,0,0] neg_hi:[1,0,0]
	v_pk_fma_f32 v[154:155], v[202:203], v[34:35], v[156:157] op_sel_hi:[0,1,1] neg_lo:[1,0,0] neg_hi:[1,0,0]
	v_pk_fma_f32 v[156:157], v[202:203], v[36:37], v[158:159] op_sel_hi:[0,1,1] neg_lo:[1,0,0] neg_hi:[1,0,0]
	v_pk_fma_f32 v[158:159], v[202:203], v[38:39], v[160:161] op_sel_hi:[0,1,1] neg_lo:[1,0,0] neg_hi:[1,0,0]
	v_pk_fma_f32 v[160:161], v[202:203], v[40:41], v[162:163] op_sel_hi:[0,1,1] neg_lo:[1,0,0] neg_hi:[1,0,0]
	v_pk_fma_f32 v[162:163], v[202:203], v[42:43], v[164:165] op_sel_hi:[0,1,1] neg_lo:[1,0,0] neg_hi:[1,0,0]
	v_pk_fma_f32 v[164:165], v[202:203], v[44:45], v[166:167] op_sel_hi:[0,1,1] neg_lo:[1,0,0] neg_hi:[1,0,0]
	v_pk_fma_f32 v[166:167], v[202:203], v[46:47], v[168:169] op_sel_hi:[0,1,1] neg_lo:[1,0,0] neg_hi:[1,0,0]
	v_pk_fma_f32 v[168:169], v[202:203], v[48:49], v[170:171] op_sel_hi:[0,1,1] neg_lo:[1,0,0] neg_hi:[1,0,0]
	v_pk_fma_f32 v[170:171], v[202:203], v[50:51], v[172:173] op_sel_hi:[0,1,1] neg_lo:[1,0,0] neg_hi:[1,0,0]
	v_pk_fma_f32 v[172:173], v[202:203], v[52:53], v[174:175] op_sel_hi:[0,1,1] neg_lo:[1,0,0] neg_hi:[1,0,0]
	v_pk_fma_f32 v[174:175], v[202:203], v[54:55], v[176:177] op_sel_hi:[0,1,1] neg_lo:[1,0,0] neg_hi:[1,0,0]
	v_pk_fma_f32 v[176:177], v[202:203], v[56:57], v[178:179] op_sel_hi:[0,1,1] neg_lo:[1,0,0] neg_hi:[1,0,0]
	v_pk_fma_f32 v[178:179], v[202:203], v[58:59], v[180:181] op_sel_hi:[0,1,1] neg_lo:[1,0,0] neg_hi:[1,0,0]
	v_pk_fma_f32 v[180:181], v[202:203], v[60:61], v[182:183] op_sel_hi:[0,1,1] neg_lo:[1,0,0] neg_hi:[1,0,0]
	v_pk_fma_f32 v[182:183], v[202:203], v[62:63], v[184:185] op_sel_hi:[0,1,1] neg_lo:[1,0,0] neg_hi:[1,0,0]
	v_pk_fma_f32 v[184:185], v[202:203], v[64:65], v[186:187] op_sel_hi:[0,1,1] neg_lo:[1,0,0] neg_hi:[1,0,0]
	v_pk_fma_f32 v[186:187], v[202:203], v[66:67], v[188:189] op_sel_hi:[0,1,1] neg_lo:[1,0,0] neg_hi:[1,0,0]
	v_pk_fma_f32 v[188:189], v[202:203], v[68:69], v[190:191] op_sel_hi:[0,1,1] neg_lo:[1,0,0] neg_hi:[1,0,0]
	v_pk_fma_f32 v[70:71], v[202:203], v[70:71], v[192:193] op_sel_hi:[0,1,1] neg_lo:[1,0,0] neg_hi:[1,0,0]
	v_fma_f32 v72, -v5, v72, v194
	v_fma_f32 v4, -v5, v73, v4
	ds_read_b128 v[8:11], v21 offset:1104
	ds_read_b128 v[12:15], v21 offset:1120
	ds_read_b128 v[16:19], v21 offset:1136
	ds_read_b128 v[22:25], v21 offset:1152
	ds_read_b128 v[26:29], v21 offset:1168
	ds_read_b128 v[30:33], v21 offset:1184
	ds_read_b128 v[34:37], v21 offset:1200
	ds_read_b128 v[38:41], v21 offset:1216
	ds_read_b128 v[42:45], v21 offset:1232
	ds_read_b128 v[46:49], v21 offset:1248
	ds_read_b128 v[50:53], v21 offset:1264
	ds_read_b128 v[54:57], v21 offset:1280
	ds_read_b128 v[58:61], v21 offset:1296
	ds_read_b128 v[62:65], v21 offset:1312
	ds_read_b128 v[66:69], v21 offset:1328
	v_fma_f32 v5, -v1, v74, v134
	v_fma_f32 v134, -v1, v75, v135
	v_fma_f32 v135, -v1, v76, v136
	v_fma_f32 v136, -v1, v77, v137
	v_fma_f32 v137, -v1, v78, v138
	v_fma_f32 v138, -v1, v79, v139
	v_fma_f32 v139, -v1, v80, v140
	v_fma_f32 v140, -v1, v81, v141
	v_fma_f32 v141, -v1, v82, v142
	v_fma_f32 v142, -v1, v83, v143
	v_fma_f32 v143, -v1, v84, v144
	v_fma_f32 v144, -v1, v85, v145
	v_fma_f32 v145, -v1, v86, v146
	v_fma_f32 v146, -v1, v87, v147
	v_fma_f32 v147, -v1, v88, v148
	v_fma_f32 v148, -v1, v89, v149
	v_fma_f32 v149, -v1, v90, v150
	v_fma_f32 v150, -v1, v91, v151
	v_fma_f32 v151, -v1, v92, v152
	v_fma_f32 v152, -v1, v93, v153
	v_fma_f32 v153, -v1, v94, v154
	v_fma_f32 v154, -v1, v95, v155
	v_fma_f32 v155, -v1, v96, v156
	v_fma_f32 v156, -v1, v97, v157
	v_fma_f32 v157, -v1, v98, v158
	v_fma_f32 v158, -v1, v99, v159
	v_fma_f32 v159, -v1, v100, v160
	v_fma_f32 v160, -v1, v101, v161
	v_fma_f32 v161, -v1, v102, v162
	v_fma_f32 v162, -v1, v103, v163
	v_fma_f32 v163, -v1, v104, v164
	v_fma_f32 v164, -v1, v105, v165
	v_fma_f32 v165, -v1, v106, v166
	v_fma_f32 v166, -v1, v107, v167
	v_fma_f32 v167, -v1, v108, v168
	v_fma_f32 v168, -v1, v109, v169
	v_fma_f32 v169, -v1, v110, v170
	v_fma_f32 v170, -v1, v111, v171
	v_fma_f32 v171, -v1, v112, v172
	v_fma_f32 v172, -v1, v113, v173
	v_fma_f32 v173, -v1, v114, v174
	v_fma_f32 v174, -v1, v115, v175
	v_fma_f32 v175, -v1, v116, v176
	v_fma_f32 v176, -v1, v117, v177
	v_fma_f32 v177, -v1, v118, v178
	v_fma_f32 v178, -v1, v119, v179
	v_fma_f32 v179, -v1, v120, v180
	v_fma_f32 v180, -v1, v121, v181
	v_fma_f32 v181, -v1, v122, v182
	v_fma_f32 v182, -v1, v123, v183
	v_fma_f32 v183, -v1, v124, v184
	v_fma_f32 v184, -v1, v125, v185
	v_fma_f32 v185, -v1, v126, v186
	v_fma_f32 v186, -v1, v127, v187
	v_fma_f32 v187, -v1, v128, v188
	v_fma_f32 v188, -v1, v129, v189
	v_mov_b32_e32 v202, v1
	v_pk_fma_f32 v[130:131], v[202:203], v[130:131], v[70:71] op_sel_hi:[0,1,1] neg_lo:[1,0,0] neg_hi:[1,0,0]
	v_fma_f32 v132, -v1, v132, v72
	v_fma_f32 v4, -v1, v133, v4
	ds_read_b128 v[70:73], v21 offset:1376
	ds_read_b128 v[74:77], v21 offset:1392
	ds_read_b128 v[78:81], v21 offset:1408
	ds_read_b128 v[82:85], v21 offset:1424
	ds_read_b128 v[86:89], v21 offset:1440
	ds_read_b128 v[90:93], v21 offset:1456
	ds_read_b128 v[94:97], v21 offset:1472
	ds_read_b128 v[98:101], v21 offset:1488
	ds_read_b128 v[102:105], v21 offset:1504
	ds_read_b128 v[106:109], v21 offset:1520
	ds_read_b128 v[110:113], v21 offset:1536
	ds_read_b128 v[114:117], v21 offset:1552
	ds_read_b128 v[118:121], v21 offset:1568
	ds_read_b128 v[122:125], v21 offset:1584
	ds_read_b128 v[126:129], v21 offset:1600
	s_waitcnt lgkmcnt(0)
	v_fma_f32 v8, -v5, v8, v5
	v_fma_f32 v9, -v5, v9, v134
	v_fma_f32 v10, -v5, v10, v135
	v_fma_f32 v11, -v5, v11, v136
	v_fma_f32 v134, -v5, v12, v137
	v_fma_f32 v135, -v5, v13, v138
	v_fma_f32 v136, -v5, v14, v139
	v_fma_f32 v137, -v5, v15, v140
	v_fma_f32 v138, -v5, v16, v141
	v_fma_f32 v139, -v5, v17, v142
	v_fma_f32 v140, -v5, v18, v143
	v_fma_f32 v141, -v5, v19, v144
	v_fma_f32 v142, -v5, v22, v145
	v_fma_f32 v143, -v5, v23, v146
	v_fma_f32 v144, -v5, v24, v147
	v_fma_f32 v145, -v5, v25, v148
	v_fma_f32 v146, -v5, v26, v149
	v_fma_f32 v147, -v5, v27, v150
	v_fma_f32 v148, -v5, v28, v151
	v_fma_f32 v149, -v5, v29, v152
	v_fma_f32 v150, -v5, v30, v153
	v_fma_f32 v151, -v5, v31, v154
	v_fma_f32 v152, -v5, v32, v155
	v_fma_f32 v153, -v5, v33, v156
	v_fma_f32 v154, -v5, v34, v157
	v_fma_f32 v155, -v5, v35, v158
	v_fma_f32 v156, -v5, v36, v159
	v_fma_f32 v157, -v5, v37, v160
	v_fma_f32 v158, -v5, v38, v161
	v_fma_f32 v159, -v5, v39, v162
	v_fma_f32 v160, -v5, v40, v163
	v_fma_f32 v161, -v5, v41, v164
	v_fma_f32 v162, -v5, v42, v165
	v_fma_f32 v163, -v5, v43, v166
	v_fma_f32 v164, -v5, v44, v167
	v_fma_f32 v165, -v5, v45, v168
	v_fma_f32 v166, -v5, v46, v169
	v_fma_f32 v167, -v5, v47, v170
	v_fma_f32 v168, -v5, v48, v171
	v_fma_f32 v169, -v5, v49, v172
	v_fma_f32 v170, -v5, v50, v173
	v_fma_f32 v171, -v5, v51, v174
	v_fma_f32 v172, -v5, v52, v175
	v_fma_f32 v173, -v5, v53, v176
	v_fma_f32 v174, -v5, v54, v177
	v_fma_f32 v175, -v5, v55, v178
	v_fma_f32 v176, -v5, v56, v179
	v_fma_f32 v177, -v5, v57, v180
	v_fma_f32 v178, -v5, v58, v181
	v_fma_f32 v179, -v5, v59, v182
	v_fma_f32 v180, -v5, v60, v183
	v_fma_f32 v181, -v5, v61, v184
	v_fma_f32 v182, -v5, v62, v185
	v_fma_f32 v183, -v5, v63, v186
	v_fma_f32 v184, -v5, v64, v187
	v_fma_f32 v185, -v5, v65, v188
	v_mov_b32_e32 v202, v5
	v_pk_fma_f32 v[186:187], v[202:203], v[66:67], v[130:131] op_sel_hi:[0,1,1] neg_lo:[1,0,0] neg_hi:[1,0,0]
	v_fma_f32 v188, -v5, v68, v132
	v_fma_f32 v4, -v5, v69, v4
	ds_read_b128 v[12:15], v21 offset:1648
	ds_read_b128 v[16:19], v21 offset:1664
	ds_read_b128 v[22:25], v21 offset:1680
	ds_read_b128 v[26:29], v21 offset:1696
	ds_read_b128 v[30:33], v21 offset:1712
	ds_read_b128 v[34:37], v21 offset:1728
	ds_read_b128 v[38:41], v21 offset:1744
	ds_read_b128 v[42:45], v21 offset:1760
	ds_read_b128 v[46:49], v21 offset:1776
	ds_read_b128 v[50:53], v21 offset:1792
	ds_read_b128 v[54:57], v21 offset:1808
	ds_read_b128 v[58:61], v21 offset:1824
	ds_read_b128 v[62:65], v21 offset:1840
	ds_read_b128 v[66:69], v21 offset:1856
	ds_read_b128 v[130:133], v21 offset:1872
	v_fma_f32 v5, -v9, v70, v8
	v_fma_f32 v8, -v9, v71, v9
	v_fma_f32 v189, -v9, v72, v10
	v_fma_f32 v190, -v9, v73, v11
	v_mov_b32_e32 v202, v9
	v_pk_fma_f32 v[134:135], v[202:203], v[74:75], v[134:135] op_sel_hi:[0,1,1] neg_lo:[1,0,0] neg_hi:[1,0,0]
	v_pk_fma_f32 v[136:137], v[202:203], v[76:77], v[136:137] op_sel_hi:[0,1,1] neg_lo:[1,0,0] neg_hi:[1,0,0]
	v_pk_fma_f32 v[138:139], v[202:203], v[78:79], v[138:139] op_sel_hi:[0,1,1] neg_lo:[1,0,0] neg_hi:[1,0,0]
	v_pk_fma_f32 v[140:141], v[202:203], v[80:81], v[140:141] op_sel_hi:[0,1,1] neg_lo:[1,0,0] neg_hi:[1,0,0]
	v_pk_fma_f32 v[142:143], v[202:203], v[82:83], v[142:143] op_sel_hi:[0,1,1] neg_lo:[1,0,0] neg_hi:[1,0,0]
	v_pk_fma_f32 v[144:145], v[202:203], v[84:85], v[144:145] op_sel_hi:[0,1,1] neg_lo:[1,0,0] neg_hi:[1,0,0]
	v_pk_fma_f32 v[146:147], v[202:203], v[86:87], v[146:147] op_sel_hi:[0,1,1] neg_lo:[1,0,0] neg_hi:[1,0,0]
	v_pk_fma_f32 v[148:149], v[202:203], v[88:89], v[148:149] op_sel_hi:[0,1,1] neg_lo:[1,0,0] neg_hi:[1,0,0]
	v_pk_fma_f32 v[150:151], v[202:203], v[90:91], v[150:151] op_sel_hi:[0,1,1] neg_lo:[1,0,0] neg_hi:[1,0,0]
	v_pk_fma_f32 v[152:153], v[202:203], v[92:93], v[152:153] op_sel_hi:[0,1,1] neg_lo:[1,0,0] neg_hi:[1,0,0]
	v_pk_fma_f32 v[154:155], v[202:203], v[94:95], v[154:155] op_sel_hi:[0,1,1] neg_lo:[1,0,0] neg_hi:[1,0,0]
	v_pk_fma_f32 v[156:157], v[202:203], v[96:97], v[156:157] op_sel_hi:[0,1,1] neg_lo:[1,0,0] neg_hi:[1,0,0]
	v_pk_fma_f32 v[158:159], v[202:203], v[98:99], v[158:159] op_sel_hi:[0,1,1] neg_lo:[1,0,0] neg_hi:[1,0,0]
	v_pk_fma_f32 v[160:161], v[202:203], v[100:101], v[160:161] op_sel_hi:[0,1,1] neg_lo:[1,0,0] neg_hi:[1,0,0]
	v_pk_fma_f32 v[162:163], v[202:203], v[102:103], v[162:163] op_sel_hi:[0,1,1] neg_lo:[1,0,0] neg_hi:[1,0,0]
	v_pk_fma_f32 v[164:165], v[202:203], v[104:105], v[164:165] op_sel_hi:[0,1,1] neg_lo:[1,0,0] neg_hi:[1,0,0]
	v_pk_fma_f32 v[166:167], v[202:203], v[106:107], v[166:167] op_sel_hi:[0,1,1] neg_lo:[1,0,0] neg_hi:[1,0,0]
	v_pk_fma_f32 v[168:169], v[202:203], v[108:109], v[168:169] op_sel_hi:[0,1,1] neg_lo:[1,0,0] neg_hi:[1,0,0]
	v_pk_fma_f32 v[170:171], v[202:203], v[110:111], v[170:171] op_sel_hi:[0,1,1] neg_lo:[1,0,0] neg_hi:[1,0,0]
	v_pk_fma_f32 v[172:173], v[202:203], v[112:113], v[172:173] op_sel_hi:[0,1,1] neg_lo:[1,0,0] neg_hi:[1,0,0]
	v_pk_fma_f32 v[174:175], v[202:203], v[114:115], v[174:175] op_sel_hi:[0,1,1] neg_lo:[1,0,0] neg_hi:[1,0,0]
	v_pk_fma_f32 v[176:177], v[202:203], v[116:117], v[176:177] op_sel_hi:[0,1,1] neg_lo:[1,0,0] neg_hi:[1,0,0]
	v_pk_fma_f32 v[178:179], v[202:203], v[118:119], v[178:179] op_sel_hi:[0,1,1] neg_lo:[1,0,0] neg_hi:[1,0,0]
	v_pk_fma_f32 v[180:181], v[202:203], v[120:121], v[180:181] op_sel_hi:[0,1,1] neg_lo:[1,0,0] neg_hi:[1,0,0]
	v_pk_fma_f32 v[182:183], v[202:203], v[122:123], v[182:183] op_sel_hi:[0,1,1] neg_lo:[1,0,0] neg_hi:[1,0,0]
	v_pk_fma_f32 v[184:185], v[202:203], v[124:125], v[184:185] op_sel_hi:[0,1,1] neg_lo:[1,0,0] neg_hi:[1,0,0]
	v_pk_fma_f32 v[126:127], v[202:203], v[126:127], v[186:187] op_sel_hi:[0,1,1] neg_lo:[1,0,0] neg_hi:[1,0,0]
	v_fma_f32 v128, -v9, v128, v188
	v_fma_f32 v4, -v9, v129, v4
	ds_read_b128 v[70:73], v21 offset:1936
	ds_read_b128 v[74:77], v21 offset:1952
	ds_read_b128 v[78:81], v21 offset:1968
	ds_read_b128 v[82:85], v21 offset:1984
	ds_read_b128 v[86:89], v21 offset:2000
	ds_read_b128 v[90:93], v21 offset:2016
	ds_read_b128 v[94:97], v21 offset:2032
	ds_read_b128 v[98:101], v21 offset:2048
	ds_read_b128 v[102:105], v21 offset:2064
	ds_read_b128 v[106:109], v21 offset:2080
	ds_read_b128 v[110:113], v21 offset:2096
	ds_read_b128 v[114:117], v21 offset:2112
	ds_read_b128 v[118:121], v21 offset:2128
	ds_read_b128 v[122:125], v21 offset:2144
	s_waitcnt lgkmcnt(0)
	v_fma_f32 v11, -v189, v12, v5
	v_fma_f32 v10, -v189, v13, v8
	v_fma_f32 v9, -v189, v14, v189
	v_fma_f32 v8, -v189, v15, v190
	v_fma_f32 v5, -v189, v16, v134
	v_fma_f32 v129, -v189, v17, v135
	v_mov_b32_e32 v202, v189
	v_pk_fma_f32 v[134:135], v[202:203], v[18:19], v[136:137] op_sel_hi:[0,1,1] neg_lo:[1,0,0] neg_hi:[1,0,0]
	v_pk_fma_f32 v[136:137], v[202:203], v[22:23], v[138:139] op_sel_hi:[0,1,1] neg_lo:[1,0,0] neg_hi:[1,0,0]
	v_pk_fma_f32 v[138:139], v[202:203], v[24:25], v[140:141] op_sel_hi:[0,1,1] neg_lo:[1,0,0] neg_hi:[1,0,0]
	v_pk_fma_f32 v[140:141], v[202:203], v[26:27], v[142:143] op_sel_hi:[0,1,1] neg_lo:[1,0,0] neg_hi:[1,0,0]
	v_pk_fma_f32 v[142:143], v[202:203], v[28:29], v[144:145] op_sel_hi:[0,1,1] neg_lo:[1,0,0] neg_hi:[1,0,0]
	v_pk_fma_f32 v[144:145], v[202:203], v[30:31], v[146:147] op_sel_hi:[0,1,1] neg_lo:[1,0,0] neg_hi:[1,0,0]
	v_pk_fma_f32 v[146:147], v[202:203], v[32:33], v[148:149] op_sel_hi:[0,1,1] neg_lo:[1,0,0] neg_hi:[1,0,0]
	v_pk_fma_f32 v[148:149], v[202:203], v[34:35], v[150:151] op_sel_hi:[0,1,1] neg_lo:[1,0,0] neg_hi:[1,0,0]
	v_pk_fma_f32 v[150:151], v[202:203], v[36:37], v[152:153] op_sel_hi:[0,1,1] neg_lo:[1,0,0] neg_hi:[1,0,0]
	v_pk_fma_f32 v[152:153], v[202:203], v[38:39], v[154:155] op_sel_hi:[0,1,1] neg_lo:[1,0,0] neg_hi:[1,0,0]
	v_pk_fma_f32 v[154:155], v[202:203], v[40:41], v[156:157] op_sel_hi:[0,1,1] neg_lo:[1,0,0] neg_hi:[1,0,0]
	v_pk_fma_f32 v[156:157], v[202:203], v[42:43], v[158:159] op_sel_hi:[0,1,1] neg_lo:[1,0,0] neg_hi:[1,0,0]
	v_pk_fma_f32 v[158:159], v[202:203], v[44:45], v[160:161] op_sel_hi:[0,1,1] neg_lo:[1,0,0] neg_hi:[1,0,0]
	v_pk_fma_f32 v[160:161], v[202:203], v[46:47], v[162:163] op_sel_hi:[0,1,1] neg_lo:[1,0,0] neg_hi:[1,0,0]
	v_pk_fma_f32 v[162:163], v[202:203], v[48:49], v[164:165] op_sel_hi:[0,1,1] neg_lo:[1,0,0] neg_hi:[1,0,0]
	v_pk_fma_f32 v[164:165], v[202:203], v[50:51], v[166:167] op_sel_hi:[0,1,1] neg_lo:[1,0,0] neg_hi:[1,0,0]
	v_pk_fma_f32 v[166:167], v[202:203], v[52:53], v[168:169] op_sel_hi:[0,1,1] neg_lo:[1,0,0] neg_hi:[1,0,0]
	v_pk_fma_f32 v[168:169], v[202:203], v[54:55], v[170:171] op_sel_hi:[0,1,1] neg_lo:[1,0,0] neg_hi:[1,0,0]
	v_pk_fma_f32 v[170:171], v[202:203], v[56:57], v[172:173] op_sel_hi:[0,1,1] neg_lo:[1,0,0] neg_hi:[1,0,0]
	v_pk_fma_f32 v[172:173], v[202:203], v[58:59], v[174:175] op_sel_hi:[0,1,1] neg_lo:[1,0,0] neg_hi:[1,0,0]
	v_pk_fma_f32 v[174:175], v[202:203], v[60:61], v[176:177] op_sel_hi:[0,1,1] neg_lo:[1,0,0] neg_hi:[1,0,0]
	v_pk_fma_f32 v[176:177], v[202:203], v[62:63], v[178:179] op_sel_hi:[0,1,1] neg_lo:[1,0,0] neg_hi:[1,0,0]
	v_pk_fma_f32 v[178:179], v[202:203], v[64:65], v[180:181] op_sel_hi:[0,1,1] neg_lo:[1,0,0] neg_hi:[1,0,0]
	v_pk_fma_f32 v[180:181], v[202:203], v[66:67], v[182:183] op_sel_hi:[0,1,1] neg_lo:[1,0,0] neg_hi:[1,0,0]
	v_pk_fma_f32 v[182:183], v[202:203], v[68:69], v[184:185] op_sel_hi:[0,1,1] neg_lo:[1,0,0] neg_hi:[1,0,0]
	v_pk_fma_f32 v[126:127], v[202:203], v[130:131], v[126:127] op_sel_hi:[0,1,1] neg_lo:[1,0,0] neg_hi:[1,0,0]
	v_fma_f32 v128, -v189, v132, v128
	v_fma_f32 v4, -v189, v133, v4
	ds_read_b128 v[12:15], v21 offset:2208
	ds_read_b128 v[16:19], v21 offset:2224
	ds_read_b128 v[22:25], v21 offset:2240
	ds_read_b128 v[26:29], v21 offset:2256
	ds_read_b128 v[30:33], v21 offset:2272
	ds_read_b128 v[34:37], v21 offset:2288
	ds_read_b128 v[38:41], v21 offset:2304
	ds_read_b128 v[42:45], v21 offset:2320
	ds_read_b128 v[46:49], v21 offset:2336
	ds_read_b128 v[50:53], v21 offset:2352
	ds_read_b128 v[54:57], v21 offset:2368
	ds_read_b128 v[58:61], v21 offset:2384
	ds_read_b128 v[62:65], v21 offset:2400
	ds_read_b128 v[66:69], v21 offset:2416
	v_fma_f32 v5, -v8, v70, v5
	v_fma_f32 v129, -v8, v71, v129
	v_pk_fma_f32 v[130:131], v[8:9], v[72:73], v[134:135] op_sel_hi:[0,1,1] neg_lo:[1,0,0] neg_hi:[1,0,0]
	v_pk_fma_f32 v[132:133], v[8:9], v[74:75], v[136:137] op_sel_hi:[0,1,1] neg_lo:[1,0,0] neg_hi:[1,0,0]
	v_pk_fma_f32 v[134:135], v[8:9], v[76:77], v[138:139] op_sel_hi:[0,1,1] neg_lo:[1,0,0] neg_hi:[1,0,0]
	v_pk_fma_f32 v[136:137], v[8:9], v[78:79], v[140:141] op_sel_hi:[0,1,1] neg_lo:[1,0,0] neg_hi:[1,0,0]
	v_pk_fma_f32 v[138:139], v[8:9], v[80:81], v[142:143] op_sel_hi:[0,1,1] neg_lo:[1,0,0] neg_hi:[1,0,0]
	v_pk_fma_f32 v[140:141], v[8:9], v[82:83], v[144:145] op_sel_hi:[0,1,1] neg_lo:[1,0,0] neg_hi:[1,0,0]
	v_pk_fma_f32 v[142:143], v[8:9], v[84:85], v[146:147] op_sel_hi:[0,1,1] neg_lo:[1,0,0] neg_hi:[1,0,0]
	v_pk_fma_f32 v[144:145], v[8:9], v[86:87], v[148:149] op_sel_hi:[0,1,1] neg_lo:[1,0,0] neg_hi:[1,0,0]
	v_pk_fma_f32 v[146:147], v[8:9], v[88:89], v[150:151] op_sel_hi:[0,1,1] neg_lo:[1,0,0] neg_hi:[1,0,0]
	v_pk_fma_f32 v[148:149], v[8:9], v[90:91], v[152:153] op_sel_hi:[0,1,1] neg_lo:[1,0,0] neg_hi:[1,0,0]
	v_pk_fma_f32 v[150:151], v[8:9], v[92:93], v[154:155] op_sel_hi:[0,1,1] neg_lo:[1,0,0] neg_hi:[1,0,0]
	v_pk_fma_f32 v[152:153], v[8:9], v[94:95], v[156:157] op_sel_hi:[0,1,1] neg_lo:[1,0,0] neg_hi:[1,0,0]
	v_pk_fma_f32 v[154:155], v[8:9], v[96:97], v[158:159] op_sel_hi:[0,1,1] neg_lo:[1,0,0] neg_hi:[1,0,0]
	v_pk_fma_f32 v[156:157], v[8:9], v[98:99], v[160:161] op_sel_hi:[0,1,1] neg_lo:[1,0,0] neg_hi:[1,0,0]
	v_pk_fma_f32 v[158:159], v[8:9], v[100:101], v[162:163] op_sel_hi:[0,1,1] neg_lo:[1,0,0] neg_hi:[1,0,0]
	v_pk_fma_f32 v[160:161], v[8:9], v[102:103], v[164:165] op_sel_hi:[0,1,1] neg_lo:[1,0,0] neg_hi:[1,0,0]
	v_pk_fma_f32 v[162:163], v[8:9], v[104:105], v[166:167] op_sel_hi:[0,1,1] neg_lo:[1,0,0] neg_hi:[1,0,0]
	v_pk_fma_f32 v[164:165], v[8:9], v[106:107], v[168:169] op_sel_hi:[0,1,1] neg_lo:[1,0,0] neg_hi:[1,0,0]
	v_pk_fma_f32 v[166:167], v[8:9], v[108:109], v[170:171] op_sel_hi:[0,1,1] neg_lo:[1,0,0] neg_hi:[1,0,0]
	v_pk_fma_f32 v[168:169], v[8:9], v[110:111], v[172:173] op_sel_hi:[0,1,1] neg_lo:[1,0,0] neg_hi:[1,0,0]
	v_pk_fma_f32 v[170:171], v[8:9], v[112:113], v[174:175] op_sel_hi:[0,1,1] neg_lo:[1,0,0] neg_hi:[1,0,0]
	v_pk_fma_f32 v[172:173], v[8:9], v[114:115], v[176:177] op_sel_hi:[0,1,1] neg_lo:[1,0,0] neg_hi:[1,0,0]
	v_pk_fma_f32 v[174:175], v[8:9], v[116:117], v[178:179] op_sel_hi:[0,1,1] neg_lo:[1,0,0] neg_hi:[1,0,0]
	v_pk_fma_f32 v[176:177], v[8:9], v[118:119], v[180:181] op_sel_hi:[0,1,1] neg_lo:[1,0,0] neg_hi:[1,0,0]
	v_pk_fma_f32 v[178:179], v[8:9], v[120:121], v[182:183] op_sel_hi:[0,1,1] neg_lo:[1,0,0] neg_hi:[1,0,0]
	v_pk_fma_f32 v[126:127], v[8:9], v[122:123], v[126:127] op_sel_hi:[0,1,1] neg_lo:[1,0,0] neg_hi:[1,0,0]
	v_fma_f32 v128, -v8, v124, v128
	v_fma_f32 v4, -v8, v125, v4
	ds_read_b128 v[70:73], v21 offset:2480
	ds_read_b128 v[74:77], v21 offset:2496
	ds_read_b128 v[78:81], v21 offset:2512
	ds_read_b128 v[82:85], v21 offset:2528
	ds_read_b128 v[86:89], v21 offset:2544
	ds_read_b128 v[90:93], v21 offset:2560
	ds_read_b128 v[94:97], v21 offset:2576
	ds_read_b128 v[98:101], v21 offset:2592
	ds_read_b128 v[102:105], v21 offset:2608
	ds_read_b128 v[106:109], v21 offset:2624
	ds_read_b128 v[110:113], v21 offset:2640
	ds_read_b128 v[114:117], v21 offset:2656
	ds_read_b128 v[118:121], v21 offset:2672
	ds_read_b128 v[122:125], v21 offset:2688
	s_waitcnt lgkmcnt(0)
	v_fma_f32 v12, -v5, v12, v5
	v_fma_f32 v13, -v5, v13, v129
	v_mov_b32_e32 v202, v5
	v_pk_fma_f32 v[14:15], v[202:203], v[14:15], v[130:131] op_sel_hi:[0,1,1] neg_lo:[1,0,0] neg_hi:[1,0,0]
	v_pk_fma_f32 v[130:131], v[202:203], v[16:17], v[132:133] op_sel_hi:[0,1,1] neg_lo:[1,0,0] neg_hi:[1,0,0]
	v_pk_fma_f32 v[132:133], v[202:203], v[18:19], v[134:135] op_sel_hi:[0,1,1] neg_lo:[1,0,0] neg_hi:[1,0,0]
	v_pk_fma_f32 v[134:135], v[202:203], v[22:23], v[136:137] op_sel_hi:[0,1,1] neg_lo:[1,0,0] neg_hi:[1,0,0]
	v_pk_fma_f32 v[136:137], v[202:203], v[24:25], v[138:139] op_sel_hi:[0,1,1] neg_lo:[1,0,0] neg_hi:[1,0,0]
	v_pk_fma_f32 v[138:139], v[202:203], v[26:27], v[140:141] op_sel_hi:[0,1,1] neg_lo:[1,0,0] neg_hi:[1,0,0]
	v_pk_fma_f32 v[140:141], v[202:203], v[28:29], v[142:143] op_sel_hi:[0,1,1] neg_lo:[1,0,0] neg_hi:[1,0,0]
	v_pk_fma_f32 v[142:143], v[202:203], v[30:31], v[144:145] op_sel_hi:[0,1,1] neg_lo:[1,0,0] neg_hi:[1,0,0]
	v_pk_fma_f32 v[144:145], v[202:203], v[32:33], v[146:147] op_sel_hi:[0,1,1] neg_lo:[1,0,0] neg_hi:[1,0,0]
	v_pk_fma_f32 v[146:147], v[202:203], v[34:35], v[148:149] op_sel_hi:[0,1,1] neg_lo:[1,0,0] neg_hi:[1,0,0]
	v_pk_fma_f32 v[148:149], v[202:203], v[36:37], v[150:151] op_sel_hi:[0,1,1] neg_lo:[1,0,0] neg_hi:[1,0,0]
	v_pk_fma_f32 v[150:151], v[202:203], v[38:39], v[152:153] op_sel_hi:[0,1,1] neg_lo:[1,0,0] neg_hi:[1,0,0]
	v_pk_fma_f32 v[152:153], v[202:203], v[40:41], v[154:155] op_sel_hi:[0,1,1] neg_lo:[1,0,0] neg_hi:[1,0,0]
	v_pk_fma_f32 v[154:155], v[202:203], v[42:43], v[156:157] op_sel_hi:[0,1,1] neg_lo:[1,0,0] neg_hi:[1,0,0]
	v_pk_fma_f32 v[156:157], v[202:203], v[44:45], v[158:159] op_sel_hi:[0,1,1] neg_lo:[1,0,0] neg_hi:[1,0,0]
	v_pk_fma_f32 v[158:159], v[202:203], v[46:47], v[160:161] op_sel_hi:[0,1,1] neg_lo:[1,0,0] neg_hi:[1,0,0]
	v_pk_fma_f32 v[160:161], v[202:203], v[48:49], v[162:163] op_sel_hi:[0,1,1] neg_lo:[1,0,0] neg_hi:[1,0,0]
	v_pk_fma_f32 v[162:163], v[202:203], v[50:51], v[164:165] op_sel_hi:[0,1,1] neg_lo:[1,0,0] neg_hi:[1,0,0]
	v_pk_fma_f32 v[164:165], v[202:203], v[52:53], v[166:167] op_sel_hi:[0,1,1] neg_lo:[1,0,0] neg_hi:[1,0,0]
	v_pk_fma_f32 v[166:167], v[202:203], v[54:55], v[168:169] op_sel_hi:[0,1,1] neg_lo:[1,0,0] neg_hi:[1,0,0]
	v_pk_fma_f32 v[168:169], v[202:203], v[56:57], v[170:171] op_sel_hi:[0,1,1] neg_lo:[1,0,0] neg_hi:[1,0,0]
	v_pk_fma_f32 v[170:171], v[202:203], v[58:59], v[172:173] op_sel_hi:[0,1,1] neg_lo:[1,0,0] neg_hi:[1,0,0]
	v_pk_fma_f32 v[172:173], v[202:203], v[60:61], v[174:175] op_sel_hi:[0,1,1] neg_lo:[1,0,0] neg_hi:[1,0,0]
	v_pk_fma_f32 v[174:175], v[202:203], v[62:63], v[176:177] op_sel_hi:[0,1,1] neg_lo:[1,0,0] neg_hi:[1,0,0]
	v_pk_fma_f32 v[176:177], v[202:203], v[64:65], v[178:179] op_sel_hi:[0,1,1] neg_lo:[1,0,0] neg_hi:[1,0,0]
	v_pk_fma_f32 v[178:179], v[202:203], v[66:67], v[126:127] op_sel_hi:[0,1,1] neg_lo:[1,0,0] neg_hi:[1,0,0]
	v_fma_f32 v180, -v5, v68, v128
	v_fma_f32 v4, -v5, v69, v4
	ds_read_b128 v[16:19], v21 offset:2752
	ds_read_b128 v[22:25], v21 offset:2768
	ds_read_b128 v[26:29], v21 offset:2784
	ds_read_b128 v[30:33], v21 offset:2800
	ds_read_b128 v[34:37], v21 offset:2816
	ds_read_b128 v[38:41], v21 offset:2832
	ds_read_b128 v[42:45], v21 offset:2848
	ds_read_b128 v[46:49], v21 offset:2864
	ds_read_b128 v[50:53], v21 offset:2880
	ds_read_b128 v[54:57], v21 offset:2896
	ds_read_b128 v[58:61], v21 offset:2912
	ds_read_b128 v[62:65], v21 offset:2928
	ds_read_b128 v[66:69], v21 offset:2944
	ds_read_b128 v[126:129], v21 offset:2960
	v_fma_f32 v5, -v13, v70, v12
	v_fma_f32 v12, -v13, v71, v13
	v_fma_f32 v181, -v13, v72, v14
	v_fma_f32 v182, -v13, v73, v15
	v_mov_b32_e32 v202, v13
	v_pk_fma_f32 v[130:131], v[202:203], v[74:75], v[130:131] op_sel_hi:[0,1,1] neg_lo:[1,0,0] neg_hi:[1,0,0]
	v_pk_fma_f32 v[132:133], v[202:203], v[76:77], v[132:133] op_sel_hi:[0,1,1] neg_lo:[1,0,0] neg_hi:[1,0,0]
	v_pk_fma_f32 v[134:135], v[202:203], v[78:79], v[134:135] op_sel_hi:[0,1,1] neg_lo:[1,0,0] neg_hi:[1,0,0]
	v_pk_fma_f32 v[136:137], v[202:203], v[80:81], v[136:137] op_sel_hi:[0,1,1] neg_lo:[1,0,0] neg_hi:[1,0,0]
	v_pk_fma_f32 v[138:139], v[202:203], v[82:83], v[138:139] op_sel_hi:[0,1,1] neg_lo:[1,0,0] neg_hi:[1,0,0]
	v_pk_fma_f32 v[140:141], v[202:203], v[84:85], v[140:141] op_sel_hi:[0,1,1] neg_lo:[1,0,0] neg_hi:[1,0,0]
	v_pk_fma_f32 v[142:143], v[202:203], v[86:87], v[142:143] op_sel_hi:[0,1,1] neg_lo:[1,0,0] neg_hi:[1,0,0]
	v_pk_fma_f32 v[144:145], v[202:203], v[88:89], v[144:145] op_sel_hi:[0,1,1] neg_lo:[1,0,0] neg_hi:[1,0,0]
	v_pk_fma_f32 v[146:147], v[202:203], v[90:91], v[146:147] op_sel_hi:[0,1,1] neg_lo:[1,0,0] neg_hi:[1,0,0]
	v_pk_fma_f32 v[148:149], v[202:203], v[92:93], v[148:149] op_sel_hi:[0,1,1] neg_lo:[1,0,0] neg_hi:[1,0,0]
	v_pk_fma_f32 v[150:151], v[202:203], v[94:95], v[150:151] op_sel_hi:[0,1,1] neg_lo:[1,0,0] neg_hi:[1,0,0]
	v_pk_fma_f32 v[152:153], v[202:203], v[96:97], v[152:153] op_sel_hi:[0,1,1] neg_lo:[1,0,0] neg_hi:[1,0,0]
	v_pk_fma_f32 v[154:155], v[202:203], v[98:99], v[154:155] op_sel_hi:[0,1,1] neg_lo:[1,0,0] neg_hi:[1,0,0]
	v_pk_fma_f32 v[156:157], v[202:203], v[100:101], v[156:157] op_sel_hi:[0,1,1] neg_lo:[1,0,0] neg_hi:[1,0,0]
	v_pk_fma_f32 v[158:159], v[202:203], v[102:103], v[158:159] op_sel_hi:[0,1,1] neg_lo:[1,0,0] neg_hi:[1,0,0]
	v_pk_fma_f32 v[160:161], v[202:203], v[104:105], v[160:161] op_sel_hi:[0,1,1] neg_lo:[1,0,0] neg_hi:[1,0,0]
	v_pk_fma_f32 v[162:163], v[202:203], v[106:107], v[162:163] op_sel_hi:[0,1,1] neg_lo:[1,0,0] neg_hi:[1,0,0]
	v_pk_fma_f32 v[164:165], v[202:203], v[108:109], v[164:165] op_sel_hi:[0,1,1] neg_lo:[1,0,0] neg_hi:[1,0,0]
	v_pk_fma_f32 v[166:167], v[202:203], v[110:111], v[166:167] op_sel_hi:[0,1,1] neg_lo:[1,0,0] neg_hi:[1,0,0]
	v_pk_fma_f32 v[168:169], v[202:203], v[112:113], v[168:169] op_sel_hi:[0,1,1] neg_lo:[1,0,0] neg_hi:[1,0,0]
	v_pk_fma_f32 v[170:171], v[202:203], v[114:115], v[170:171] op_sel_hi:[0,1,1] neg_lo:[1,0,0] neg_hi:[1,0,0]
	v_pk_fma_f32 v[172:173], v[202:203], v[116:117], v[172:173] op_sel_hi:[0,1,1] neg_lo:[1,0,0] neg_hi:[1,0,0]
	v_pk_fma_f32 v[174:175], v[202:203], v[118:119], v[174:175] op_sel_hi:[0,1,1] neg_lo:[1,0,0] neg_hi:[1,0,0]
	v_pk_fma_f32 v[176:177], v[202:203], v[120:121], v[176:177] op_sel_hi:[0,1,1] neg_lo:[1,0,0] neg_hi:[1,0,0]
	v_pk_fma_f32 v[122:123], v[202:203], v[122:123], v[178:179] op_sel_hi:[0,1,1] neg_lo:[1,0,0] neg_hi:[1,0,0]
	v_fma_f32 v124, -v13, v124, v180
	v_fma_f32 v4, -v13, v125, v4
	ds_read_b128 v[70:73], v21 offset:3040
	ds_read_b128 v[74:77], v21 offset:3056
	ds_read_b128 v[78:81], v21 offset:3072
	ds_read_b128 v[82:85], v21 offset:3088
	ds_read_b128 v[86:89], v21 offset:3104
	ds_read_b128 v[90:93], v21 offset:3120
	ds_read_b128 v[94:97], v21 offset:3136
	ds_read_b128 v[98:101], v21 offset:3152
	ds_read_b128 v[102:105], v21 offset:3168
	ds_read_b128 v[106:109], v21 offset:3184
	ds_read_b128 v[110:113], v21 offset:3200
	ds_read_b128 v[114:117], v21 offset:3216
	ds_read_b128 v[118:121], v21 offset:3232
	s_waitcnt lgkmcnt(0)
	v_fma_f32 v15, -v181, v16, v5
	v_fma_f32 v14, -v181, v17, v12
	v_fma_f32 v13, -v181, v18, v181
	v_fma_f32 v12, -v181, v19, v182
	v_fma_f32 v5, -v181, v22, v130
	v_fma_f32 v125, -v181, v23, v131
	v_mov_b32_e32 v202, v181
	v_pk_fma_f32 v[130:131], v[202:203], v[24:25], v[132:133] op_sel_hi:[0,1,1] neg_lo:[1,0,0] neg_hi:[1,0,0]
	v_pk_fma_f32 v[132:133], v[202:203], v[26:27], v[134:135] op_sel_hi:[0,1,1] neg_lo:[1,0,0] neg_hi:[1,0,0]
	v_pk_fma_f32 v[134:135], v[202:203], v[28:29], v[136:137] op_sel_hi:[0,1,1] neg_lo:[1,0,0] neg_hi:[1,0,0]
	v_pk_fma_f32 v[136:137], v[202:203], v[30:31], v[138:139] op_sel_hi:[0,1,1] neg_lo:[1,0,0] neg_hi:[1,0,0]
	v_pk_fma_f32 v[138:139], v[202:203], v[32:33], v[140:141] op_sel_hi:[0,1,1] neg_lo:[1,0,0] neg_hi:[1,0,0]
	v_pk_fma_f32 v[140:141], v[202:203], v[34:35], v[142:143] op_sel_hi:[0,1,1] neg_lo:[1,0,0] neg_hi:[1,0,0]
	v_pk_fma_f32 v[142:143], v[202:203], v[36:37], v[144:145] op_sel_hi:[0,1,1] neg_lo:[1,0,0] neg_hi:[1,0,0]
	v_pk_fma_f32 v[144:145], v[202:203], v[38:39], v[146:147] op_sel_hi:[0,1,1] neg_lo:[1,0,0] neg_hi:[1,0,0]
	v_pk_fma_f32 v[146:147], v[202:203], v[40:41], v[148:149] op_sel_hi:[0,1,1] neg_lo:[1,0,0] neg_hi:[1,0,0]
	v_pk_fma_f32 v[148:149], v[202:203], v[42:43], v[150:151] op_sel_hi:[0,1,1] neg_lo:[1,0,0] neg_hi:[1,0,0]
	v_pk_fma_f32 v[150:151], v[202:203], v[44:45], v[152:153] op_sel_hi:[0,1,1] neg_lo:[1,0,0] neg_hi:[1,0,0]
	v_pk_fma_f32 v[152:153], v[202:203], v[46:47], v[154:155] op_sel_hi:[0,1,1] neg_lo:[1,0,0] neg_hi:[1,0,0]
	v_pk_fma_f32 v[154:155], v[202:203], v[48:49], v[156:157] op_sel_hi:[0,1,1] neg_lo:[1,0,0] neg_hi:[1,0,0]
	v_pk_fma_f32 v[156:157], v[202:203], v[50:51], v[158:159] op_sel_hi:[0,1,1] neg_lo:[1,0,0] neg_hi:[1,0,0]
	v_pk_fma_f32 v[158:159], v[202:203], v[52:53], v[160:161] op_sel_hi:[0,1,1] neg_lo:[1,0,0] neg_hi:[1,0,0]
	v_pk_fma_f32 v[160:161], v[202:203], v[54:55], v[162:163] op_sel_hi:[0,1,1] neg_lo:[1,0,0] neg_hi:[1,0,0]
	v_pk_fma_f32 v[162:163], v[202:203], v[56:57], v[164:165] op_sel_hi:[0,1,1] neg_lo:[1,0,0] neg_hi:[1,0,0]
	v_pk_fma_f32 v[164:165], v[202:203], v[58:59], v[166:167] op_sel_hi:[0,1,1] neg_lo:[1,0,0] neg_hi:[1,0,0]
	v_pk_fma_f32 v[166:167], v[202:203], v[60:61], v[168:169] op_sel_hi:[0,1,1] neg_lo:[1,0,0] neg_hi:[1,0,0]
	v_pk_fma_f32 v[168:169], v[202:203], v[62:63], v[170:171] op_sel_hi:[0,1,1] neg_lo:[1,0,0] neg_hi:[1,0,0]
	v_pk_fma_f32 v[170:171], v[202:203], v[64:65], v[172:173] op_sel_hi:[0,1,1] neg_lo:[1,0,0] neg_hi:[1,0,0]
	v_pk_fma_f32 v[172:173], v[202:203], v[66:67], v[174:175] op_sel_hi:[0,1,1] neg_lo:[1,0,0] neg_hi:[1,0,0]
	v_pk_fma_f32 v[174:175], v[202:203], v[68:69], v[176:177] op_sel_hi:[0,1,1] neg_lo:[1,0,0] neg_hi:[1,0,0]
	v_pk_fma_f32 v[122:123], v[202:203], v[126:127], v[122:123] op_sel_hi:[0,1,1] neg_lo:[1,0,0] neg_hi:[1,0,0]
	v_fma_f32 v124, -v181, v128, v124
	v_fma_f32 v4, -v181, v129, v4
	ds_read_b128 v[16:19], v21 offset:3312
	ds_read_b128 v[22:25], v21 offset:3328
	ds_read_b128 v[26:29], v21 offset:3344
	ds_read_b128 v[30:33], v21 offset:3360
	ds_read_b128 v[34:37], v21 offset:3376
	ds_read_b128 v[38:41], v21 offset:3392
	ds_read_b128 v[42:45], v21 offset:3408
	ds_read_b128 v[46:49], v21 offset:3424
	ds_read_b128 v[50:53], v21 offset:3440
	ds_read_b128 v[54:57], v21 offset:3456
	ds_read_b128 v[58:61], v21 offset:3472
	ds_read_b128 v[62:65], v21 offset:3488
	ds_read_b128 v[66:69], v21 offset:3504
	v_fma_f32 v5, -v12, v70, v5
	v_fma_f32 v125, -v12, v71, v125
	v_pk_fma_f32 v[126:127], v[12:13], v[72:73], v[130:131] op_sel_hi:[0,1,1] neg_lo:[1,0,0] neg_hi:[1,0,0]
	v_pk_fma_f32 v[128:129], v[12:13], v[74:75], v[132:133] op_sel_hi:[0,1,1] neg_lo:[1,0,0] neg_hi:[1,0,0]
	v_pk_fma_f32 v[130:131], v[12:13], v[76:77], v[134:135] op_sel_hi:[0,1,1] neg_lo:[1,0,0] neg_hi:[1,0,0]
	v_pk_fma_f32 v[132:133], v[12:13], v[78:79], v[136:137] op_sel_hi:[0,1,1] neg_lo:[1,0,0] neg_hi:[1,0,0]
	v_pk_fma_f32 v[134:135], v[12:13], v[80:81], v[138:139] op_sel_hi:[0,1,1] neg_lo:[1,0,0] neg_hi:[1,0,0]
	v_pk_fma_f32 v[136:137], v[12:13], v[82:83], v[140:141] op_sel_hi:[0,1,1] neg_lo:[1,0,0] neg_hi:[1,0,0]
	v_pk_fma_f32 v[138:139], v[12:13], v[84:85], v[142:143] op_sel_hi:[0,1,1] neg_lo:[1,0,0] neg_hi:[1,0,0]
	v_pk_fma_f32 v[140:141], v[12:13], v[86:87], v[144:145] op_sel_hi:[0,1,1] neg_lo:[1,0,0] neg_hi:[1,0,0]
	v_pk_fma_f32 v[142:143], v[12:13], v[88:89], v[146:147] op_sel_hi:[0,1,1] neg_lo:[1,0,0] neg_hi:[1,0,0]
	v_pk_fma_f32 v[144:145], v[12:13], v[90:91], v[148:149] op_sel_hi:[0,1,1] neg_lo:[1,0,0] neg_hi:[1,0,0]
	v_pk_fma_f32 v[146:147], v[12:13], v[92:93], v[150:151] op_sel_hi:[0,1,1] neg_lo:[1,0,0] neg_hi:[1,0,0]
	v_pk_fma_f32 v[148:149], v[12:13], v[94:95], v[152:153] op_sel_hi:[0,1,1] neg_lo:[1,0,0] neg_hi:[1,0,0]
	v_pk_fma_f32 v[150:151], v[12:13], v[96:97], v[154:155] op_sel_hi:[0,1,1] neg_lo:[1,0,0] neg_hi:[1,0,0]
	v_pk_fma_f32 v[152:153], v[12:13], v[98:99], v[156:157] op_sel_hi:[0,1,1] neg_lo:[1,0,0] neg_hi:[1,0,0]
	v_pk_fma_f32 v[154:155], v[12:13], v[100:101], v[158:159] op_sel_hi:[0,1,1] neg_lo:[1,0,0] neg_hi:[1,0,0]
	v_pk_fma_f32 v[156:157], v[12:13], v[102:103], v[160:161] op_sel_hi:[0,1,1] neg_lo:[1,0,0] neg_hi:[1,0,0]
	v_pk_fma_f32 v[158:159], v[12:13], v[104:105], v[162:163] op_sel_hi:[0,1,1] neg_lo:[1,0,0] neg_hi:[1,0,0]
	v_pk_fma_f32 v[160:161], v[12:13], v[106:107], v[164:165] op_sel_hi:[0,1,1] neg_lo:[1,0,0] neg_hi:[1,0,0]
	v_pk_fma_f32 v[162:163], v[12:13], v[108:109], v[166:167] op_sel_hi:[0,1,1] neg_lo:[1,0,0] neg_hi:[1,0,0]
	v_pk_fma_f32 v[164:165], v[12:13], v[110:111], v[168:169] op_sel_hi:[0,1,1] neg_lo:[1,0,0] neg_hi:[1,0,0]
	v_pk_fma_f32 v[166:167], v[12:13], v[112:113], v[170:171] op_sel_hi:[0,1,1] neg_lo:[1,0,0] neg_hi:[1,0,0]
	v_pk_fma_f32 v[168:169], v[12:13], v[114:115], v[172:173] op_sel_hi:[0,1,1] neg_lo:[1,0,0] neg_hi:[1,0,0]
	v_pk_fma_f32 v[170:171], v[12:13], v[116:117], v[174:175] op_sel_hi:[0,1,1] neg_lo:[1,0,0] neg_hi:[1,0,0]
	v_pk_fma_f32 v[122:123], v[12:13], v[118:119], v[122:123] op_sel_hi:[0,1,1] neg_lo:[1,0,0] neg_hi:[1,0,0]
	v_fma_f32 v124, -v12, v120, v124
	v_fma_f32 v4, -v12, v121, v4
	ds_read_b128 v[70:73], v21 offset:3584
	ds_read_b128 v[74:77], v21 offset:3600
	ds_read_b128 v[78:81], v21 offset:3616
	ds_read_b128 v[82:85], v21 offset:3632
	ds_read_b128 v[86:89], v21 offset:3648
	ds_read_b128 v[90:93], v21 offset:3664
	ds_read_b128 v[94:97], v21 offset:3680
	ds_read_b128 v[98:101], v21 offset:3696
	ds_read_b128 v[102:105], v21 offset:3712
	ds_read_b128 v[106:109], v21 offset:3728
	ds_read_b128 v[110:113], v21 offset:3744
	ds_read_b128 v[114:117], v21 offset:3760
	ds_read_b128 v[118:121], v21 offset:3776
	s_waitcnt lgkmcnt(0)
	v_fma_f32 v16, -v5, v16, v5
	v_fma_f32 v17, -v5, v17, v125
	v_mov_b32_e32 v202, v5
	v_pk_fma_f32 v[18:19], v[202:203], v[18:19], v[126:127] op_sel_hi:[0,1,1] neg_lo:[1,0,0] neg_hi:[1,0,0]
	v_pk_fma_f32 v[126:127], v[202:203], v[22:23], v[128:129] op_sel_hi:[0,1,1] neg_lo:[1,0,0] neg_hi:[1,0,0]
	v_pk_fma_f32 v[128:129], v[202:203], v[24:25], v[130:131] op_sel_hi:[0,1,1] neg_lo:[1,0,0] neg_hi:[1,0,0]
	v_pk_fma_f32 v[130:131], v[202:203], v[26:27], v[132:133] op_sel_hi:[0,1,1] neg_lo:[1,0,0] neg_hi:[1,0,0]
	v_pk_fma_f32 v[132:133], v[202:203], v[28:29], v[134:135] op_sel_hi:[0,1,1] neg_lo:[1,0,0] neg_hi:[1,0,0]
	v_pk_fma_f32 v[134:135], v[202:203], v[30:31], v[136:137] op_sel_hi:[0,1,1] neg_lo:[1,0,0] neg_hi:[1,0,0]
	v_pk_fma_f32 v[136:137], v[202:203], v[32:33], v[138:139] op_sel_hi:[0,1,1] neg_lo:[1,0,0] neg_hi:[1,0,0]
	v_pk_fma_f32 v[138:139], v[202:203], v[34:35], v[140:141] op_sel_hi:[0,1,1] neg_lo:[1,0,0] neg_hi:[1,0,0]
	v_pk_fma_f32 v[140:141], v[202:203], v[36:37], v[142:143] op_sel_hi:[0,1,1] neg_lo:[1,0,0] neg_hi:[1,0,0]
	v_pk_fma_f32 v[142:143], v[202:203], v[38:39], v[144:145] op_sel_hi:[0,1,1] neg_lo:[1,0,0] neg_hi:[1,0,0]
	v_pk_fma_f32 v[144:145], v[202:203], v[40:41], v[146:147] op_sel_hi:[0,1,1] neg_lo:[1,0,0] neg_hi:[1,0,0]
	v_pk_fma_f32 v[146:147], v[202:203], v[42:43], v[148:149] op_sel_hi:[0,1,1] neg_lo:[1,0,0] neg_hi:[1,0,0]
	v_pk_fma_f32 v[148:149], v[202:203], v[44:45], v[150:151] op_sel_hi:[0,1,1] neg_lo:[1,0,0] neg_hi:[1,0,0]
	v_pk_fma_f32 v[150:151], v[202:203], v[46:47], v[152:153] op_sel_hi:[0,1,1] neg_lo:[1,0,0] neg_hi:[1,0,0]
	v_pk_fma_f32 v[152:153], v[202:203], v[48:49], v[154:155] op_sel_hi:[0,1,1] neg_lo:[1,0,0] neg_hi:[1,0,0]
	v_pk_fma_f32 v[154:155], v[202:203], v[50:51], v[156:157] op_sel_hi:[0,1,1] neg_lo:[1,0,0] neg_hi:[1,0,0]
	v_pk_fma_f32 v[156:157], v[202:203], v[52:53], v[158:159] op_sel_hi:[0,1,1] neg_lo:[1,0,0] neg_hi:[1,0,0]
	v_pk_fma_f32 v[158:159], v[202:203], v[54:55], v[160:161] op_sel_hi:[0,1,1] neg_lo:[1,0,0] neg_hi:[1,0,0]
	v_pk_fma_f32 v[160:161], v[202:203], v[56:57], v[162:163] op_sel_hi:[0,1,1] neg_lo:[1,0,0] neg_hi:[1,0,0]
	v_pk_fma_f32 v[162:163], v[202:203], v[58:59], v[164:165] op_sel_hi:[0,1,1] neg_lo:[1,0,0] neg_hi:[1,0,0]
	v_pk_fma_f32 v[164:165], v[202:203], v[60:61], v[166:167] op_sel_hi:[0,1,1] neg_lo:[1,0,0] neg_hi:[1,0,0]
	v_pk_fma_f32 v[166:167], v[202:203], v[62:63], v[168:169] op_sel_hi:[0,1,1] neg_lo:[1,0,0] neg_hi:[1,0,0]
	v_pk_fma_f32 v[168:169], v[202:203], v[64:65], v[170:171] op_sel_hi:[0,1,1] neg_lo:[1,0,0] neg_hi:[1,0,0]
	v_pk_fma_f32 v[170:171], v[202:203], v[66:67], v[122:123] op_sel_hi:[0,1,1] neg_lo:[1,0,0] neg_hi:[1,0,0]
	v_fma_f32 v172, -v5, v68, v124
	v_fma_f32 v4, -v5, v69, v4
	ds_read_b128 v[22:25], v21 offset:3856
	ds_read_b128 v[26:29], v21 offset:3872
	ds_read_b128 v[30:33], v21 offset:3888
	ds_read_b128 v[34:37], v21 offset:3904
	ds_read_b128 v[38:41], v21 offset:3920
	ds_read_b128 v[42:45], v21 offset:3936
	ds_read_b128 v[46:49], v21 offset:3952
	ds_read_b128 v[50:53], v21 offset:3968
	ds_read_b128 v[54:57], v21 offset:3984
	ds_read_b128 v[58:61], v21 offset:4000
	ds_read_b128 v[62:65], v21 offset:4016
	ds_read_b128 v[66:69], v21 offset:4032
	ds_read_b128 v[122:125], v21 offset:4048
	v_fma_f32 v5, -v17, v70, v16
	v_fma_f32 v16, -v17, v71, v17
	v_fma_f32 v173, -v17, v72, v18
	v_fma_f32 v174, -v17, v73, v19
	v_mov_b32_e32 v202, v17
	v_pk_fma_f32 v[126:127], v[202:203], v[74:75], v[126:127] op_sel_hi:[0,1,1] neg_lo:[1,0,0] neg_hi:[1,0,0]
	v_pk_fma_f32 v[128:129], v[202:203], v[76:77], v[128:129] op_sel_hi:[0,1,1] neg_lo:[1,0,0] neg_hi:[1,0,0]
	v_pk_fma_f32 v[130:131], v[202:203], v[78:79], v[130:131] op_sel_hi:[0,1,1] neg_lo:[1,0,0] neg_hi:[1,0,0]
	v_pk_fma_f32 v[132:133], v[202:203], v[80:81], v[132:133] op_sel_hi:[0,1,1] neg_lo:[1,0,0] neg_hi:[1,0,0]
	v_pk_fma_f32 v[134:135], v[202:203], v[82:83], v[134:135] op_sel_hi:[0,1,1] neg_lo:[1,0,0] neg_hi:[1,0,0]
	v_pk_fma_f32 v[136:137], v[202:203], v[84:85], v[136:137] op_sel_hi:[0,1,1] neg_lo:[1,0,0] neg_hi:[1,0,0]
	v_pk_fma_f32 v[138:139], v[202:203], v[86:87], v[138:139] op_sel_hi:[0,1,1] neg_lo:[1,0,0] neg_hi:[1,0,0]
	v_pk_fma_f32 v[140:141], v[202:203], v[88:89], v[140:141] op_sel_hi:[0,1,1] neg_lo:[1,0,0] neg_hi:[1,0,0]
	v_pk_fma_f32 v[142:143], v[202:203], v[90:91], v[142:143] op_sel_hi:[0,1,1] neg_lo:[1,0,0] neg_hi:[1,0,0]
	v_pk_fma_f32 v[144:145], v[202:203], v[92:93], v[144:145] op_sel_hi:[0,1,1] neg_lo:[1,0,0] neg_hi:[1,0,0]
	v_pk_fma_f32 v[146:147], v[202:203], v[94:95], v[146:147] op_sel_hi:[0,1,1] neg_lo:[1,0,0] neg_hi:[1,0,0]
	v_pk_fma_f32 v[148:149], v[202:203], v[96:97], v[148:149] op_sel_hi:[0,1,1] neg_lo:[1,0,0] neg_hi:[1,0,0]
	v_pk_fma_f32 v[150:151], v[202:203], v[98:99], v[150:151] op_sel_hi:[0,1,1] neg_lo:[1,0,0] neg_hi:[1,0,0]
	v_pk_fma_f32 v[152:153], v[202:203], v[100:101], v[152:153] op_sel_hi:[0,1,1] neg_lo:[1,0,0] neg_hi:[1,0,0]
	v_pk_fma_f32 v[154:155], v[202:203], v[102:103], v[154:155] op_sel_hi:[0,1,1] neg_lo:[1,0,0] neg_hi:[1,0,0]
	v_pk_fma_f32 v[156:157], v[202:203], v[104:105], v[156:157] op_sel_hi:[0,1,1] neg_lo:[1,0,0] neg_hi:[1,0,0]
	v_pk_fma_f32 v[158:159], v[202:203], v[106:107], v[158:159] op_sel_hi:[0,1,1] neg_lo:[1,0,0] neg_hi:[1,0,0]
	v_pk_fma_f32 v[160:161], v[202:203], v[108:109], v[160:161] op_sel_hi:[0,1,1] neg_lo:[1,0,0] neg_hi:[1,0,0]
	v_pk_fma_f32 v[162:163], v[202:203], v[110:111], v[162:163] op_sel_hi:[0,1,1] neg_lo:[1,0,0] neg_hi:[1,0,0]
	v_pk_fma_f32 v[164:165], v[202:203], v[112:113], v[164:165] op_sel_hi:[0,1,1] neg_lo:[1,0,0] neg_hi:[1,0,0]
	v_pk_fma_f32 v[166:167], v[202:203], v[114:115], v[166:167] op_sel_hi:[0,1,1] neg_lo:[1,0,0] neg_hi:[1,0,0]
	v_pk_fma_f32 v[168:169], v[202:203], v[116:117], v[168:169] op_sel_hi:[0,1,1] neg_lo:[1,0,0] neg_hi:[1,0,0]
	v_pk_fma_f32 v[118:119], v[202:203], v[118:119], v[170:171] op_sel_hi:[0,1,1] neg_lo:[1,0,0] neg_hi:[1,0,0]
	v_fma_f32 v120, -v17, v120, v172
	v_fma_f32 v4, -v17, v121, v4
	ds_read_b128 v[70:73], v21 offset:4144
	ds_read_b128 v[74:77], v21 offset:4160
	ds_read_b128 v[78:81], v21 offset:4176
	ds_read_b128 v[82:85], v21 offset:4192
	ds_read_b128 v[86:89], v21 offset:4208
	ds_read_b128 v[90:93], v21 offset:4224
	ds_read_b128 v[94:97], v21 offset:4240
	ds_read_b128 v[98:101], v21 offset:4256
	ds_read_b128 v[102:105], v21 offset:4272
	ds_read_b128 v[106:109], v21 offset:4288
	ds_read_b128 v[110:113], v21 offset:4304
	ds_read_b128 v[114:117], v21 offset:4320
	s_waitcnt lgkmcnt(0)
	v_fma_f32 v19, -v173, v22, v5
	v_fma_f32 v18, -v173, v23, v16
	v_fma_f32 v17, -v173, v24, v173
	v_fma_f32 v16, -v173, v25, v174
	v_fma_f32 v5, -v173, v26, v126
	v_fma_f32 v121, -v173, v27, v127
	v_mov_b32_e32 v202, v173
	v_pk_fma_f32 v[126:127], v[202:203], v[28:29], v[128:129] op_sel_hi:[0,1,1] neg_lo:[1,0,0] neg_hi:[1,0,0]
	v_pk_fma_f32 v[128:129], v[202:203], v[30:31], v[130:131] op_sel_hi:[0,1,1] neg_lo:[1,0,0] neg_hi:[1,0,0]
	v_pk_fma_f32 v[130:131], v[202:203], v[32:33], v[132:133] op_sel_hi:[0,1,1] neg_lo:[1,0,0] neg_hi:[1,0,0]
	v_pk_fma_f32 v[132:133], v[202:203], v[34:35], v[134:135] op_sel_hi:[0,1,1] neg_lo:[1,0,0] neg_hi:[1,0,0]
	v_pk_fma_f32 v[134:135], v[202:203], v[36:37], v[136:137] op_sel_hi:[0,1,1] neg_lo:[1,0,0] neg_hi:[1,0,0]
	v_pk_fma_f32 v[136:137], v[202:203], v[38:39], v[138:139] op_sel_hi:[0,1,1] neg_lo:[1,0,0] neg_hi:[1,0,0]
	v_pk_fma_f32 v[138:139], v[202:203], v[40:41], v[140:141] op_sel_hi:[0,1,1] neg_lo:[1,0,0] neg_hi:[1,0,0]
	v_pk_fma_f32 v[140:141], v[202:203], v[42:43], v[142:143] op_sel_hi:[0,1,1] neg_lo:[1,0,0] neg_hi:[1,0,0]
	v_pk_fma_f32 v[142:143], v[202:203], v[44:45], v[144:145] op_sel_hi:[0,1,1] neg_lo:[1,0,0] neg_hi:[1,0,0]
	v_pk_fma_f32 v[144:145], v[202:203], v[46:47], v[146:147] op_sel_hi:[0,1,1] neg_lo:[1,0,0] neg_hi:[1,0,0]
	v_pk_fma_f32 v[146:147], v[202:203], v[48:49], v[148:149] op_sel_hi:[0,1,1] neg_lo:[1,0,0] neg_hi:[1,0,0]
	v_pk_fma_f32 v[148:149], v[202:203], v[50:51], v[150:151] op_sel_hi:[0,1,1] neg_lo:[1,0,0] neg_hi:[1,0,0]
	v_pk_fma_f32 v[150:151], v[202:203], v[52:53], v[152:153] op_sel_hi:[0,1,1] neg_lo:[1,0,0] neg_hi:[1,0,0]
	v_pk_fma_f32 v[152:153], v[202:203], v[54:55], v[154:155] op_sel_hi:[0,1,1] neg_lo:[1,0,0] neg_hi:[1,0,0]
	v_pk_fma_f32 v[154:155], v[202:203], v[56:57], v[156:157] op_sel_hi:[0,1,1] neg_lo:[1,0,0] neg_hi:[1,0,0]
	v_pk_fma_f32 v[156:157], v[202:203], v[58:59], v[158:159] op_sel_hi:[0,1,1] neg_lo:[1,0,0] neg_hi:[1,0,0]
	v_pk_fma_f32 v[158:159], v[202:203], v[60:61], v[160:161] op_sel_hi:[0,1,1] neg_lo:[1,0,0] neg_hi:[1,0,0]
	v_pk_fma_f32 v[160:161], v[202:203], v[62:63], v[162:163] op_sel_hi:[0,1,1] neg_lo:[1,0,0] neg_hi:[1,0,0]
	v_pk_fma_f32 v[162:163], v[202:203], v[64:65], v[164:165] op_sel_hi:[0,1,1] neg_lo:[1,0,0] neg_hi:[1,0,0]
	v_pk_fma_f32 v[164:165], v[202:203], v[66:67], v[166:167] op_sel_hi:[0,1,1] neg_lo:[1,0,0] neg_hi:[1,0,0]
	v_pk_fma_f32 v[166:167], v[202:203], v[68:69], v[168:169] op_sel_hi:[0,1,1] neg_lo:[1,0,0] neg_hi:[1,0,0]
	v_pk_fma_f32 v[118:119], v[202:203], v[122:123], v[118:119] op_sel_hi:[0,1,1] neg_lo:[1,0,0] neg_hi:[1,0,0]
	v_fma_f32 v120, -v173, v124, v120
	v_fma_f32 v4, -v173, v125, v4
	ds_read_b128 v[22:25], v21 offset:4416
	ds_read_b128 v[26:29], v21 offset:4432
	ds_read_b128 v[30:33], v21 offset:4448
	ds_read_b128 v[34:37], v21 offset:4464
	ds_read_b128 v[38:41], v21 offset:4480
	ds_read_b128 v[42:45], v21 offset:4496
	ds_read_b128 v[46:49], v21 offset:4512
	ds_read_b128 v[50:53], v21 offset:4528
	ds_read_b128 v[54:57], v21 offset:4544
	ds_read_b128 v[58:61], v21 offset:4560
	ds_read_b128 v[62:65], v21 offset:4576
	ds_read_b128 v[66:69], v21 offset:4592
	v_fma_f32 v5, -v16, v70, v5
	v_fma_f32 v121, -v16, v71, v121
	v_pk_fma_f32 v[122:123], v[16:17], v[72:73], v[126:127] op_sel_hi:[0,1,1] neg_lo:[1,0,0] neg_hi:[1,0,0]
	v_pk_fma_f32 v[124:125], v[16:17], v[74:75], v[128:129] op_sel_hi:[0,1,1] neg_lo:[1,0,0] neg_hi:[1,0,0]
	v_pk_fma_f32 v[126:127], v[16:17], v[76:77], v[130:131] op_sel_hi:[0,1,1] neg_lo:[1,0,0] neg_hi:[1,0,0]
	v_pk_fma_f32 v[128:129], v[16:17], v[78:79], v[132:133] op_sel_hi:[0,1,1] neg_lo:[1,0,0] neg_hi:[1,0,0]
	v_pk_fma_f32 v[130:131], v[16:17], v[80:81], v[134:135] op_sel_hi:[0,1,1] neg_lo:[1,0,0] neg_hi:[1,0,0]
	v_pk_fma_f32 v[132:133], v[16:17], v[82:83], v[136:137] op_sel_hi:[0,1,1] neg_lo:[1,0,0] neg_hi:[1,0,0]
	v_pk_fma_f32 v[134:135], v[16:17], v[84:85], v[138:139] op_sel_hi:[0,1,1] neg_lo:[1,0,0] neg_hi:[1,0,0]
	v_pk_fma_f32 v[136:137], v[16:17], v[86:87], v[140:141] op_sel_hi:[0,1,1] neg_lo:[1,0,0] neg_hi:[1,0,0]
	v_pk_fma_f32 v[138:139], v[16:17], v[88:89], v[142:143] op_sel_hi:[0,1,1] neg_lo:[1,0,0] neg_hi:[1,0,0]
	v_pk_fma_f32 v[140:141], v[16:17], v[90:91], v[144:145] op_sel_hi:[0,1,1] neg_lo:[1,0,0] neg_hi:[1,0,0]
	v_pk_fma_f32 v[142:143], v[16:17], v[92:93], v[146:147] op_sel_hi:[0,1,1] neg_lo:[1,0,0] neg_hi:[1,0,0]
	v_pk_fma_f32 v[144:145], v[16:17], v[94:95], v[148:149] op_sel_hi:[0,1,1] neg_lo:[1,0,0] neg_hi:[1,0,0]
	v_pk_fma_f32 v[146:147], v[16:17], v[96:97], v[150:151] op_sel_hi:[0,1,1] neg_lo:[1,0,0] neg_hi:[1,0,0]
	v_pk_fma_f32 v[148:149], v[16:17], v[98:99], v[152:153] op_sel_hi:[0,1,1] neg_lo:[1,0,0] neg_hi:[1,0,0]
	v_pk_fma_f32 v[150:151], v[16:17], v[100:101], v[154:155] op_sel_hi:[0,1,1] neg_lo:[1,0,0] neg_hi:[1,0,0]
	v_pk_fma_f32 v[152:153], v[16:17], v[102:103], v[156:157] op_sel_hi:[0,1,1] neg_lo:[1,0,0] neg_hi:[1,0,0]
	v_pk_fma_f32 v[154:155], v[16:17], v[104:105], v[158:159] op_sel_hi:[0,1,1] neg_lo:[1,0,0] neg_hi:[1,0,0]
	v_pk_fma_f32 v[156:157], v[16:17], v[106:107], v[160:161] op_sel_hi:[0,1,1] neg_lo:[1,0,0] neg_hi:[1,0,0]
	v_pk_fma_f32 v[158:159], v[16:17], v[108:109], v[162:163] op_sel_hi:[0,1,1] neg_lo:[1,0,0] neg_hi:[1,0,0]
	v_pk_fma_f32 v[160:161], v[16:17], v[110:111], v[164:165] op_sel_hi:[0,1,1] neg_lo:[1,0,0] neg_hi:[1,0,0]
	v_pk_fma_f32 v[162:163], v[16:17], v[112:113], v[166:167] op_sel_hi:[0,1,1] neg_lo:[1,0,0] neg_hi:[1,0,0]
	v_pk_fma_f32 v[118:119], v[16:17], v[114:115], v[118:119] op_sel_hi:[0,1,1] neg_lo:[1,0,0] neg_hi:[1,0,0]
	v_fma_f32 v120, -v16, v116, v120
	v_fma_f32 v4, -v16, v117, v4
	ds_read_b128 v[70:73], v21 offset:4688
	ds_read_b128 v[74:77], v21 offset:4704
	ds_read_b128 v[78:81], v21 offset:4720
	ds_read_b128 v[82:85], v21 offset:4736
	ds_read_b128 v[86:89], v21 offset:4752
	ds_read_b128 v[90:93], v21 offset:4768
	ds_read_b128 v[94:97], v21 offset:4784
	ds_read_b128 v[98:101], v21 offset:4800
	ds_read_b128 v[102:105], v21 offset:4816
	ds_read_b128 v[106:109], v21 offset:4832
	ds_read_b128 v[110:113], v21 offset:4848
	ds_read_b128 v[114:117], v21 offset:4864
	s_waitcnt lgkmcnt(0)
	v_fma_f32 v22, -v5, v22, v5
	v_fma_f32 v23, -v5, v23, v121
	v_mov_b32_e32 v202, v5
	v_pk_fma_f32 v[24:25], v[202:203], v[24:25], v[122:123] op_sel_hi:[0,1,1] neg_lo:[1,0,0] neg_hi:[1,0,0]
	v_pk_fma_f32 v[122:123], v[202:203], v[26:27], v[124:125] op_sel_hi:[0,1,1] neg_lo:[1,0,0] neg_hi:[1,0,0]
	v_pk_fma_f32 v[124:125], v[202:203], v[28:29], v[126:127] op_sel_hi:[0,1,1] neg_lo:[1,0,0] neg_hi:[1,0,0]
	v_pk_fma_f32 v[126:127], v[202:203], v[30:31], v[128:129] op_sel_hi:[0,1,1] neg_lo:[1,0,0] neg_hi:[1,0,0]
	v_pk_fma_f32 v[128:129], v[202:203], v[32:33], v[130:131] op_sel_hi:[0,1,1] neg_lo:[1,0,0] neg_hi:[1,0,0]
	v_pk_fma_f32 v[130:131], v[202:203], v[34:35], v[132:133] op_sel_hi:[0,1,1] neg_lo:[1,0,0] neg_hi:[1,0,0]
	v_pk_fma_f32 v[132:133], v[202:203], v[36:37], v[134:135] op_sel_hi:[0,1,1] neg_lo:[1,0,0] neg_hi:[1,0,0]
	v_pk_fma_f32 v[134:135], v[202:203], v[38:39], v[136:137] op_sel_hi:[0,1,1] neg_lo:[1,0,0] neg_hi:[1,0,0]
	v_pk_fma_f32 v[136:137], v[202:203], v[40:41], v[138:139] op_sel_hi:[0,1,1] neg_lo:[1,0,0] neg_hi:[1,0,0]
	v_pk_fma_f32 v[138:139], v[202:203], v[42:43], v[140:141] op_sel_hi:[0,1,1] neg_lo:[1,0,0] neg_hi:[1,0,0]
	v_pk_fma_f32 v[140:141], v[202:203], v[44:45], v[142:143] op_sel_hi:[0,1,1] neg_lo:[1,0,0] neg_hi:[1,0,0]
	v_pk_fma_f32 v[142:143], v[202:203], v[46:47], v[144:145] op_sel_hi:[0,1,1] neg_lo:[1,0,0] neg_hi:[1,0,0]
	v_pk_fma_f32 v[144:145], v[202:203], v[48:49], v[146:147] op_sel_hi:[0,1,1] neg_lo:[1,0,0] neg_hi:[1,0,0]
	v_pk_fma_f32 v[146:147], v[202:203], v[50:51], v[148:149] op_sel_hi:[0,1,1] neg_lo:[1,0,0] neg_hi:[1,0,0]
	v_pk_fma_f32 v[148:149], v[202:203], v[52:53], v[150:151] op_sel_hi:[0,1,1] neg_lo:[1,0,0] neg_hi:[1,0,0]
	v_pk_fma_f32 v[150:151], v[202:203], v[54:55], v[152:153] op_sel_hi:[0,1,1] neg_lo:[1,0,0] neg_hi:[1,0,0]
	v_pk_fma_f32 v[152:153], v[202:203], v[56:57], v[154:155] op_sel_hi:[0,1,1] neg_lo:[1,0,0] neg_hi:[1,0,0]
	v_pk_fma_f32 v[154:155], v[202:203], v[58:59], v[156:157] op_sel_hi:[0,1,1] neg_lo:[1,0,0] neg_hi:[1,0,0]
	v_pk_fma_f32 v[156:157], v[202:203], v[60:61], v[158:159] op_sel_hi:[0,1,1] neg_lo:[1,0,0] neg_hi:[1,0,0]
	v_pk_fma_f32 v[158:159], v[202:203], v[62:63], v[160:161] op_sel_hi:[0,1,1] neg_lo:[1,0,0] neg_hi:[1,0,0]
	v_pk_fma_f32 v[160:161], v[202:203], v[64:65], v[162:163] op_sel_hi:[0,1,1] neg_lo:[1,0,0] neg_hi:[1,0,0]
	v_pk_fma_f32 v[162:163], v[202:203], v[66:67], v[118:119] op_sel_hi:[0,1,1] neg_lo:[1,0,0] neg_hi:[1,0,0]
	v_fma_f32 v164, -v5, v68, v120
	v_fma_f32 v4, -v5, v69, v4
	ds_read_b128 v[26:29], v21 offset:4960
	ds_read_b128 v[30:33], v21 offset:4976
	ds_read_b128 v[34:37], v21 offset:4992
	ds_read_b128 v[38:41], v21 offset:5008
	ds_read_b128 v[42:45], v21 offset:5024
	ds_read_b128 v[46:49], v21 offset:5040
	ds_read_b128 v[50:53], v21 offset:5056
	ds_read_b128 v[54:57], v21 offset:5072
	ds_read_b128 v[58:61], v21 offset:5088
	ds_read_b128 v[62:65], v21 offset:5104
	ds_read_b128 v[66:69], v21 offset:5120
	ds_read_b128 v[118:121], v21 offset:5136
	v_fma_f32 v5, -v23, v70, v22
	v_fma_f32 v22, -v23, v71, v23
	v_fma_f32 v165, -v23, v72, v24
	v_fma_f32 v166, -v23, v73, v25
	v_mov_b32_e32 v202, v23
	v_pk_fma_f32 v[122:123], v[202:203], v[74:75], v[122:123] op_sel_hi:[0,1,1] neg_lo:[1,0,0] neg_hi:[1,0,0]
	v_pk_fma_f32 v[124:125], v[202:203], v[76:77], v[124:125] op_sel_hi:[0,1,1] neg_lo:[1,0,0] neg_hi:[1,0,0]
	v_pk_fma_f32 v[126:127], v[202:203], v[78:79], v[126:127] op_sel_hi:[0,1,1] neg_lo:[1,0,0] neg_hi:[1,0,0]
	v_pk_fma_f32 v[128:129], v[202:203], v[80:81], v[128:129] op_sel_hi:[0,1,1] neg_lo:[1,0,0] neg_hi:[1,0,0]
	v_pk_fma_f32 v[130:131], v[202:203], v[82:83], v[130:131] op_sel_hi:[0,1,1] neg_lo:[1,0,0] neg_hi:[1,0,0]
	v_pk_fma_f32 v[132:133], v[202:203], v[84:85], v[132:133] op_sel_hi:[0,1,1] neg_lo:[1,0,0] neg_hi:[1,0,0]
	v_pk_fma_f32 v[134:135], v[202:203], v[86:87], v[134:135] op_sel_hi:[0,1,1] neg_lo:[1,0,0] neg_hi:[1,0,0]
	v_pk_fma_f32 v[136:137], v[202:203], v[88:89], v[136:137] op_sel_hi:[0,1,1] neg_lo:[1,0,0] neg_hi:[1,0,0]
	v_pk_fma_f32 v[138:139], v[202:203], v[90:91], v[138:139] op_sel_hi:[0,1,1] neg_lo:[1,0,0] neg_hi:[1,0,0]
	v_pk_fma_f32 v[140:141], v[202:203], v[92:93], v[140:141] op_sel_hi:[0,1,1] neg_lo:[1,0,0] neg_hi:[1,0,0]
	v_pk_fma_f32 v[142:143], v[202:203], v[94:95], v[142:143] op_sel_hi:[0,1,1] neg_lo:[1,0,0] neg_hi:[1,0,0]
	v_pk_fma_f32 v[144:145], v[202:203], v[96:97], v[144:145] op_sel_hi:[0,1,1] neg_lo:[1,0,0] neg_hi:[1,0,0]
	v_pk_fma_f32 v[146:147], v[202:203], v[98:99], v[146:147] op_sel_hi:[0,1,1] neg_lo:[1,0,0] neg_hi:[1,0,0]
	v_pk_fma_f32 v[148:149], v[202:203], v[100:101], v[148:149] op_sel_hi:[0,1,1] neg_lo:[1,0,0] neg_hi:[1,0,0]
	v_pk_fma_f32 v[150:151], v[202:203], v[102:103], v[150:151] op_sel_hi:[0,1,1] neg_lo:[1,0,0] neg_hi:[1,0,0]
	v_pk_fma_f32 v[152:153], v[202:203], v[104:105], v[152:153] op_sel_hi:[0,1,1] neg_lo:[1,0,0] neg_hi:[1,0,0]
	v_pk_fma_f32 v[154:155], v[202:203], v[106:107], v[154:155] op_sel_hi:[0,1,1] neg_lo:[1,0,0] neg_hi:[1,0,0]
	v_pk_fma_f32 v[156:157], v[202:203], v[108:109], v[156:157] op_sel_hi:[0,1,1] neg_lo:[1,0,0] neg_hi:[1,0,0]
	v_pk_fma_f32 v[158:159], v[202:203], v[110:111], v[158:159] op_sel_hi:[0,1,1] neg_lo:[1,0,0] neg_hi:[1,0,0]
	v_pk_fma_f32 v[160:161], v[202:203], v[112:113], v[160:161] op_sel_hi:[0,1,1] neg_lo:[1,0,0] neg_hi:[1,0,0]
	v_pk_fma_f32 v[114:115], v[202:203], v[114:115], v[162:163] op_sel_hi:[0,1,1] neg_lo:[1,0,0] neg_hi:[1,0,0]
	v_fma_f32 v116, -v23, v116, v164
	v_fma_f32 v4, -v23, v117, v4
	ds_read_b128 v[70:73], v21 offset:5248
	ds_read_b128 v[74:77], v21 offset:5264
	ds_read_b128 v[78:81], v21 offset:5280
	ds_read_b128 v[82:85], v21 offset:5296
	ds_read_b128 v[86:89], v21 offset:5312
	ds_read_b128 v[90:93], v21 offset:5328
	ds_read_b128 v[94:97], v21 offset:5344
	ds_read_b128 v[98:101], v21 offset:5360
	ds_read_b128 v[102:105], v21 offset:5376
	ds_read_b128 v[106:109], v21 offset:5392
	ds_read_b128 v[110:113], v21 offset:5408
	s_waitcnt lgkmcnt(0)
	v_fma_f32 v25, -v165, v26, v5
	v_fma_f32 v24, -v165, v27, v22
	v_fma_f32 v23, -v165, v28, v165
	v_fma_f32 v22, -v165, v29, v166
	v_fma_f32 v5, -v165, v30, v122
	v_fma_f32 v117, -v165, v31, v123
	v_mov_b32_e32 v202, v165
	v_pk_fma_f32 v[122:123], v[202:203], v[32:33], v[124:125] op_sel_hi:[0,1,1] neg_lo:[1,0,0] neg_hi:[1,0,0]
	v_pk_fma_f32 v[124:125], v[202:203], v[34:35], v[126:127] op_sel_hi:[0,1,1] neg_lo:[1,0,0] neg_hi:[1,0,0]
	v_pk_fma_f32 v[126:127], v[202:203], v[36:37], v[128:129] op_sel_hi:[0,1,1] neg_lo:[1,0,0] neg_hi:[1,0,0]
	v_pk_fma_f32 v[128:129], v[202:203], v[38:39], v[130:131] op_sel_hi:[0,1,1] neg_lo:[1,0,0] neg_hi:[1,0,0]
	v_pk_fma_f32 v[130:131], v[202:203], v[40:41], v[132:133] op_sel_hi:[0,1,1] neg_lo:[1,0,0] neg_hi:[1,0,0]
	v_pk_fma_f32 v[132:133], v[202:203], v[42:43], v[134:135] op_sel_hi:[0,1,1] neg_lo:[1,0,0] neg_hi:[1,0,0]
	v_pk_fma_f32 v[134:135], v[202:203], v[44:45], v[136:137] op_sel_hi:[0,1,1] neg_lo:[1,0,0] neg_hi:[1,0,0]
	v_pk_fma_f32 v[136:137], v[202:203], v[46:47], v[138:139] op_sel_hi:[0,1,1] neg_lo:[1,0,0] neg_hi:[1,0,0]
	v_pk_fma_f32 v[138:139], v[202:203], v[48:49], v[140:141] op_sel_hi:[0,1,1] neg_lo:[1,0,0] neg_hi:[1,0,0]
	v_pk_fma_f32 v[140:141], v[202:203], v[50:51], v[142:143] op_sel_hi:[0,1,1] neg_lo:[1,0,0] neg_hi:[1,0,0]
	v_pk_fma_f32 v[142:143], v[202:203], v[52:53], v[144:145] op_sel_hi:[0,1,1] neg_lo:[1,0,0] neg_hi:[1,0,0]
	v_pk_fma_f32 v[144:145], v[202:203], v[54:55], v[146:147] op_sel_hi:[0,1,1] neg_lo:[1,0,0] neg_hi:[1,0,0]
	v_pk_fma_f32 v[146:147], v[202:203], v[56:57], v[148:149] op_sel_hi:[0,1,1] neg_lo:[1,0,0] neg_hi:[1,0,0]
	v_pk_fma_f32 v[148:149], v[202:203], v[58:59], v[150:151] op_sel_hi:[0,1,1] neg_lo:[1,0,0] neg_hi:[1,0,0]
	v_pk_fma_f32 v[150:151], v[202:203], v[60:61], v[152:153] op_sel_hi:[0,1,1] neg_lo:[1,0,0] neg_hi:[1,0,0]
	v_pk_fma_f32 v[152:153], v[202:203], v[62:63], v[154:155] op_sel_hi:[0,1,1] neg_lo:[1,0,0] neg_hi:[1,0,0]
	v_pk_fma_f32 v[154:155], v[202:203], v[64:65], v[156:157] op_sel_hi:[0,1,1] neg_lo:[1,0,0] neg_hi:[1,0,0]
	v_pk_fma_f32 v[156:157], v[202:203], v[66:67], v[158:159] op_sel_hi:[0,1,1] neg_lo:[1,0,0] neg_hi:[1,0,0]
	v_pk_fma_f32 v[158:159], v[202:203], v[68:69], v[160:161] op_sel_hi:[0,1,1] neg_lo:[1,0,0] neg_hi:[1,0,0]
	v_pk_fma_f32 v[114:115], v[202:203], v[118:119], v[114:115] op_sel_hi:[0,1,1] neg_lo:[1,0,0] neg_hi:[1,0,0]
	v_fma_f32 v116, -v165, v120, v116
	v_fma_f32 v4, -v165, v121, v4
	ds_read_b128 v[26:29], v21 offset:5520
	ds_read_b128 v[30:33], v21 offset:5536
	ds_read_b128 v[34:37], v21 offset:5552
	ds_read_b128 v[38:41], v21 offset:5568
	ds_read_b128 v[42:45], v21 offset:5584
	ds_read_b128 v[46:49], v21 offset:5600
	ds_read_b128 v[50:53], v21 offset:5616
	ds_read_b128 v[54:57], v21 offset:5632
	ds_read_b128 v[58:61], v21 offset:5648
	ds_read_b128 v[62:65], v21 offset:5664
	ds_read_b128 v[66:69], v21 offset:5680
	v_fma_f32 v5, -v22, v70, v5
	v_fma_f32 v117, -v22, v71, v117
	v_pk_fma_f32 v[118:119], v[22:23], v[72:73], v[122:123] op_sel_hi:[0,1,1] neg_lo:[1,0,0] neg_hi:[1,0,0]
	v_pk_fma_f32 v[120:121], v[22:23], v[74:75], v[124:125] op_sel_hi:[0,1,1] neg_lo:[1,0,0] neg_hi:[1,0,0]
	v_pk_fma_f32 v[122:123], v[22:23], v[76:77], v[126:127] op_sel_hi:[0,1,1] neg_lo:[1,0,0] neg_hi:[1,0,0]
	v_pk_fma_f32 v[124:125], v[22:23], v[78:79], v[128:129] op_sel_hi:[0,1,1] neg_lo:[1,0,0] neg_hi:[1,0,0]
	v_pk_fma_f32 v[126:127], v[22:23], v[80:81], v[130:131] op_sel_hi:[0,1,1] neg_lo:[1,0,0] neg_hi:[1,0,0]
	v_pk_fma_f32 v[128:129], v[22:23], v[82:83], v[132:133] op_sel_hi:[0,1,1] neg_lo:[1,0,0] neg_hi:[1,0,0]
	v_pk_fma_f32 v[130:131], v[22:23], v[84:85], v[134:135] op_sel_hi:[0,1,1] neg_lo:[1,0,0] neg_hi:[1,0,0]
	v_pk_fma_f32 v[132:133], v[22:23], v[86:87], v[136:137] op_sel_hi:[0,1,1] neg_lo:[1,0,0] neg_hi:[1,0,0]
	v_pk_fma_f32 v[134:135], v[22:23], v[88:89], v[138:139] op_sel_hi:[0,1,1] neg_lo:[1,0,0] neg_hi:[1,0,0]
	v_pk_fma_f32 v[136:137], v[22:23], v[90:91], v[140:141] op_sel_hi:[0,1,1] neg_lo:[1,0,0] neg_hi:[1,0,0]
	v_pk_fma_f32 v[138:139], v[22:23], v[92:93], v[142:143] op_sel_hi:[0,1,1] neg_lo:[1,0,0] neg_hi:[1,0,0]
	v_pk_fma_f32 v[140:141], v[22:23], v[94:95], v[144:145] op_sel_hi:[0,1,1] neg_lo:[1,0,0] neg_hi:[1,0,0]
	v_pk_fma_f32 v[142:143], v[22:23], v[96:97], v[146:147] op_sel_hi:[0,1,1] neg_lo:[1,0,0] neg_hi:[1,0,0]
	v_pk_fma_f32 v[144:145], v[22:23], v[98:99], v[148:149] op_sel_hi:[0,1,1] neg_lo:[1,0,0] neg_hi:[1,0,0]
	v_pk_fma_f32 v[146:147], v[22:23], v[100:101], v[150:151] op_sel_hi:[0,1,1] neg_lo:[1,0,0] neg_hi:[1,0,0]
	v_pk_fma_f32 v[148:149], v[22:23], v[102:103], v[152:153] op_sel_hi:[0,1,1] neg_lo:[1,0,0] neg_hi:[1,0,0]
	v_pk_fma_f32 v[150:151], v[22:23], v[104:105], v[154:155] op_sel_hi:[0,1,1] neg_lo:[1,0,0] neg_hi:[1,0,0]
	v_pk_fma_f32 v[152:153], v[22:23], v[106:107], v[156:157] op_sel_hi:[0,1,1] neg_lo:[1,0,0] neg_hi:[1,0,0]
	v_pk_fma_f32 v[154:155], v[22:23], v[108:109], v[158:159] op_sel_hi:[0,1,1] neg_lo:[1,0,0] neg_hi:[1,0,0]
	v_pk_fma_f32 v[114:115], v[22:23], v[110:111], v[114:115] op_sel_hi:[0,1,1] neg_lo:[1,0,0] neg_hi:[1,0,0]
	v_fma_f32 v116, -v22, v112, v116
	v_fma_f32 v4, -v22, v113, v4
	ds_read_b128 v[70:73], v21 offset:5792
	ds_read_b128 v[74:77], v21 offset:5808
	ds_read_b128 v[78:81], v21 offset:5824
	ds_read_b128 v[82:85], v21 offset:5840
	ds_read_b128 v[86:89], v21 offset:5856
	ds_read_b128 v[90:93], v21 offset:5872
	ds_read_b128 v[94:97], v21 offset:5888
	ds_read_b128 v[98:101], v21 offset:5904
	ds_read_b128 v[102:105], v21 offset:5920
	ds_read_b128 v[106:109], v21 offset:5936
	ds_read_b128 v[110:113], v21 offset:5952
	s_waitcnt lgkmcnt(0)
	v_fma_f32 v26, -v5, v26, v5
	v_fma_f32 v27, -v5, v27, v117
	v_mov_b32_e32 v202, v5
	v_pk_fma_f32 v[28:29], v[202:203], v[28:29], v[118:119] op_sel_hi:[0,1,1] neg_lo:[1,0,0] neg_hi:[1,0,0]
	v_pk_fma_f32 v[118:119], v[202:203], v[30:31], v[120:121] op_sel_hi:[0,1,1] neg_lo:[1,0,0] neg_hi:[1,0,0]
	v_pk_fma_f32 v[120:121], v[202:203], v[32:33], v[122:123] op_sel_hi:[0,1,1] neg_lo:[1,0,0] neg_hi:[1,0,0]
	v_pk_fma_f32 v[122:123], v[202:203], v[34:35], v[124:125] op_sel_hi:[0,1,1] neg_lo:[1,0,0] neg_hi:[1,0,0]
	v_pk_fma_f32 v[124:125], v[202:203], v[36:37], v[126:127] op_sel_hi:[0,1,1] neg_lo:[1,0,0] neg_hi:[1,0,0]
	v_pk_fma_f32 v[126:127], v[202:203], v[38:39], v[128:129] op_sel_hi:[0,1,1] neg_lo:[1,0,0] neg_hi:[1,0,0]
	v_pk_fma_f32 v[128:129], v[202:203], v[40:41], v[130:131] op_sel_hi:[0,1,1] neg_lo:[1,0,0] neg_hi:[1,0,0]
	v_pk_fma_f32 v[130:131], v[202:203], v[42:43], v[132:133] op_sel_hi:[0,1,1] neg_lo:[1,0,0] neg_hi:[1,0,0]
	v_pk_fma_f32 v[132:133], v[202:203], v[44:45], v[134:135] op_sel_hi:[0,1,1] neg_lo:[1,0,0] neg_hi:[1,0,0]
	v_pk_fma_f32 v[134:135], v[202:203], v[46:47], v[136:137] op_sel_hi:[0,1,1] neg_lo:[1,0,0] neg_hi:[1,0,0]
	v_pk_fma_f32 v[136:137], v[202:203], v[48:49], v[138:139] op_sel_hi:[0,1,1] neg_lo:[1,0,0] neg_hi:[1,0,0]
	v_pk_fma_f32 v[138:139], v[202:203], v[50:51], v[140:141] op_sel_hi:[0,1,1] neg_lo:[1,0,0] neg_hi:[1,0,0]
	v_pk_fma_f32 v[140:141], v[202:203], v[52:53], v[142:143] op_sel_hi:[0,1,1] neg_lo:[1,0,0] neg_hi:[1,0,0]
	v_pk_fma_f32 v[142:143], v[202:203], v[54:55], v[144:145] op_sel_hi:[0,1,1] neg_lo:[1,0,0] neg_hi:[1,0,0]
	v_pk_fma_f32 v[144:145], v[202:203], v[56:57], v[146:147] op_sel_hi:[0,1,1] neg_lo:[1,0,0] neg_hi:[1,0,0]
	v_pk_fma_f32 v[146:147], v[202:203], v[58:59], v[148:149] op_sel_hi:[0,1,1] neg_lo:[1,0,0] neg_hi:[1,0,0]
	v_pk_fma_f32 v[148:149], v[202:203], v[60:61], v[150:151] op_sel_hi:[0,1,1] neg_lo:[1,0,0] neg_hi:[1,0,0]
	v_pk_fma_f32 v[150:151], v[202:203], v[62:63], v[152:153] op_sel_hi:[0,1,1] neg_lo:[1,0,0] neg_hi:[1,0,0]
	v_pk_fma_f32 v[152:153], v[202:203], v[64:65], v[154:155] op_sel_hi:[0,1,1] neg_lo:[1,0,0] neg_hi:[1,0,0]
	v_pk_fma_f32 v[154:155], v[202:203], v[66:67], v[114:115] op_sel_hi:[0,1,1] neg_lo:[1,0,0] neg_hi:[1,0,0]
	v_fma_f32 v156, -v5, v68, v116
	v_fma_f32 v4, -v5, v69, v4
	ds_read_b128 v[30:33], v21 offset:6064
	ds_read_b128 v[34:37], v21 offset:6080
	ds_read_b128 v[38:41], v21 offset:6096
	ds_read_b128 v[42:45], v21 offset:6112
	ds_read_b128 v[46:49], v21 offset:6128
	ds_read_b128 v[50:53], v21 offset:6144
	ds_read_b128 v[54:57], v21 offset:6160
	ds_read_b128 v[58:61], v21 offset:6176
	ds_read_b128 v[62:65], v21 offset:6192
	ds_read_b128 v[66:69], v21 offset:6208
	ds_read_b128 v[114:117], v21 offset:6224
	v_fma_f32 v5, -v27, v70, v26
	v_fma_f32 v26, -v27, v71, v27
	v_fma_f32 v157, -v27, v72, v28
	v_fma_f32 v158, -v27, v73, v29
	v_mov_b32_e32 v202, v27
	v_pk_fma_f32 v[118:119], v[202:203], v[74:75], v[118:119] op_sel_hi:[0,1,1] neg_lo:[1,0,0] neg_hi:[1,0,0]
	v_pk_fma_f32 v[120:121], v[202:203], v[76:77], v[120:121] op_sel_hi:[0,1,1] neg_lo:[1,0,0] neg_hi:[1,0,0]
	v_pk_fma_f32 v[122:123], v[202:203], v[78:79], v[122:123] op_sel_hi:[0,1,1] neg_lo:[1,0,0] neg_hi:[1,0,0]
	v_pk_fma_f32 v[124:125], v[202:203], v[80:81], v[124:125] op_sel_hi:[0,1,1] neg_lo:[1,0,0] neg_hi:[1,0,0]
	v_pk_fma_f32 v[126:127], v[202:203], v[82:83], v[126:127] op_sel_hi:[0,1,1] neg_lo:[1,0,0] neg_hi:[1,0,0]
	v_pk_fma_f32 v[128:129], v[202:203], v[84:85], v[128:129] op_sel_hi:[0,1,1] neg_lo:[1,0,0] neg_hi:[1,0,0]
	v_pk_fma_f32 v[130:131], v[202:203], v[86:87], v[130:131] op_sel_hi:[0,1,1] neg_lo:[1,0,0] neg_hi:[1,0,0]
	v_pk_fma_f32 v[132:133], v[202:203], v[88:89], v[132:133] op_sel_hi:[0,1,1] neg_lo:[1,0,0] neg_hi:[1,0,0]
	v_pk_fma_f32 v[134:135], v[202:203], v[90:91], v[134:135] op_sel_hi:[0,1,1] neg_lo:[1,0,0] neg_hi:[1,0,0]
	v_pk_fma_f32 v[136:137], v[202:203], v[92:93], v[136:137] op_sel_hi:[0,1,1] neg_lo:[1,0,0] neg_hi:[1,0,0]
	v_pk_fma_f32 v[138:139], v[202:203], v[94:95], v[138:139] op_sel_hi:[0,1,1] neg_lo:[1,0,0] neg_hi:[1,0,0]
	v_pk_fma_f32 v[140:141], v[202:203], v[96:97], v[140:141] op_sel_hi:[0,1,1] neg_lo:[1,0,0] neg_hi:[1,0,0]
	v_pk_fma_f32 v[142:143], v[202:203], v[98:99], v[142:143] op_sel_hi:[0,1,1] neg_lo:[1,0,0] neg_hi:[1,0,0]
	v_pk_fma_f32 v[144:145], v[202:203], v[100:101], v[144:145] op_sel_hi:[0,1,1] neg_lo:[1,0,0] neg_hi:[1,0,0]
	v_pk_fma_f32 v[146:147], v[202:203], v[102:103], v[146:147] op_sel_hi:[0,1,1] neg_lo:[1,0,0] neg_hi:[1,0,0]
	v_pk_fma_f32 v[148:149], v[202:203], v[104:105], v[148:149] op_sel_hi:[0,1,1] neg_lo:[1,0,0] neg_hi:[1,0,0]
	v_pk_fma_f32 v[150:151], v[202:203], v[106:107], v[150:151] op_sel_hi:[0,1,1] neg_lo:[1,0,0] neg_hi:[1,0,0]
	v_pk_fma_f32 v[152:153], v[202:203], v[108:109], v[152:153] op_sel_hi:[0,1,1] neg_lo:[1,0,0] neg_hi:[1,0,0]
	v_pk_fma_f32 v[110:111], v[202:203], v[110:111], v[154:155] op_sel_hi:[0,1,1] neg_lo:[1,0,0] neg_hi:[1,0,0]
	v_fma_f32 v112, -v27, v112, v156
	v_fma_f32 v4, -v27, v113, v4
	ds_read_b128 v[70:73], v21 offset:6352
	ds_read_b128 v[74:77], v21 offset:6368
	ds_read_b128 v[78:81], v21 offset:6384
	ds_read_b128 v[82:85], v21 offset:6400
	ds_read_b128 v[86:89], v21 offset:6416
	ds_read_b128 v[90:93], v21 offset:6432
	ds_read_b128 v[94:97], v21 offset:6448
	ds_read_b128 v[98:101], v21 offset:6464
	ds_read_b128 v[102:105], v21 offset:6480
	ds_read_b128 v[106:109], v21 offset:6496
	s_waitcnt lgkmcnt(0)
	v_fma_f32 v29, -v157, v30, v5
	v_fma_f32 v28, -v157, v31, v26
	v_fma_f32 v27, -v157, v32, v157
	v_fma_f32 v26, -v157, v33, v158
	v_fma_f32 v5, -v157, v34, v118
	v_fma_f32 v113, -v157, v35, v119
	v_mov_b32_e32 v202, v157
	v_pk_fma_f32 v[118:119], v[202:203], v[36:37], v[120:121] op_sel_hi:[0,1,1] neg_lo:[1,0,0] neg_hi:[1,0,0]
	v_pk_fma_f32 v[120:121], v[202:203], v[38:39], v[122:123] op_sel_hi:[0,1,1] neg_lo:[1,0,0] neg_hi:[1,0,0]
	v_pk_fma_f32 v[122:123], v[202:203], v[40:41], v[124:125] op_sel_hi:[0,1,1] neg_lo:[1,0,0] neg_hi:[1,0,0]
	v_pk_fma_f32 v[124:125], v[202:203], v[42:43], v[126:127] op_sel_hi:[0,1,1] neg_lo:[1,0,0] neg_hi:[1,0,0]
	v_pk_fma_f32 v[126:127], v[202:203], v[44:45], v[128:129] op_sel_hi:[0,1,1] neg_lo:[1,0,0] neg_hi:[1,0,0]
	v_pk_fma_f32 v[128:129], v[202:203], v[46:47], v[130:131] op_sel_hi:[0,1,1] neg_lo:[1,0,0] neg_hi:[1,0,0]
	v_pk_fma_f32 v[130:131], v[202:203], v[48:49], v[132:133] op_sel_hi:[0,1,1] neg_lo:[1,0,0] neg_hi:[1,0,0]
	v_pk_fma_f32 v[132:133], v[202:203], v[50:51], v[134:135] op_sel_hi:[0,1,1] neg_lo:[1,0,0] neg_hi:[1,0,0]
	v_pk_fma_f32 v[134:135], v[202:203], v[52:53], v[136:137] op_sel_hi:[0,1,1] neg_lo:[1,0,0] neg_hi:[1,0,0]
	v_pk_fma_f32 v[136:137], v[202:203], v[54:55], v[138:139] op_sel_hi:[0,1,1] neg_lo:[1,0,0] neg_hi:[1,0,0]
	v_pk_fma_f32 v[138:139], v[202:203], v[56:57], v[140:141] op_sel_hi:[0,1,1] neg_lo:[1,0,0] neg_hi:[1,0,0]
	v_pk_fma_f32 v[140:141], v[202:203], v[58:59], v[142:143] op_sel_hi:[0,1,1] neg_lo:[1,0,0] neg_hi:[1,0,0]
	v_pk_fma_f32 v[142:143], v[202:203], v[60:61], v[144:145] op_sel_hi:[0,1,1] neg_lo:[1,0,0] neg_hi:[1,0,0]
	v_pk_fma_f32 v[144:145], v[202:203], v[62:63], v[146:147] op_sel_hi:[0,1,1] neg_lo:[1,0,0] neg_hi:[1,0,0]
	v_pk_fma_f32 v[146:147], v[202:203], v[64:65], v[148:149] op_sel_hi:[0,1,1] neg_lo:[1,0,0] neg_hi:[1,0,0]
	v_pk_fma_f32 v[148:149], v[202:203], v[66:67], v[150:151] op_sel_hi:[0,1,1] neg_lo:[1,0,0] neg_hi:[1,0,0]
	v_pk_fma_f32 v[150:151], v[202:203], v[68:69], v[152:153] op_sel_hi:[0,1,1] neg_lo:[1,0,0] neg_hi:[1,0,0]
	v_pk_fma_f32 v[110:111], v[202:203], v[114:115], v[110:111] op_sel_hi:[0,1,1] neg_lo:[1,0,0] neg_hi:[1,0,0]
	v_fma_f32 v112, -v157, v116, v112
	v_fma_f32 v4, -v157, v117, v4
	ds_read_b128 v[30:33], v21 offset:6624
	ds_read_b128 v[34:37], v21 offset:6640
	ds_read_b128 v[38:41], v21 offset:6656
	ds_read_b128 v[42:45], v21 offset:6672
	ds_read_b128 v[46:49], v21 offset:6688
	ds_read_b128 v[50:53], v21 offset:6704
	ds_read_b128 v[54:57], v21 offset:6720
	ds_read_b128 v[58:61], v21 offset:6736
	ds_read_b128 v[62:65], v21 offset:6752
	ds_read_b128 v[66:69], v21 offset:6768
	v_fma_f32 v5, -v26, v70, v5
	v_fma_f32 v113, -v26, v71, v113
	v_pk_fma_f32 v[114:115], v[26:27], v[72:73], v[118:119] op_sel_hi:[0,1,1] neg_lo:[1,0,0] neg_hi:[1,0,0]
	v_pk_fma_f32 v[116:117], v[26:27], v[74:75], v[120:121] op_sel_hi:[0,1,1] neg_lo:[1,0,0] neg_hi:[1,0,0]
	v_pk_fma_f32 v[118:119], v[26:27], v[76:77], v[122:123] op_sel_hi:[0,1,1] neg_lo:[1,0,0] neg_hi:[1,0,0]
	v_pk_fma_f32 v[120:121], v[26:27], v[78:79], v[124:125] op_sel_hi:[0,1,1] neg_lo:[1,0,0] neg_hi:[1,0,0]
	v_pk_fma_f32 v[122:123], v[26:27], v[80:81], v[126:127] op_sel_hi:[0,1,1] neg_lo:[1,0,0] neg_hi:[1,0,0]
	v_pk_fma_f32 v[124:125], v[26:27], v[82:83], v[128:129] op_sel_hi:[0,1,1] neg_lo:[1,0,0] neg_hi:[1,0,0]
	v_pk_fma_f32 v[126:127], v[26:27], v[84:85], v[130:131] op_sel_hi:[0,1,1] neg_lo:[1,0,0] neg_hi:[1,0,0]
	v_pk_fma_f32 v[128:129], v[26:27], v[86:87], v[132:133] op_sel_hi:[0,1,1] neg_lo:[1,0,0] neg_hi:[1,0,0]
	v_pk_fma_f32 v[130:131], v[26:27], v[88:89], v[134:135] op_sel_hi:[0,1,1] neg_lo:[1,0,0] neg_hi:[1,0,0]
	v_pk_fma_f32 v[132:133], v[26:27], v[90:91], v[136:137] op_sel_hi:[0,1,1] neg_lo:[1,0,0] neg_hi:[1,0,0]
	v_pk_fma_f32 v[134:135], v[26:27], v[92:93], v[138:139] op_sel_hi:[0,1,1] neg_lo:[1,0,0] neg_hi:[1,0,0]
	v_pk_fma_f32 v[136:137], v[26:27], v[94:95], v[140:141] op_sel_hi:[0,1,1] neg_lo:[1,0,0] neg_hi:[1,0,0]
	v_pk_fma_f32 v[138:139], v[26:27], v[96:97], v[142:143] op_sel_hi:[0,1,1] neg_lo:[1,0,0] neg_hi:[1,0,0]
	v_pk_fma_f32 v[140:141], v[26:27], v[98:99], v[144:145] op_sel_hi:[0,1,1] neg_lo:[1,0,0] neg_hi:[1,0,0]
	v_pk_fma_f32 v[142:143], v[26:27], v[100:101], v[146:147] op_sel_hi:[0,1,1] neg_lo:[1,0,0] neg_hi:[1,0,0]
	v_pk_fma_f32 v[144:145], v[26:27], v[102:103], v[148:149] op_sel_hi:[0,1,1] neg_lo:[1,0,0] neg_hi:[1,0,0]
	v_pk_fma_f32 v[146:147], v[26:27], v[104:105], v[150:151] op_sel_hi:[0,1,1] neg_lo:[1,0,0] neg_hi:[1,0,0]
	v_pk_fma_f32 v[110:111], v[26:27], v[106:107], v[110:111] op_sel_hi:[0,1,1] neg_lo:[1,0,0] neg_hi:[1,0,0]
	v_fma_f32 v112, -v26, v108, v112
	v_fma_f32 v4, -v26, v109, v4
	ds_read_b128 v[70:73], v21 offset:6896
	ds_read_b128 v[74:77], v21 offset:6912
	ds_read_b128 v[78:81], v21 offset:6928
	ds_read_b128 v[82:85], v21 offset:6944
	ds_read_b128 v[86:89], v21 offset:6960
	ds_read_b128 v[90:93], v21 offset:6976
	ds_read_b128 v[94:97], v21 offset:6992
	ds_read_b128 v[98:101], v21 offset:7008
	ds_read_b128 v[102:105], v21 offset:7024
	ds_read_b128 v[106:109], v21 offset:7040
	s_waitcnt lgkmcnt(0)
	v_fma_f32 v30, -v5, v30, v5
	v_fma_f32 v31, -v5, v31, v113
	v_mov_b32_e32 v202, v5
	v_pk_fma_f32 v[32:33], v[202:203], v[32:33], v[114:115] op_sel_hi:[0,1,1] neg_lo:[1,0,0] neg_hi:[1,0,0]
	v_pk_fma_f32 v[114:115], v[202:203], v[34:35], v[116:117] op_sel_hi:[0,1,1] neg_lo:[1,0,0] neg_hi:[1,0,0]
	v_pk_fma_f32 v[116:117], v[202:203], v[36:37], v[118:119] op_sel_hi:[0,1,1] neg_lo:[1,0,0] neg_hi:[1,0,0]
	v_pk_fma_f32 v[118:119], v[202:203], v[38:39], v[120:121] op_sel_hi:[0,1,1] neg_lo:[1,0,0] neg_hi:[1,0,0]
	v_pk_fma_f32 v[120:121], v[202:203], v[40:41], v[122:123] op_sel_hi:[0,1,1] neg_lo:[1,0,0] neg_hi:[1,0,0]
	v_pk_fma_f32 v[122:123], v[202:203], v[42:43], v[124:125] op_sel_hi:[0,1,1] neg_lo:[1,0,0] neg_hi:[1,0,0]
	v_pk_fma_f32 v[124:125], v[202:203], v[44:45], v[126:127] op_sel_hi:[0,1,1] neg_lo:[1,0,0] neg_hi:[1,0,0]
	v_pk_fma_f32 v[126:127], v[202:203], v[46:47], v[128:129] op_sel_hi:[0,1,1] neg_lo:[1,0,0] neg_hi:[1,0,0]
	v_pk_fma_f32 v[128:129], v[202:203], v[48:49], v[130:131] op_sel_hi:[0,1,1] neg_lo:[1,0,0] neg_hi:[1,0,0]
	v_pk_fma_f32 v[130:131], v[202:203], v[50:51], v[132:133] op_sel_hi:[0,1,1] neg_lo:[1,0,0] neg_hi:[1,0,0]
	v_pk_fma_f32 v[132:133], v[202:203], v[52:53], v[134:135] op_sel_hi:[0,1,1] neg_lo:[1,0,0] neg_hi:[1,0,0]
	v_pk_fma_f32 v[134:135], v[202:203], v[54:55], v[136:137] op_sel_hi:[0,1,1] neg_lo:[1,0,0] neg_hi:[1,0,0]
	v_pk_fma_f32 v[136:137], v[202:203], v[56:57], v[138:139] op_sel_hi:[0,1,1] neg_lo:[1,0,0] neg_hi:[1,0,0]
	v_pk_fma_f32 v[138:139], v[202:203], v[58:59], v[140:141] op_sel_hi:[0,1,1] neg_lo:[1,0,0] neg_hi:[1,0,0]
	v_pk_fma_f32 v[140:141], v[202:203], v[60:61], v[142:143] op_sel_hi:[0,1,1] neg_lo:[1,0,0] neg_hi:[1,0,0]
	v_pk_fma_f32 v[142:143], v[202:203], v[62:63], v[144:145] op_sel_hi:[0,1,1] neg_lo:[1,0,0] neg_hi:[1,0,0]
	v_pk_fma_f32 v[144:145], v[202:203], v[64:65], v[146:147] op_sel_hi:[0,1,1] neg_lo:[1,0,0] neg_hi:[1,0,0]
	v_pk_fma_f32 v[146:147], v[202:203], v[66:67], v[110:111] op_sel_hi:[0,1,1] neg_lo:[1,0,0] neg_hi:[1,0,0]
	v_fma_f32 v148, -v5, v68, v112
	v_fma_f32 v4, -v5, v69, v4
	ds_read_b128 v[34:37], v21 offset:7168
	ds_read_b128 v[38:41], v21 offset:7184
	ds_read_b128 v[42:45], v21 offset:7200
	ds_read_b128 v[46:49], v21 offset:7216
	ds_read_b128 v[50:53], v21 offset:7232
	ds_read_b128 v[54:57], v21 offset:7248
	ds_read_b128 v[58:61], v21 offset:7264
	ds_read_b128 v[62:65], v21 offset:7280
	ds_read_b128 v[66:69], v21 offset:7296
	ds_read_b128 v[110:113], v21 offset:7312
	v_fma_f32 v5, -v31, v70, v30
	v_fma_f32 v30, -v31, v71, v31
	v_fma_f32 v149, -v31, v72, v32
	v_fma_f32 v150, -v31, v73, v33
	v_mov_b32_e32 v202, v31
	v_pk_fma_f32 v[114:115], v[202:203], v[74:75], v[114:115] op_sel_hi:[0,1,1] neg_lo:[1,0,0] neg_hi:[1,0,0]
	v_pk_fma_f32 v[116:117], v[202:203], v[76:77], v[116:117] op_sel_hi:[0,1,1] neg_lo:[1,0,0] neg_hi:[1,0,0]
	v_pk_fma_f32 v[118:119], v[202:203], v[78:79], v[118:119] op_sel_hi:[0,1,1] neg_lo:[1,0,0] neg_hi:[1,0,0]
	v_pk_fma_f32 v[120:121], v[202:203], v[80:81], v[120:121] op_sel_hi:[0,1,1] neg_lo:[1,0,0] neg_hi:[1,0,0]
	v_pk_fma_f32 v[122:123], v[202:203], v[82:83], v[122:123] op_sel_hi:[0,1,1] neg_lo:[1,0,0] neg_hi:[1,0,0]
	v_pk_fma_f32 v[124:125], v[202:203], v[84:85], v[124:125] op_sel_hi:[0,1,1] neg_lo:[1,0,0] neg_hi:[1,0,0]
	v_pk_fma_f32 v[126:127], v[202:203], v[86:87], v[126:127] op_sel_hi:[0,1,1] neg_lo:[1,0,0] neg_hi:[1,0,0]
	v_pk_fma_f32 v[128:129], v[202:203], v[88:89], v[128:129] op_sel_hi:[0,1,1] neg_lo:[1,0,0] neg_hi:[1,0,0]
	v_pk_fma_f32 v[130:131], v[202:203], v[90:91], v[130:131] op_sel_hi:[0,1,1] neg_lo:[1,0,0] neg_hi:[1,0,0]
	v_pk_fma_f32 v[132:133], v[202:203], v[92:93], v[132:133] op_sel_hi:[0,1,1] neg_lo:[1,0,0] neg_hi:[1,0,0]
	v_pk_fma_f32 v[134:135], v[202:203], v[94:95], v[134:135] op_sel_hi:[0,1,1] neg_lo:[1,0,0] neg_hi:[1,0,0]
	v_pk_fma_f32 v[136:137], v[202:203], v[96:97], v[136:137] op_sel_hi:[0,1,1] neg_lo:[1,0,0] neg_hi:[1,0,0]
	v_pk_fma_f32 v[138:139], v[202:203], v[98:99], v[138:139] op_sel_hi:[0,1,1] neg_lo:[1,0,0] neg_hi:[1,0,0]
	v_pk_fma_f32 v[140:141], v[202:203], v[100:101], v[140:141] op_sel_hi:[0,1,1] neg_lo:[1,0,0] neg_hi:[1,0,0]
	v_pk_fma_f32 v[142:143], v[202:203], v[102:103], v[142:143] op_sel_hi:[0,1,1] neg_lo:[1,0,0] neg_hi:[1,0,0]
	v_pk_fma_f32 v[144:145], v[202:203], v[104:105], v[144:145] op_sel_hi:[0,1,1] neg_lo:[1,0,0] neg_hi:[1,0,0]
	v_pk_fma_f32 v[106:107], v[202:203], v[106:107], v[146:147] op_sel_hi:[0,1,1] neg_lo:[1,0,0] neg_hi:[1,0,0]
	v_fma_f32 v108, -v31, v108, v148
	v_fma_f32 v4, -v31, v109, v4
	ds_read_b128 v[70:73], v21 offset:7456
	ds_read_b128 v[74:77], v21 offset:7472
	ds_read_b128 v[78:81], v21 offset:7488
	ds_read_b128 v[82:85], v21 offset:7504
	ds_read_b128 v[86:89], v21 offset:7520
	ds_read_b128 v[90:93], v21 offset:7536
	ds_read_b128 v[94:97], v21 offset:7552
	ds_read_b128 v[98:101], v21 offset:7568
	ds_read_b128 v[102:105], v21 offset:7584
	s_waitcnt lgkmcnt(0)
	v_fma_f32 v33, -v149, v34, v5
	v_fma_f32 v32, -v149, v35, v30
	v_fma_f32 v31, -v149, v36, v149
	v_fma_f32 v30, -v149, v37, v150
	v_fma_f32 v5, -v149, v38, v114
	v_fma_f32 v109, -v149, v39, v115
	v_mov_b32_e32 v202, v149
	v_pk_fma_f32 v[114:115], v[202:203], v[40:41], v[116:117] op_sel_hi:[0,1,1] neg_lo:[1,0,0] neg_hi:[1,0,0]
	v_pk_fma_f32 v[116:117], v[202:203], v[42:43], v[118:119] op_sel_hi:[0,1,1] neg_lo:[1,0,0] neg_hi:[1,0,0]
	v_pk_fma_f32 v[118:119], v[202:203], v[44:45], v[120:121] op_sel_hi:[0,1,1] neg_lo:[1,0,0] neg_hi:[1,0,0]
	v_pk_fma_f32 v[120:121], v[202:203], v[46:47], v[122:123] op_sel_hi:[0,1,1] neg_lo:[1,0,0] neg_hi:[1,0,0]
	v_pk_fma_f32 v[122:123], v[202:203], v[48:49], v[124:125] op_sel_hi:[0,1,1] neg_lo:[1,0,0] neg_hi:[1,0,0]
	v_pk_fma_f32 v[124:125], v[202:203], v[50:51], v[126:127] op_sel_hi:[0,1,1] neg_lo:[1,0,0] neg_hi:[1,0,0]
	v_pk_fma_f32 v[126:127], v[202:203], v[52:53], v[128:129] op_sel_hi:[0,1,1] neg_lo:[1,0,0] neg_hi:[1,0,0]
	v_pk_fma_f32 v[128:129], v[202:203], v[54:55], v[130:131] op_sel_hi:[0,1,1] neg_lo:[1,0,0] neg_hi:[1,0,0]
	v_pk_fma_f32 v[130:131], v[202:203], v[56:57], v[132:133] op_sel_hi:[0,1,1] neg_lo:[1,0,0] neg_hi:[1,0,0]
	v_pk_fma_f32 v[132:133], v[202:203], v[58:59], v[134:135] op_sel_hi:[0,1,1] neg_lo:[1,0,0] neg_hi:[1,0,0]
	v_pk_fma_f32 v[134:135], v[202:203], v[60:61], v[136:137] op_sel_hi:[0,1,1] neg_lo:[1,0,0] neg_hi:[1,0,0]
	v_pk_fma_f32 v[136:137], v[202:203], v[62:63], v[138:139] op_sel_hi:[0,1,1] neg_lo:[1,0,0] neg_hi:[1,0,0]
	v_pk_fma_f32 v[138:139], v[202:203], v[64:65], v[140:141] op_sel_hi:[0,1,1] neg_lo:[1,0,0] neg_hi:[1,0,0]
	v_pk_fma_f32 v[140:141], v[202:203], v[66:67], v[142:143] op_sel_hi:[0,1,1] neg_lo:[1,0,0] neg_hi:[1,0,0]
	v_pk_fma_f32 v[142:143], v[202:203], v[68:69], v[144:145] op_sel_hi:[0,1,1] neg_lo:[1,0,0] neg_hi:[1,0,0]
	v_pk_fma_f32 v[106:107], v[202:203], v[110:111], v[106:107] op_sel_hi:[0,1,1] neg_lo:[1,0,0] neg_hi:[1,0,0]
	v_fma_f32 v108, -v149, v112, v108
	v_fma_f32 v4, -v149, v113, v4
	ds_read_b128 v[34:37], v21 offset:7728
	ds_read_b128 v[38:41], v21 offset:7744
	ds_read_b128 v[42:45], v21 offset:7760
	ds_read_b128 v[46:49], v21 offset:7776
	ds_read_b128 v[50:53], v21 offset:7792
	ds_read_b128 v[54:57], v21 offset:7808
	ds_read_b128 v[58:61], v21 offset:7824
	ds_read_b128 v[62:65], v21 offset:7840
	ds_read_b128 v[66:69], v21 offset:7856
	v_fma_f32 v5, -v30, v70, v5
	v_fma_f32 v109, -v30, v71, v109
	v_pk_fma_f32 v[110:111], v[30:31], v[72:73], v[114:115] op_sel_hi:[0,1,1] neg_lo:[1,0,0] neg_hi:[1,0,0]
	v_pk_fma_f32 v[112:113], v[30:31], v[74:75], v[116:117] op_sel_hi:[0,1,1] neg_lo:[1,0,0] neg_hi:[1,0,0]
	v_pk_fma_f32 v[114:115], v[30:31], v[76:77], v[118:119] op_sel_hi:[0,1,1] neg_lo:[1,0,0] neg_hi:[1,0,0]
	v_pk_fma_f32 v[116:117], v[30:31], v[78:79], v[120:121] op_sel_hi:[0,1,1] neg_lo:[1,0,0] neg_hi:[1,0,0]
	v_pk_fma_f32 v[118:119], v[30:31], v[80:81], v[122:123] op_sel_hi:[0,1,1] neg_lo:[1,0,0] neg_hi:[1,0,0]
	v_pk_fma_f32 v[120:121], v[30:31], v[82:83], v[124:125] op_sel_hi:[0,1,1] neg_lo:[1,0,0] neg_hi:[1,0,0]
	v_pk_fma_f32 v[122:123], v[30:31], v[84:85], v[126:127] op_sel_hi:[0,1,1] neg_lo:[1,0,0] neg_hi:[1,0,0]
	v_pk_fma_f32 v[124:125], v[30:31], v[86:87], v[128:129] op_sel_hi:[0,1,1] neg_lo:[1,0,0] neg_hi:[1,0,0]
	v_pk_fma_f32 v[126:127], v[30:31], v[88:89], v[130:131] op_sel_hi:[0,1,1] neg_lo:[1,0,0] neg_hi:[1,0,0]
	v_pk_fma_f32 v[128:129], v[30:31], v[90:91], v[132:133] op_sel_hi:[0,1,1] neg_lo:[1,0,0] neg_hi:[1,0,0]
	v_pk_fma_f32 v[130:131], v[30:31], v[92:93], v[134:135] op_sel_hi:[0,1,1] neg_lo:[1,0,0] neg_hi:[1,0,0]
	v_pk_fma_f32 v[132:133], v[30:31], v[94:95], v[136:137] op_sel_hi:[0,1,1] neg_lo:[1,0,0] neg_hi:[1,0,0]
	v_pk_fma_f32 v[134:135], v[30:31], v[96:97], v[138:139] op_sel_hi:[0,1,1] neg_lo:[1,0,0] neg_hi:[1,0,0]
	v_pk_fma_f32 v[136:137], v[30:31], v[98:99], v[140:141] op_sel_hi:[0,1,1] neg_lo:[1,0,0] neg_hi:[1,0,0]
	v_pk_fma_f32 v[138:139], v[30:31], v[100:101], v[142:143] op_sel_hi:[0,1,1] neg_lo:[1,0,0] neg_hi:[1,0,0]
	v_pk_fma_f32 v[106:107], v[30:31], v[102:103], v[106:107] op_sel_hi:[0,1,1] neg_lo:[1,0,0] neg_hi:[1,0,0]
	v_fma_f32 v108, -v30, v104, v108
	v_fma_f32 v4, -v30, v105, v4
	ds_read_b128 v[70:73], v21 offset:8000
	ds_read_b128 v[74:77], v21 offset:8016
	ds_read_b128 v[78:81], v21 offset:8032
	ds_read_b128 v[82:85], v21 offset:8048
	ds_read_b128 v[86:89], v21 offset:8064
	ds_read_b128 v[90:93], v21 offset:8080
	ds_read_b128 v[94:97], v21 offset:8096
	ds_read_b128 v[98:101], v21 offset:8112
	ds_read_b128 v[102:105], v21 offset:8128
	s_waitcnt lgkmcnt(0)
	v_fma_f32 v34, -v5, v34, v5
	v_fma_f32 v35, -v5, v35, v109
	v_mov_b32_e32 v202, v5
	v_pk_fma_f32 v[36:37], v[202:203], v[36:37], v[110:111] op_sel_hi:[0,1,1] neg_lo:[1,0,0] neg_hi:[1,0,0]
	v_pk_fma_f32 v[110:111], v[202:203], v[38:39], v[112:113] op_sel_hi:[0,1,1] neg_lo:[1,0,0] neg_hi:[1,0,0]
	v_pk_fma_f32 v[112:113], v[202:203], v[40:41], v[114:115] op_sel_hi:[0,1,1] neg_lo:[1,0,0] neg_hi:[1,0,0]
	v_pk_fma_f32 v[114:115], v[202:203], v[42:43], v[116:117] op_sel_hi:[0,1,1] neg_lo:[1,0,0] neg_hi:[1,0,0]
	v_pk_fma_f32 v[116:117], v[202:203], v[44:45], v[118:119] op_sel_hi:[0,1,1] neg_lo:[1,0,0] neg_hi:[1,0,0]
	v_pk_fma_f32 v[118:119], v[202:203], v[46:47], v[120:121] op_sel_hi:[0,1,1] neg_lo:[1,0,0] neg_hi:[1,0,0]
	v_pk_fma_f32 v[120:121], v[202:203], v[48:49], v[122:123] op_sel_hi:[0,1,1] neg_lo:[1,0,0] neg_hi:[1,0,0]
	v_pk_fma_f32 v[122:123], v[202:203], v[50:51], v[124:125] op_sel_hi:[0,1,1] neg_lo:[1,0,0] neg_hi:[1,0,0]
	v_pk_fma_f32 v[124:125], v[202:203], v[52:53], v[126:127] op_sel_hi:[0,1,1] neg_lo:[1,0,0] neg_hi:[1,0,0]
	v_pk_fma_f32 v[126:127], v[202:203], v[54:55], v[128:129] op_sel_hi:[0,1,1] neg_lo:[1,0,0] neg_hi:[1,0,0]
	v_pk_fma_f32 v[128:129], v[202:203], v[56:57], v[130:131] op_sel_hi:[0,1,1] neg_lo:[1,0,0] neg_hi:[1,0,0]
	v_pk_fma_f32 v[130:131], v[202:203], v[58:59], v[132:133] op_sel_hi:[0,1,1] neg_lo:[1,0,0] neg_hi:[1,0,0]
	v_pk_fma_f32 v[132:133], v[202:203], v[60:61], v[134:135] op_sel_hi:[0,1,1] neg_lo:[1,0,0] neg_hi:[1,0,0]
	v_pk_fma_f32 v[134:135], v[202:203], v[62:63], v[136:137] op_sel_hi:[0,1,1] neg_lo:[1,0,0] neg_hi:[1,0,0]
	v_pk_fma_f32 v[136:137], v[202:203], v[64:65], v[138:139] op_sel_hi:[0,1,1] neg_lo:[1,0,0] neg_hi:[1,0,0]
	v_pk_fma_f32 v[138:139], v[202:203], v[66:67], v[106:107] op_sel_hi:[0,1,1] neg_lo:[1,0,0] neg_hi:[1,0,0]
	v_fma_f32 v140, -v5, v68, v108
	v_fma_f32 v4, -v5, v69, v4
	ds_read_b128 v[38:41], v21 offset:8272
	ds_read_b128 v[42:45], v21 offset:8288
	ds_read_b128 v[46:49], v21 offset:8304
	ds_read_b128 v[50:53], v21 offset:8320
	ds_read_b128 v[54:57], v21 offset:8336
	ds_read_b128 v[58:61], v21 offset:8352
	ds_read_b128 v[62:65], v21 offset:8368
	ds_read_b128 v[66:69], v21 offset:8384
	ds_read_b128 v[106:109], v21 offset:8400
	v_fma_f32 v5, -v35, v70, v34
	v_fma_f32 v34, -v35, v71, v35
	v_fma_f32 v141, -v35, v72, v36
	v_fma_f32 v142, -v35, v73, v37
	v_mov_b32_e32 v202, v35
	v_pk_fma_f32 v[110:111], v[202:203], v[74:75], v[110:111] op_sel_hi:[0,1,1] neg_lo:[1,0,0] neg_hi:[1,0,0]
	v_pk_fma_f32 v[112:113], v[202:203], v[76:77], v[112:113] op_sel_hi:[0,1,1] neg_lo:[1,0,0] neg_hi:[1,0,0]
	v_pk_fma_f32 v[114:115], v[202:203], v[78:79], v[114:115] op_sel_hi:[0,1,1] neg_lo:[1,0,0] neg_hi:[1,0,0]
	v_pk_fma_f32 v[116:117], v[202:203], v[80:81], v[116:117] op_sel_hi:[0,1,1] neg_lo:[1,0,0] neg_hi:[1,0,0]
	v_pk_fma_f32 v[118:119], v[202:203], v[82:83], v[118:119] op_sel_hi:[0,1,1] neg_lo:[1,0,0] neg_hi:[1,0,0]
	v_pk_fma_f32 v[120:121], v[202:203], v[84:85], v[120:121] op_sel_hi:[0,1,1] neg_lo:[1,0,0] neg_hi:[1,0,0]
	v_pk_fma_f32 v[122:123], v[202:203], v[86:87], v[122:123] op_sel_hi:[0,1,1] neg_lo:[1,0,0] neg_hi:[1,0,0]
	v_pk_fma_f32 v[124:125], v[202:203], v[88:89], v[124:125] op_sel_hi:[0,1,1] neg_lo:[1,0,0] neg_hi:[1,0,0]
	v_pk_fma_f32 v[126:127], v[202:203], v[90:91], v[126:127] op_sel_hi:[0,1,1] neg_lo:[1,0,0] neg_hi:[1,0,0]
	v_pk_fma_f32 v[128:129], v[202:203], v[92:93], v[128:129] op_sel_hi:[0,1,1] neg_lo:[1,0,0] neg_hi:[1,0,0]
	v_pk_fma_f32 v[130:131], v[202:203], v[94:95], v[130:131] op_sel_hi:[0,1,1] neg_lo:[1,0,0] neg_hi:[1,0,0]
	v_pk_fma_f32 v[132:133], v[202:203], v[96:97], v[132:133] op_sel_hi:[0,1,1] neg_lo:[1,0,0] neg_hi:[1,0,0]
	v_pk_fma_f32 v[134:135], v[202:203], v[98:99], v[134:135] op_sel_hi:[0,1,1] neg_lo:[1,0,0] neg_hi:[1,0,0]
	v_pk_fma_f32 v[136:137], v[202:203], v[100:101], v[136:137] op_sel_hi:[0,1,1] neg_lo:[1,0,0] neg_hi:[1,0,0]
	v_pk_fma_f32 v[102:103], v[202:203], v[102:103], v[138:139] op_sel_hi:[0,1,1] neg_lo:[1,0,0] neg_hi:[1,0,0]
	v_fma_f32 v104, -v35, v104, v140
	v_fma_f32 v4, -v35, v105, v4
	ds_read_b128 v[70:73], v21 offset:8560
	ds_read_b128 v[74:77], v21 offset:8576
	ds_read_b128 v[78:81], v21 offset:8592
	ds_read_b128 v[82:85], v21 offset:8608
	ds_read_b128 v[86:89], v21 offset:8624
	ds_read_b128 v[90:93], v21 offset:8640
	ds_read_b128 v[94:97], v21 offset:8656
	ds_read_b128 v[98:101], v21 offset:8672
	s_waitcnt lgkmcnt(0)
	v_fma_f32 v37, -v141, v38, v5
	v_fma_f32 v36, -v141, v39, v34
	v_fma_f32 v35, -v141, v40, v141
	v_fma_f32 v34, -v141, v41, v142
	v_fma_f32 v5, -v141, v42, v110
	v_fma_f32 v105, -v141, v43, v111
	v_mov_b32_e32 v202, v141
	v_pk_fma_f32 v[110:111], v[202:203], v[44:45], v[112:113] op_sel_hi:[0,1,1] neg_lo:[1,0,0] neg_hi:[1,0,0]
	v_pk_fma_f32 v[112:113], v[202:203], v[46:47], v[114:115] op_sel_hi:[0,1,1] neg_lo:[1,0,0] neg_hi:[1,0,0]
	v_pk_fma_f32 v[114:115], v[202:203], v[48:49], v[116:117] op_sel_hi:[0,1,1] neg_lo:[1,0,0] neg_hi:[1,0,0]
	v_pk_fma_f32 v[116:117], v[202:203], v[50:51], v[118:119] op_sel_hi:[0,1,1] neg_lo:[1,0,0] neg_hi:[1,0,0]
	v_pk_fma_f32 v[118:119], v[202:203], v[52:53], v[120:121] op_sel_hi:[0,1,1] neg_lo:[1,0,0] neg_hi:[1,0,0]
	v_pk_fma_f32 v[120:121], v[202:203], v[54:55], v[122:123] op_sel_hi:[0,1,1] neg_lo:[1,0,0] neg_hi:[1,0,0]
	v_pk_fma_f32 v[122:123], v[202:203], v[56:57], v[124:125] op_sel_hi:[0,1,1] neg_lo:[1,0,0] neg_hi:[1,0,0]
	v_pk_fma_f32 v[124:125], v[202:203], v[58:59], v[126:127] op_sel_hi:[0,1,1] neg_lo:[1,0,0] neg_hi:[1,0,0]
	v_pk_fma_f32 v[126:127], v[202:203], v[60:61], v[128:129] op_sel_hi:[0,1,1] neg_lo:[1,0,0] neg_hi:[1,0,0]
	v_pk_fma_f32 v[128:129], v[202:203], v[62:63], v[130:131] op_sel_hi:[0,1,1] neg_lo:[1,0,0] neg_hi:[1,0,0]
	v_pk_fma_f32 v[130:131], v[202:203], v[64:65], v[132:133] op_sel_hi:[0,1,1] neg_lo:[1,0,0] neg_hi:[1,0,0]
	v_pk_fma_f32 v[132:133], v[202:203], v[66:67], v[134:135] op_sel_hi:[0,1,1] neg_lo:[1,0,0] neg_hi:[1,0,0]
	v_pk_fma_f32 v[134:135], v[202:203], v[68:69], v[136:137] op_sel_hi:[0,1,1] neg_lo:[1,0,0] neg_hi:[1,0,0]
	v_pk_fma_f32 v[102:103], v[202:203], v[106:107], v[102:103] op_sel_hi:[0,1,1] neg_lo:[1,0,0] neg_hi:[1,0,0]
	v_fma_f32 v104, -v141, v108, v104
	v_fma_f32 v4, -v141, v109, v4
	ds_read_b128 v[38:41], v21 offset:8832
	ds_read_b128 v[42:45], v21 offset:8848
	ds_read_b128 v[46:49], v21 offset:8864
	ds_read_b128 v[50:53], v21 offset:8880
	ds_read_b128 v[54:57], v21 offset:8896
	ds_read_b128 v[58:61], v21 offset:8912
	ds_read_b128 v[62:65], v21 offset:8928
	ds_read_b128 v[66:69], v21 offset:8944
	v_fma_f32 v5, -v34, v70, v5
	v_fma_f32 v105, -v34, v71, v105
	v_pk_fma_f32 v[106:107], v[34:35], v[72:73], v[110:111] op_sel_hi:[0,1,1] neg_lo:[1,0,0] neg_hi:[1,0,0]
	v_pk_fma_f32 v[108:109], v[34:35], v[74:75], v[112:113] op_sel_hi:[0,1,1] neg_lo:[1,0,0] neg_hi:[1,0,0]
	v_pk_fma_f32 v[110:111], v[34:35], v[76:77], v[114:115] op_sel_hi:[0,1,1] neg_lo:[1,0,0] neg_hi:[1,0,0]
	v_pk_fma_f32 v[112:113], v[34:35], v[78:79], v[116:117] op_sel_hi:[0,1,1] neg_lo:[1,0,0] neg_hi:[1,0,0]
	v_pk_fma_f32 v[114:115], v[34:35], v[80:81], v[118:119] op_sel_hi:[0,1,1] neg_lo:[1,0,0] neg_hi:[1,0,0]
	v_pk_fma_f32 v[116:117], v[34:35], v[82:83], v[120:121] op_sel_hi:[0,1,1] neg_lo:[1,0,0] neg_hi:[1,0,0]
	v_pk_fma_f32 v[118:119], v[34:35], v[84:85], v[122:123] op_sel_hi:[0,1,1] neg_lo:[1,0,0] neg_hi:[1,0,0]
	v_pk_fma_f32 v[120:121], v[34:35], v[86:87], v[124:125] op_sel_hi:[0,1,1] neg_lo:[1,0,0] neg_hi:[1,0,0]
	v_pk_fma_f32 v[122:123], v[34:35], v[88:89], v[126:127] op_sel_hi:[0,1,1] neg_lo:[1,0,0] neg_hi:[1,0,0]
	v_pk_fma_f32 v[124:125], v[34:35], v[90:91], v[128:129] op_sel_hi:[0,1,1] neg_lo:[1,0,0] neg_hi:[1,0,0]
	v_pk_fma_f32 v[126:127], v[34:35], v[92:93], v[130:131] op_sel_hi:[0,1,1] neg_lo:[1,0,0] neg_hi:[1,0,0]
	v_pk_fma_f32 v[128:129], v[34:35], v[94:95], v[132:133] op_sel_hi:[0,1,1] neg_lo:[1,0,0] neg_hi:[1,0,0]
	v_pk_fma_f32 v[130:131], v[34:35], v[96:97], v[134:135] op_sel_hi:[0,1,1] neg_lo:[1,0,0] neg_hi:[1,0,0]
	v_pk_fma_f32 v[102:103], v[34:35], v[98:99], v[102:103] op_sel_hi:[0,1,1] neg_lo:[1,0,0] neg_hi:[1,0,0]
	v_fma_f32 v104, -v34, v100, v104
	v_fma_f32 v4, -v34, v101, v4
	ds_read_b128 v[70:73], v21 offset:9104
	ds_read_b128 v[74:77], v21 offset:9120
	ds_read_b128 v[78:81], v21 offset:9136
	ds_read_b128 v[82:85], v21 offset:9152
	ds_read_b128 v[86:89], v21 offset:9168
	ds_read_b128 v[90:93], v21 offset:9184
	ds_read_b128 v[94:97], v21 offset:9200
	ds_read_b128 v[98:101], v21 offset:9216
	s_waitcnt lgkmcnt(0)
	v_fma_f32 v38, -v5, v38, v5
	v_fma_f32 v39, -v5, v39, v105
	v_mov_b32_e32 v202, v5
	v_pk_fma_f32 v[40:41], v[202:203], v[40:41], v[106:107] op_sel_hi:[0,1,1] neg_lo:[1,0,0] neg_hi:[1,0,0]
	v_pk_fma_f32 v[106:107], v[202:203], v[42:43], v[108:109] op_sel_hi:[0,1,1] neg_lo:[1,0,0] neg_hi:[1,0,0]
	v_pk_fma_f32 v[108:109], v[202:203], v[44:45], v[110:111] op_sel_hi:[0,1,1] neg_lo:[1,0,0] neg_hi:[1,0,0]
	v_pk_fma_f32 v[110:111], v[202:203], v[46:47], v[112:113] op_sel_hi:[0,1,1] neg_lo:[1,0,0] neg_hi:[1,0,0]
	v_pk_fma_f32 v[112:113], v[202:203], v[48:49], v[114:115] op_sel_hi:[0,1,1] neg_lo:[1,0,0] neg_hi:[1,0,0]
	v_pk_fma_f32 v[114:115], v[202:203], v[50:51], v[116:117] op_sel_hi:[0,1,1] neg_lo:[1,0,0] neg_hi:[1,0,0]
	v_pk_fma_f32 v[116:117], v[202:203], v[52:53], v[118:119] op_sel_hi:[0,1,1] neg_lo:[1,0,0] neg_hi:[1,0,0]
	v_pk_fma_f32 v[118:119], v[202:203], v[54:55], v[120:121] op_sel_hi:[0,1,1] neg_lo:[1,0,0] neg_hi:[1,0,0]
	v_pk_fma_f32 v[120:121], v[202:203], v[56:57], v[122:123] op_sel_hi:[0,1,1] neg_lo:[1,0,0] neg_hi:[1,0,0]
	v_pk_fma_f32 v[122:123], v[202:203], v[58:59], v[124:125] op_sel_hi:[0,1,1] neg_lo:[1,0,0] neg_hi:[1,0,0]
	v_pk_fma_f32 v[124:125], v[202:203], v[60:61], v[126:127] op_sel_hi:[0,1,1] neg_lo:[1,0,0] neg_hi:[1,0,0]
	v_pk_fma_f32 v[126:127], v[202:203], v[62:63], v[128:129] op_sel_hi:[0,1,1] neg_lo:[1,0,0] neg_hi:[1,0,0]
	v_pk_fma_f32 v[128:129], v[202:203], v[64:65], v[130:131] op_sel_hi:[0,1,1] neg_lo:[1,0,0] neg_hi:[1,0,0]
	v_pk_fma_f32 v[130:131], v[202:203], v[66:67], v[102:103] op_sel_hi:[0,1,1] neg_lo:[1,0,0] neg_hi:[1,0,0]
	v_fma_f32 v132, -v5, v68, v104
	v_fma_f32 v4, -v5, v69, v4
	ds_read_b128 v[42:45], v21 offset:9376
	ds_read_b128 v[46:49], v21 offset:9392
	ds_read_b128 v[50:53], v21 offset:9408
	ds_read_b128 v[54:57], v21 offset:9424
	ds_read_b128 v[58:61], v21 offset:9440
	ds_read_b128 v[62:65], v21 offset:9456
	ds_read_b128 v[66:69], v21 offset:9472
	ds_read_b128 v[102:105], v21 offset:9488
	v_fma_f32 v5, -v39, v70, v38
	v_fma_f32 v38, -v39, v71, v39
	v_fma_f32 v133, -v39, v72, v40
	v_fma_f32 v134, -v39, v73, v41
	v_mov_b32_e32 v202, v39
	v_pk_fma_f32 v[106:107], v[202:203], v[74:75], v[106:107] op_sel_hi:[0,1,1] neg_lo:[1,0,0] neg_hi:[1,0,0]
	v_pk_fma_f32 v[108:109], v[202:203], v[76:77], v[108:109] op_sel_hi:[0,1,1] neg_lo:[1,0,0] neg_hi:[1,0,0]
	v_pk_fma_f32 v[110:111], v[202:203], v[78:79], v[110:111] op_sel_hi:[0,1,1] neg_lo:[1,0,0] neg_hi:[1,0,0]
	v_pk_fma_f32 v[112:113], v[202:203], v[80:81], v[112:113] op_sel_hi:[0,1,1] neg_lo:[1,0,0] neg_hi:[1,0,0]
	v_pk_fma_f32 v[114:115], v[202:203], v[82:83], v[114:115] op_sel_hi:[0,1,1] neg_lo:[1,0,0] neg_hi:[1,0,0]
	v_pk_fma_f32 v[116:117], v[202:203], v[84:85], v[116:117] op_sel_hi:[0,1,1] neg_lo:[1,0,0] neg_hi:[1,0,0]
	v_pk_fma_f32 v[118:119], v[202:203], v[86:87], v[118:119] op_sel_hi:[0,1,1] neg_lo:[1,0,0] neg_hi:[1,0,0]
	v_pk_fma_f32 v[120:121], v[202:203], v[88:89], v[120:121] op_sel_hi:[0,1,1] neg_lo:[1,0,0] neg_hi:[1,0,0]
	v_pk_fma_f32 v[122:123], v[202:203], v[90:91], v[122:123] op_sel_hi:[0,1,1] neg_lo:[1,0,0] neg_hi:[1,0,0]
	v_pk_fma_f32 v[124:125], v[202:203], v[92:93], v[124:125] op_sel_hi:[0,1,1] neg_lo:[1,0,0] neg_hi:[1,0,0]
	v_pk_fma_f32 v[126:127], v[202:203], v[94:95], v[126:127] op_sel_hi:[0,1,1] neg_lo:[1,0,0] neg_hi:[1,0,0]
	v_pk_fma_f32 v[128:129], v[202:203], v[96:97], v[128:129] op_sel_hi:[0,1,1] neg_lo:[1,0,0] neg_hi:[1,0,0]
	v_pk_fma_f32 v[98:99], v[202:203], v[98:99], v[130:131] op_sel_hi:[0,1,1] neg_lo:[1,0,0] neg_hi:[1,0,0]
	v_fma_f32 v100, -v39, v100, v132
	v_fma_f32 v4, -v39, v101, v4
	ds_read_b128 v[70:73], v21 offset:9664
	ds_read_b128 v[74:77], v21 offset:9680
	ds_read_b128 v[78:81], v21 offset:9696
	ds_read_b128 v[82:85], v21 offset:9712
	ds_read_b128 v[86:89], v21 offset:9728
	ds_read_b128 v[90:93], v21 offset:9744
	ds_read_b128 v[94:97], v21 offset:9760
	s_waitcnt lgkmcnt(0)
	v_fma_f32 v41, -v133, v42, v5
	v_fma_f32 v40, -v133, v43, v38
	v_fma_f32 v39, -v133, v44, v133
	v_fma_f32 v38, -v133, v45, v134
	v_fma_f32 v5, -v133, v46, v106
	v_fma_f32 v101, -v133, v47, v107
	v_mov_b32_e32 v202, v133
	v_pk_fma_f32 v[106:107], v[202:203], v[48:49], v[108:109] op_sel_hi:[0,1,1] neg_lo:[1,0,0] neg_hi:[1,0,0]
	v_pk_fma_f32 v[108:109], v[202:203], v[50:51], v[110:111] op_sel_hi:[0,1,1] neg_lo:[1,0,0] neg_hi:[1,0,0]
	v_pk_fma_f32 v[110:111], v[202:203], v[52:53], v[112:113] op_sel_hi:[0,1,1] neg_lo:[1,0,0] neg_hi:[1,0,0]
	v_pk_fma_f32 v[112:113], v[202:203], v[54:55], v[114:115] op_sel_hi:[0,1,1] neg_lo:[1,0,0] neg_hi:[1,0,0]
	v_pk_fma_f32 v[114:115], v[202:203], v[56:57], v[116:117] op_sel_hi:[0,1,1] neg_lo:[1,0,0] neg_hi:[1,0,0]
	v_pk_fma_f32 v[116:117], v[202:203], v[58:59], v[118:119] op_sel_hi:[0,1,1] neg_lo:[1,0,0] neg_hi:[1,0,0]
	v_pk_fma_f32 v[118:119], v[202:203], v[60:61], v[120:121] op_sel_hi:[0,1,1] neg_lo:[1,0,0] neg_hi:[1,0,0]
	v_pk_fma_f32 v[120:121], v[202:203], v[62:63], v[122:123] op_sel_hi:[0,1,1] neg_lo:[1,0,0] neg_hi:[1,0,0]
	v_pk_fma_f32 v[122:123], v[202:203], v[64:65], v[124:125] op_sel_hi:[0,1,1] neg_lo:[1,0,0] neg_hi:[1,0,0]
	v_pk_fma_f32 v[124:125], v[202:203], v[66:67], v[126:127] op_sel_hi:[0,1,1] neg_lo:[1,0,0] neg_hi:[1,0,0]
	v_pk_fma_f32 v[126:127], v[202:203], v[68:69], v[128:129] op_sel_hi:[0,1,1] neg_lo:[1,0,0] neg_hi:[1,0,0]
	v_pk_fma_f32 v[98:99], v[202:203], v[102:103], v[98:99] op_sel_hi:[0,1,1] neg_lo:[1,0,0] neg_hi:[1,0,0]
	v_fma_f32 v100, -v133, v104, v100
	v_fma_f32 v4, -v133, v105, v4
	ds_read_b128 v[42:45], v21 offset:9936
	ds_read_b128 v[46:49], v21 offset:9952
	ds_read_b128 v[50:53], v21 offset:9968
	ds_read_b128 v[54:57], v21 offset:9984
	ds_read_b128 v[58:61], v21 offset:10000
	ds_read_b128 v[62:65], v21 offset:10016
	ds_read_b128 v[66:69], v21 offset:10032
	v_fma_f32 v5, -v38, v70, v5
	v_fma_f32 v101, -v38, v71, v101
	v_pk_fma_f32 v[102:103], v[38:39], v[72:73], v[106:107] op_sel_hi:[0,1,1] neg_lo:[1,0,0] neg_hi:[1,0,0]
	v_pk_fma_f32 v[104:105], v[38:39], v[74:75], v[108:109] op_sel_hi:[0,1,1] neg_lo:[1,0,0] neg_hi:[1,0,0]
	v_pk_fma_f32 v[106:107], v[38:39], v[76:77], v[110:111] op_sel_hi:[0,1,1] neg_lo:[1,0,0] neg_hi:[1,0,0]
	v_pk_fma_f32 v[108:109], v[38:39], v[78:79], v[112:113] op_sel_hi:[0,1,1] neg_lo:[1,0,0] neg_hi:[1,0,0]
	v_pk_fma_f32 v[110:111], v[38:39], v[80:81], v[114:115] op_sel_hi:[0,1,1] neg_lo:[1,0,0] neg_hi:[1,0,0]
	v_pk_fma_f32 v[112:113], v[38:39], v[82:83], v[116:117] op_sel_hi:[0,1,1] neg_lo:[1,0,0] neg_hi:[1,0,0]
	v_pk_fma_f32 v[114:115], v[38:39], v[84:85], v[118:119] op_sel_hi:[0,1,1] neg_lo:[1,0,0] neg_hi:[1,0,0]
	v_pk_fma_f32 v[116:117], v[38:39], v[86:87], v[120:121] op_sel_hi:[0,1,1] neg_lo:[1,0,0] neg_hi:[1,0,0]
	v_pk_fma_f32 v[118:119], v[38:39], v[88:89], v[122:123] op_sel_hi:[0,1,1] neg_lo:[1,0,0] neg_hi:[1,0,0]
	v_pk_fma_f32 v[120:121], v[38:39], v[90:91], v[124:125] op_sel_hi:[0,1,1] neg_lo:[1,0,0] neg_hi:[1,0,0]
	v_pk_fma_f32 v[122:123], v[38:39], v[92:93], v[126:127] op_sel_hi:[0,1,1] neg_lo:[1,0,0] neg_hi:[1,0,0]
	v_pk_fma_f32 v[98:99], v[38:39], v[94:95], v[98:99] op_sel_hi:[0,1,1] neg_lo:[1,0,0] neg_hi:[1,0,0]
	v_fma_f32 v100, -v38, v96, v100
	v_fma_f32 v4, -v38, v97, v4
	ds_read_b128 v[70:73], v21 offset:10208
	ds_read_b128 v[74:77], v21 offset:10224
	ds_read_b128 v[78:81], v21 offset:10240
	ds_read_b128 v[82:85], v21 offset:10256
	ds_read_b128 v[86:89], v21 offset:10272
	ds_read_b128 v[90:93], v21 offset:10288
	ds_read_b128 v[94:97], v21 offset:10304
	s_waitcnt lgkmcnt(0)
	v_fma_f32 v42, -v5, v42, v5
	v_fma_f32 v43, -v5, v43, v101
	v_mov_b32_e32 v202, v5
	v_pk_fma_f32 v[44:45], v[202:203], v[44:45], v[102:103] op_sel_hi:[0,1,1] neg_lo:[1,0,0] neg_hi:[1,0,0]
	v_pk_fma_f32 v[102:103], v[202:203], v[46:47], v[104:105] op_sel_hi:[0,1,1] neg_lo:[1,0,0] neg_hi:[1,0,0]
	v_pk_fma_f32 v[104:105], v[202:203], v[48:49], v[106:107] op_sel_hi:[0,1,1] neg_lo:[1,0,0] neg_hi:[1,0,0]
	v_pk_fma_f32 v[106:107], v[202:203], v[50:51], v[108:109] op_sel_hi:[0,1,1] neg_lo:[1,0,0] neg_hi:[1,0,0]
	v_pk_fma_f32 v[108:109], v[202:203], v[52:53], v[110:111] op_sel_hi:[0,1,1] neg_lo:[1,0,0] neg_hi:[1,0,0]
	v_pk_fma_f32 v[110:111], v[202:203], v[54:55], v[112:113] op_sel_hi:[0,1,1] neg_lo:[1,0,0] neg_hi:[1,0,0]
	v_pk_fma_f32 v[112:113], v[202:203], v[56:57], v[114:115] op_sel_hi:[0,1,1] neg_lo:[1,0,0] neg_hi:[1,0,0]
	v_pk_fma_f32 v[114:115], v[202:203], v[58:59], v[116:117] op_sel_hi:[0,1,1] neg_lo:[1,0,0] neg_hi:[1,0,0]
	v_pk_fma_f32 v[116:117], v[202:203], v[60:61], v[118:119] op_sel_hi:[0,1,1] neg_lo:[1,0,0] neg_hi:[1,0,0]
	v_pk_fma_f32 v[118:119], v[202:203], v[62:63], v[120:121] op_sel_hi:[0,1,1] neg_lo:[1,0,0] neg_hi:[1,0,0]
	v_pk_fma_f32 v[120:121], v[202:203], v[64:65], v[122:123] op_sel_hi:[0,1,1] neg_lo:[1,0,0] neg_hi:[1,0,0]
	v_pk_fma_f32 v[122:123], v[202:203], v[66:67], v[98:99] op_sel_hi:[0,1,1] neg_lo:[1,0,0] neg_hi:[1,0,0]
	v_fma_f32 v124, -v5, v68, v100
	v_fma_f32 v4, -v5, v69, v4
	ds_read_b128 v[46:49], v21 offset:10480
	ds_read_b128 v[50:53], v21 offset:10496
	ds_read_b128 v[54:57], v21 offset:10512
	ds_read_b128 v[58:61], v21 offset:10528
	ds_read_b128 v[62:65], v21 offset:10544
	ds_read_b128 v[66:69], v21 offset:10560
	ds_read_b128 v[98:101], v21 offset:10576
	v_fma_f32 v5, -v43, v70, v42
	v_fma_f32 v42, -v43, v71, v43
	v_fma_f32 v125, -v43, v72, v44
	v_fma_f32 v126, -v43, v73, v45
	v_mov_b32_e32 v202, v43
	v_pk_fma_f32 v[102:103], v[202:203], v[74:75], v[102:103] op_sel_hi:[0,1,1] neg_lo:[1,0,0] neg_hi:[1,0,0]
	v_pk_fma_f32 v[104:105], v[202:203], v[76:77], v[104:105] op_sel_hi:[0,1,1] neg_lo:[1,0,0] neg_hi:[1,0,0]
	v_pk_fma_f32 v[106:107], v[202:203], v[78:79], v[106:107] op_sel_hi:[0,1,1] neg_lo:[1,0,0] neg_hi:[1,0,0]
	v_pk_fma_f32 v[108:109], v[202:203], v[80:81], v[108:109] op_sel_hi:[0,1,1] neg_lo:[1,0,0] neg_hi:[1,0,0]
	v_pk_fma_f32 v[110:111], v[202:203], v[82:83], v[110:111] op_sel_hi:[0,1,1] neg_lo:[1,0,0] neg_hi:[1,0,0]
	v_pk_fma_f32 v[112:113], v[202:203], v[84:85], v[112:113] op_sel_hi:[0,1,1] neg_lo:[1,0,0] neg_hi:[1,0,0]
	v_pk_fma_f32 v[114:115], v[202:203], v[86:87], v[114:115] op_sel_hi:[0,1,1] neg_lo:[1,0,0] neg_hi:[1,0,0]
	v_pk_fma_f32 v[116:117], v[202:203], v[88:89], v[116:117] op_sel_hi:[0,1,1] neg_lo:[1,0,0] neg_hi:[1,0,0]
	v_pk_fma_f32 v[118:119], v[202:203], v[90:91], v[118:119] op_sel_hi:[0,1,1] neg_lo:[1,0,0] neg_hi:[1,0,0]
	v_pk_fma_f32 v[120:121], v[202:203], v[92:93], v[120:121] op_sel_hi:[0,1,1] neg_lo:[1,0,0] neg_hi:[1,0,0]
	v_pk_fma_f32 v[94:95], v[202:203], v[94:95], v[122:123] op_sel_hi:[0,1,1] neg_lo:[1,0,0] neg_hi:[1,0,0]
	v_fma_f32 v96, -v43, v96, v124
	v_fma_f32 v4, -v43, v97, v4
	ds_read_b128 v[70:73], v21 offset:10768
	ds_read_b128 v[74:77], v21 offset:10784
	ds_read_b128 v[78:81], v21 offset:10800
	ds_read_b128 v[82:85], v21 offset:10816
	ds_read_b128 v[86:89], v21 offset:10832
	ds_read_b128 v[90:93], v21 offset:10848
	s_waitcnt lgkmcnt(0)
	v_fma_f32 v45, -v125, v46, v5
	v_fma_f32 v44, -v125, v47, v42
	v_fma_f32 v43, -v125, v48, v125
	v_fma_f32 v42, -v125, v49, v126
	v_fma_f32 v5, -v125, v50, v102
	v_fma_f32 v97, -v125, v51, v103
	v_mov_b32_e32 v202, v125
	v_pk_fma_f32 v[102:103], v[202:203], v[52:53], v[104:105] op_sel_hi:[0,1,1] neg_lo:[1,0,0] neg_hi:[1,0,0]
	v_pk_fma_f32 v[104:105], v[202:203], v[54:55], v[106:107] op_sel_hi:[0,1,1] neg_lo:[1,0,0] neg_hi:[1,0,0]
	v_pk_fma_f32 v[106:107], v[202:203], v[56:57], v[108:109] op_sel_hi:[0,1,1] neg_lo:[1,0,0] neg_hi:[1,0,0]
	v_pk_fma_f32 v[108:109], v[202:203], v[58:59], v[110:111] op_sel_hi:[0,1,1] neg_lo:[1,0,0] neg_hi:[1,0,0]
	v_pk_fma_f32 v[110:111], v[202:203], v[60:61], v[112:113] op_sel_hi:[0,1,1] neg_lo:[1,0,0] neg_hi:[1,0,0]
	v_pk_fma_f32 v[112:113], v[202:203], v[62:63], v[114:115] op_sel_hi:[0,1,1] neg_lo:[1,0,0] neg_hi:[1,0,0]
	v_pk_fma_f32 v[114:115], v[202:203], v[64:65], v[116:117] op_sel_hi:[0,1,1] neg_lo:[1,0,0] neg_hi:[1,0,0]
	v_pk_fma_f32 v[116:117], v[202:203], v[66:67], v[118:119] op_sel_hi:[0,1,1] neg_lo:[1,0,0] neg_hi:[1,0,0]
	v_pk_fma_f32 v[118:119], v[202:203], v[68:69], v[120:121] op_sel_hi:[0,1,1] neg_lo:[1,0,0] neg_hi:[1,0,0]
	v_pk_fma_f32 v[94:95], v[202:203], v[98:99], v[94:95] op_sel_hi:[0,1,1] neg_lo:[1,0,0] neg_hi:[1,0,0]
	v_fma_f32 v96, -v125, v100, v96
	v_fma_f32 v4, -v125, v101, v4
	ds_read_b128 v[46:49], v21 offset:11040
	ds_read_b128 v[50:53], v21 offset:11056
	ds_read_b128 v[54:57], v21 offset:11072
	ds_read_b128 v[58:61], v21 offset:11088
	ds_read_b128 v[62:65], v21 offset:11104
	ds_read_b128 v[66:69], v21 offset:11120
	v_fma_f32 v5, -v42, v70, v5
	v_fma_f32 v97, -v42, v71, v97
	v_pk_fma_f32 v[98:99], v[42:43], v[72:73], v[102:103] op_sel_hi:[0,1,1] neg_lo:[1,0,0] neg_hi:[1,0,0]
	v_pk_fma_f32 v[100:101], v[42:43], v[74:75], v[104:105] op_sel_hi:[0,1,1] neg_lo:[1,0,0] neg_hi:[1,0,0]
	v_pk_fma_f32 v[102:103], v[42:43], v[76:77], v[106:107] op_sel_hi:[0,1,1] neg_lo:[1,0,0] neg_hi:[1,0,0]
	v_pk_fma_f32 v[104:105], v[42:43], v[78:79], v[108:109] op_sel_hi:[0,1,1] neg_lo:[1,0,0] neg_hi:[1,0,0]
	v_pk_fma_f32 v[106:107], v[42:43], v[80:81], v[110:111] op_sel_hi:[0,1,1] neg_lo:[1,0,0] neg_hi:[1,0,0]
	v_pk_fma_f32 v[108:109], v[42:43], v[82:83], v[112:113] op_sel_hi:[0,1,1] neg_lo:[1,0,0] neg_hi:[1,0,0]
	v_pk_fma_f32 v[110:111], v[42:43], v[84:85], v[114:115] op_sel_hi:[0,1,1] neg_lo:[1,0,0] neg_hi:[1,0,0]
	v_pk_fma_f32 v[112:113], v[42:43], v[86:87], v[116:117] op_sel_hi:[0,1,1] neg_lo:[1,0,0] neg_hi:[1,0,0]
	v_pk_fma_f32 v[114:115], v[42:43], v[88:89], v[118:119] op_sel_hi:[0,1,1] neg_lo:[1,0,0] neg_hi:[1,0,0]
	v_pk_fma_f32 v[94:95], v[42:43], v[90:91], v[94:95] op_sel_hi:[0,1,1] neg_lo:[1,0,0] neg_hi:[1,0,0]
	v_fma_f32 v96, -v42, v92, v96
	v_fma_f32 v4, -v42, v93, v4
	ds_read_b128 v[70:73], v21 offset:11312
	ds_read_b128 v[74:77], v21 offset:11328
	ds_read_b128 v[78:81], v21 offset:11344
	ds_read_b128 v[82:85], v21 offset:11360
	ds_read_b128 v[86:89], v21 offset:11376
	ds_read_b128 v[90:93], v21 offset:11392
	s_waitcnt lgkmcnt(0)
	v_fma_f32 v46, -v5, v46, v5
	v_fma_f32 v47, -v5, v47, v97
	v_mov_b32_e32 v202, v5
	v_pk_fma_f32 v[48:49], v[202:203], v[48:49], v[98:99] op_sel_hi:[0,1,1] neg_lo:[1,0,0] neg_hi:[1,0,0]
	v_pk_fma_f32 v[98:99], v[202:203], v[50:51], v[100:101] op_sel_hi:[0,1,1] neg_lo:[1,0,0] neg_hi:[1,0,0]
	v_pk_fma_f32 v[100:101], v[202:203], v[52:53], v[102:103] op_sel_hi:[0,1,1] neg_lo:[1,0,0] neg_hi:[1,0,0]
	v_pk_fma_f32 v[102:103], v[202:203], v[54:55], v[104:105] op_sel_hi:[0,1,1] neg_lo:[1,0,0] neg_hi:[1,0,0]
	v_pk_fma_f32 v[104:105], v[202:203], v[56:57], v[106:107] op_sel_hi:[0,1,1] neg_lo:[1,0,0] neg_hi:[1,0,0]
	v_pk_fma_f32 v[106:107], v[202:203], v[58:59], v[108:109] op_sel_hi:[0,1,1] neg_lo:[1,0,0] neg_hi:[1,0,0]
	v_pk_fma_f32 v[108:109], v[202:203], v[60:61], v[110:111] op_sel_hi:[0,1,1] neg_lo:[1,0,0] neg_hi:[1,0,0]
	v_pk_fma_f32 v[110:111], v[202:203], v[62:63], v[112:113] op_sel_hi:[0,1,1] neg_lo:[1,0,0] neg_hi:[1,0,0]
	v_pk_fma_f32 v[112:113], v[202:203], v[64:65], v[114:115] op_sel_hi:[0,1,1] neg_lo:[1,0,0] neg_hi:[1,0,0]
	v_pk_fma_f32 v[114:115], v[202:203], v[66:67], v[94:95] op_sel_hi:[0,1,1] neg_lo:[1,0,0] neg_hi:[1,0,0]
	v_fma_f32 v116, -v5, v68, v96
	v_fma_f32 v4, -v5, v69, v4
	ds_read_b128 v[50:53], v21 offset:11584
	ds_read_b128 v[54:57], v21 offset:11600
	ds_read_b128 v[58:61], v21 offset:11616
	ds_read_b128 v[62:65], v21 offset:11632
	ds_read_b128 v[66:69], v21 offset:11648
	ds_read_b128 v[94:97], v21 offset:11664
	v_fma_f32 v5, -v47, v70, v46
	v_fma_f32 v46, -v47, v71, v47
	v_fma_f32 v117, -v47, v72, v48
	v_fma_f32 v118, -v47, v73, v49
	v_mov_b32_e32 v202, v47
	v_pk_fma_f32 v[98:99], v[202:203], v[74:75], v[98:99] op_sel_hi:[0,1,1] neg_lo:[1,0,0] neg_hi:[1,0,0]
	v_pk_fma_f32 v[100:101], v[202:203], v[76:77], v[100:101] op_sel_hi:[0,1,1] neg_lo:[1,0,0] neg_hi:[1,0,0]
	v_pk_fma_f32 v[102:103], v[202:203], v[78:79], v[102:103] op_sel_hi:[0,1,1] neg_lo:[1,0,0] neg_hi:[1,0,0]
	v_pk_fma_f32 v[104:105], v[202:203], v[80:81], v[104:105] op_sel_hi:[0,1,1] neg_lo:[1,0,0] neg_hi:[1,0,0]
	v_pk_fma_f32 v[106:107], v[202:203], v[82:83], v[106:107] op_sel_hi:[0,1,1] neg_lo:[1,0,0] neg_hi:[1,0,0]
	v_pk_fma_f32 v[108:109], v[202:203], v[84:85], v[108:109] op_sel_hi:[0,1,1] neg_lo:[1,0,0] neg_hi:[1,0,0]
	v_pk_fma_f32 v[110:111], v[202:203], v[86:87], v[110:111] op_sel_hi:[0,1,1] neg_lo:[1,0,0] neg_hi:[1,0,0]
	v_pk_fma_f32 v[112:113], v[202:203], v[88:89], v[112:113] op_sel_hi:[0,1,1] neg_lo:[1,0,0] neg_hi:[1,0,0]
	v_pk_fma_f32 v[90:91], v[202:203], v[90:91], v[114:115] op_sel_hi:[0,1,1] neg_lo:[1,0,0] neg_hi:[1,0,0]
	v_fma_f32 v92, -v47, v92, v116
	v_fma_f32 v4, -v47, v93, v4
	ds_read_b128 v[70:73], v21 offset:11872
	ds_read_b128 v[74:77], v21 offset:11888
	ds_read_b128 v[78:81], v21 offset:11904
	ds_read_b128 v[82:85], v21 offset:11920
	ds_read_b128 v[86:89], v21 offset:11936
	s_waitcnt lgkmcnt(0)
	v_fma_f32 v49, -v117, v50, v5
	v_fma_f32 v48, -v117, v51, v46
	v_fma_f32 v47, -v117, v52, v117
	v_fma_f32 v46, -v117, v53, v118
	v_fma_f32 v5, -v117, v54, v98
	v_fma_f32 v93, -v117, v55, v99
	v_mov_b32_e32 v202, v117
	v_pk_fma_f32 v[98:99], v[202:203], v[56:57], v[100:101] op_sel_hi:[0,1,1] neg_lo:[1,0,0] neg_hi:[1,0,0]
	v_pk_fma_f32 v[100:101], v[202:203], v[58:59], v[102:103] op_sel_hi:[0,1,1] neg_lo:[1,0,0] neg_hi:[1,0,0]
	v_pk_fma_f32 v[102:103], v[202:203], v[60:61], v[104:105] op_sel_hi:[0,1,1] neg_lo:[1,0,0] neg_hi:[1,0,0]
	v_pk_fma_f32 v[104:105], v[202:203], v[62:63], v[106:107] op_sel_hi:[0,1,1] neg_lo:[1,0,0] neg_hi:[1,0,0]
	v_pk_fma_f32 v[106:107], v[202:203], v[64:65], v[108:109] op_sel_hi:[0,1,1] neg_lo:[1,0,0] neg_hi:[1,0,0]
	v_pk_fma_f32 v[108:109], v[202:203], v[66:67], v[110:111] op_sel_hi:[0,1,1] neg_lo:[1,0,0] neg_hi:[1,0,0]
	v_pk_fma_f32 v[110:111], v[202:203], v[68:69], v[112:113] op_sel_hi:[0,1,1] neg_lo:[1,0,0] neg_hi:[1,0,0]
	v_pk_fma_f32 v[90:91], v[202:203], v[94:95], v[90:91] op_sel_hi:[0,1,1] neg_lo:[1,0,0] neg_hi:[1,0,0]
	v_fma_f32 v92, -v117, v96, v92
	v_fma_f32 v4, -v117, v97, v4
	ds_read_b128 v[50:53], v21 offset:12144
	ds_read_b128 v[54:57], v21 offset:12160
	ds_read_b128 v[58:61], v21 offset:12176
	ds_read_b128 v[62:65], v21 offset:12192
	ds_read_b128 v[66:69], v21 offset:12208
	v_fma_f32 v5, -v46, v70, v5
	v_fma_f32 v93, -v46, v71, v93
	v_pk_fma_f32 v[94:95], v[46:47], v[72:73], v[98:99] op_sel_hi:[0,1,1] neg_lo:[1,0,0] neg_hi:[1,0,0]
	v_pk_fma_f32 v[96:97], v[46:47], v[74:75], v[100:101] op_sel_hi:[0,1,1] neg_lo:[1,0,0] neg_hi:[1,0,0]
	v_pk_fma_f32 v[98:99], v[46:47], v[76:77], v[102:103] op_sel_hi:[0,1,1] neg_lo:[1,0,0] neg_hi:[1,0,0]
	v_pk_fma_f32 v[100:101], v[46:47], v[78:79], v[104:105] op_sel_hi:[0,1,1] neg_lo:[1,0,0] neg_hi:[1,0,0]
	v_pk_fma_f32 v[102:103], v[46:47], v[80:81], v[106:107] op_sel_hi:[0,1,1] neg_lo:[1,0,0] neg_hi:[1,0,0]
	v_pk_fma_f32 v[104:105], v[46:47], v[82:83], v[108:109] op_sel_hi:[0,1,1] neg_lo:[1,0,0] neg_hi:[1,0,0]
	v_pk_fma_f32 v[106:107], v[46:47], v[84:85], v[110:111] op_sel_hi:[0,1,1] neg_lo:[1,0,0] neg_hi:[1,0,0]
	v_pk_fma_f32 v[90:91], v[46:47], v[86:87], v[90:91] op_sel_hi:[0,1,1] neg_lo:[1,0,0] neg_hi:[1,0,0]
	v_fma_f32 v92, -v46, v88, v92
	v_fma_f32 v4, -v46, v89, v4
	ds_read_b128 v[70:73], v21 offset:12416
	ds_read_b128 v[74:77], v21 offset:12432
	ds_read_b128 v[78:81], v21 offset:12448
	ds_read_b128 v[82:85], v21 offset:12464
	ds_read_b128 v[86:89], v21 offset:12480
	s_waitcnt lgkmcnt(0)
	v_fma_f32 v50, -v5, v50, v5
	v_fma_f32 v51, -v5, v51, v93
	v_mov_b32_e32 v202, v5
	v_pk_fma_f32 v[52:53], v[202:203], v[52:53], v[94:95] op_sel_hi:[0,1,1] neg_lo:[1,0,0] neg_hi:[1,0,0]
	v_pk_fma_f32 v[94:95], v[202:203], v[54:55], v[96:97] op_sel_hi:[0,1,1] neg_lo:[1,0,0] neg_hi:[1,0,0]
	v_pk_fma_f32 v[96:97], v[202:203], v[56:57], v[98:99] op_sel_hi:[0,1,1] neg_lo:[1,0,0] neg_hi:[1,0,0]
	v_pk_fma_f32 v[98:99], v[202:203], v[58:59], v[100:101] op_sel_hi:[0,1,1] neg_lo:[1,0,0] neg_hi:[1,0,0]
	v_pk_fma_f32 v[100:101], v[202:203], v[60:61], v[102:103] op_sel_hi:[0,1,1] neg_lo:[1,0,0] neg_hi:[1,0,0]
	v_pk_fma_f32 v[102:103], v[202:203], v[62:63], v[104:105] op_sel_hi:[0,1,1] neg_lo:[1,0,0] neg_hi:[1,0,0]
	v_pk_fma_f32 v[104:105], v[202:203], v[64:65], v[106:107] op_sel_hi:[0,1,1] neg_lo:[1,0,0] neg_hi:[1,0,0]
	v_pk_fma_f32 v[106:107], v[202:203], v[66:67], v[90:91] op_sel_hi:[0,1,1] neg_lo:[1,0,0] neg_hi:[1,0,0]
	v_fma_f32 v108, -v5, v68, v92
	v_fma_f32 v4, -v5, v69, v4
	ds_read_b128 v[54:57], v21 offset:12688
	ds_read_b128 v[58:61], v21 offset:12704
	ds_read_b128 v[62:65], v21 offset:12720
	ds_read_b128 v[66:69], v21 offset:12736
	ds_read_b128 v[90:93], v21 offset:12752
	v_fma_f32 v5, -v51, v70, v50
	v_fma_f32 v50, -v51, v71, v51
	v_fma_f32 v109, -v51, v72, v52
	v_fma_f32 v110, -v51, v73, v53
	v_mov_b32_e32 v202, v51
	v_pk_fma_f32 v[94:95], v[202:203], v[74:75], v[94:95] op_sel_hi:[0,1,1] neg_lo:[1,0,0] neg_hi:[1,0,0]
	v_pk_fma_f32 v[96:97], v[202:203], v[76:77], v[96:97] op_sel_hi:[0,1,1] neg_lo:[1,0,0] neg_hi:[1,0,0]
	v_pk_fma_f32 v[98:99], v[202:203], v[78:79], v[98:99] op_sel_hi:[0,1,1] neg_lo:[1,0,0] neg_hi:[1,0,0]
	v_pk_fma_f32 v[100:101], v[202:203], v[80:81], v[100:101] op_sel_hi:[0,1,1] neg_lo:[1,0,0] neg_hi:[1,0,0]
	v_pk_fma_f32 v[102:103], v[202:203], v[82:83], v[102:103] op_sel_hi:[0,1,1] neg_lo:[1,0,0] neg_hi:[1,0,0]
	v_pk_fma_f32 v[104:105], v[202:203], v[84:85], v[104:105] op_sel_hi:[0,1,1] neg_lo:[1,0,0] neg_hi:[1,0,0]
	v_pk_fma_f32 v[86:87], v[202:203], v[86:87], v[106:107] op_sel_hi:[0,1,1] neg_lo:[1,0,0] neg_hi:[1,0,0]
	v_fma_f32 v88, -v51, v88, v108
	v_fma_f32 v4, -v51, v89, v4
	ds_read_b128 v[70:73], v21 offset:12976
	ds_read_b128 v[74:77], v21 offset:12992
	ds_read_b128 v[78:81], v21 offset:13008
	ds_read_b128 v[82:85], v21 offset:13024
	s_waitcnt lgkmcnt(0)
	v_fma_f32 v53, -v109, v54, v5
	v_fma_f32 v52, -v109, v55, v50
	v_fma_f32 v51, -v109, v56, v109
	v_fma_f32 v50, -v109, v57, v110
	v_fma_f32 v5, -v109, v58, v94
	v_fma_f32 v89, -v109, v59, v95
	v_mov_b32_e32 v202, v109
	v_pk_fma_f32 v[94:95], v[202:203], v[60:61], v[96:97] op_sel_hi:[0,1,1] neg_lo:[1,0,0] neg_hi:[1,0,0]
	v_pk_fma_f32 v[96:97], v[202:203], v[62:63], v[98:99] op_sel_hi:[0,1,1] neg_lo:[1,0,0] neg_hi:[1,0,0]
	v_pk_fma_f32 v[98:99], v[202:203], v[64:65], v[100:101] op_sel_hi:[0,1,1] neg_lo:[1,0,0] neg_hi:[1,0,0]
	v_pk_fma_f32 v[100:101], v[202:203], v[66:67], v[102:103] op_sel_hi:[0,1,1] neg_lo:[1,0,0] neg_hi:[1,0,0]
	v_pk_fma_f32 v[102:103], v[202:203], v[68:69], v[104:105] op_sel_hi:[0,1,1] neg_lo:[1,0,0] neg_hi:[1,0,0]
	v_pk_fma_f32 v[86:87], v[202:203], v[90:91], v[86:87] op_sel_hi:[0,1,1] neg_lo:[1,0,0] neg_hi:[1,0,0]
	v_fma_f32 v88, -v109, v92, v88
	v_fma_f32 v4, -v109, v93, v4
	ds_read_b128 v[54:57], v21 offset:13248
	ds_read_b128 v[58:61], v21 offset:13264
	ds_read_b128 v[62:65], v21 offset:13280
	ds_read_b128 v[66:69], v21 offset:13296
	v_fma_f32 v5, -v50, v70, v5
	v_fma_f32 v89, -v50, v71, v89
	v_pk_fma_f32 v[90:91], v[50:51], v[72:73], v[94:95] op_sel_hi:[0,1,1] neg_lo:[1,0,0] neg_hi:[1,0,0]
	v_pk_fma_f32 v[92:93], v[50:51], v[74:75], v[96:97] op_sel_hi:[0,1,1] neg_lo:[1,0,0] neg_hi:[1,0,0]
	v_pk_fma_f32 v[94:95], v[50:51], v[76:77], v[98:99] op_sel_hi:[0,1,1] neg_lo:[1,0,0] neg_hi:[1,0,0]
	v_pk_fma_f32 v[96:97], v[50:51], v[78:79], v[100:101] op_sel_hi:[0,1,1] neg_lo:[1,0,0] neg_hi:[1,0,0]
	v_pk_fma_f32 v[98:99], v[50:51], v[80:81], v[102:103] op_sel_hi:[0,1,1] neg_lo:[1,0,0] neg_hi:[1,0,0]
	v_pk_fma_f32 v[86:87], v[50:51], v[82:83], v[86:87] op_sel_hi:[0,1,1] neg_lo:[1,0,0] neg_hi:[1,0,0]
	v_fma_f32 v88, -v50, v84, v88
	v_fma_f32 v4, -v50, v85, v4
	ds_read_b128 v[70:73], v21 offset:13520
	ds_read_b128 v[74:77], v21 offset:13536
	ds_read_b128 v[78:81], v21 offset:13552
	ds_read_b128 v[82:85], v21 offset:13568
	s_waitcnt lgkmcnt(0)
	v_fma_f32 v54, -v5, v54, v5
	v_fma_f32 v55, -v5, v55, v89
	v_mov_b32_e32 v202, v5
	v_pk_fma_f32 v[56:57], v[202:203], v[56:57], v[90:91] op_sel_hi:[0,1,1] neg_lo:[1,0,0] neg_hi:[1,0,0]
	v_pk_fma_f32 v[90:91], v[202:203], v[58:59], v[92:93] op_sel_hi:[0,1,1] neg_lo:[1,0,0] neg_hi:[1,0,0]
	v_pk_fma_f32 v[92:93], v[202:203], v[60:61], v[94:95] op_sel_hi:[0,1,1] neg_lo:[1,0,0] neg_hi:[1,0,0]
	v_pk_fma_f32 v[94:95], v[202:203], v[62:63], v[96:97] op_sel_hi:[0,1,1] neg_lo:[1,0,0] neg_hi:[1,0,0]
	v_pk_fma_f32 v[96:97], v[202:203], v[64:65], v[98:99] op_sel_hi:[0,1,1] neg_lo:[1,0,0] neg_hi:[1,0,0]
	v_pk_fma_f32 v[98:99], v[202:203], v[66:67], v[86:87] op_sel_hi:[0,1,1] neg_lo:[1,0,0] neg_hi:[1,0,0]
	v_fma_f32 v100, -v5, v68, v88
	v_fma_f32 v4, -v5, v69, v4
	ds_read_b128 v[58:61], v21 offset:13792
	ds_read_b128 v[62:65], v21 offset:13808
	ds_read_b128 v[66:69], v21 offset:13824
	ds_read_b128 v[86:89], v21 offset:13840
	v_fma_f32 v5, -v55, v70, v54
	v_fma_f32 v54, -v55, v71, v55
	v_fma_f32 v101, -v55, v72, v56
	v_fma_f32 v102, -v55, v73, v57
	v_mov_b32_e32 v202, v55
	v_pk_fma_f32 v[90:91], v[202:203], v[74:75], v[90:91] op_sel_hi:[0,1,1] neg_lo:[1,0,0] neg_hi:[1,0,0]
	v_pk_fma_f32 v[92:93], v[202:203], v[76:77], v[92:93] op_sel_hi:[0,1,1] neg_lo:[1,0,0] neg_hi:[1,0,0]
	v_pk_fma_f32 v[94:95], v[202:203], v[78:79], v[94:95] op_sel_hi:[0,1,1] neg_lo:[1,0,0] neg_hi:[1,0,0]
	v_pk_fma_f32 v[96:97], v[202:203], v[80:81], v[96:97] op_sel_hi:[0,1,1] neg_lo:[1,0,0] neg_hi:[1,0,0]
	v_pk_fma_f32 v[82:83], v[202:203], v[82:83], v[98:99] op_sel_hi:[0,1,1] neg_lo:[1,0,0] neg_hi:[1,0,0]
	v_fma_f32 v84, -v55, v84, v100
	v_fma_f32 v4, -v55, v85, v4
	ds_read_b128 v[70:73], v21 offset:14080
	ds_read_b128 v[74:77], v21 offset:14096
	ds_read_b128 v[78:81], v21 offset:14112
	s_waitcnt lgkmcnt(0)
	v_fma_f32 v57, -v101, v58, v5
	v_fma_f32 v56, -v101, v59, v54
	v_fma_f32 v55, -v101, v60, v101
	v_fma_f32 v54, -v101, v61, v102
	v_fma_f32 v5, -v101, v62, v90
	v_fma_f32 v85, -v101, v63, v91
	v_mov_b32_e32 v202, v101
	v_pk_fma_f32 v[90:91], v[202:203], v[64:65], v[92:93] op_sel_hi:[0,1,1] neg_lo:[1,0,0] neg_hi:[1,0,0]
	v_pk_fma_f32 v[92:93], v[202:203], v[66:67], v[94:95] op_sel_hi:[0,1,1] neg_lo:[1,0,0] neg_hi:[1,0,0]
	v_pk_fma_f32 v[94:95], v[202:203], v[68:69], v[96:97] op_sel_hi:[0,1,1] neg_lo:[1,0,0] neg_hi:[1,0,0]
	v_pk_fma_f32 v[82:83], v[202:203], v[86:87], v[82:83] op_sel_hi:[0,1,1] neg_lo:[1,0,0] neg_hi:[1,0,0]
	v_fma_f32 v84, -v101, v88, v84
	v_fma_f32 v4, -v101, v89, v4
	ds_read_b128 v[58:61], v21 offset:14352
	ds_read_b128 v[62:65], v21 offset:14368
	ds_read_b128 v[66:69], v21 offset:14384
	v_fma_f32 v5, -v54, v70, v5
	v_fma_f32 v85, -v54, v71, v85
	v_pk_fma_f32 v[86:87], v[54:55], v[72:73], v[90:91] op_sel_hi:[0,1,1] neg_lo:[1,0,0] neg_hi:[1,0,0]
	v_pk_fma_f32 v[88:89], v[54:55], v[74:75], v[92:93] op_sel_hi:[0,1,1] neg_lo:[1,0,0] neg_hi:[1,0,0]
	v_pk_fma_f32 v[90:91], v[54:55], v[76:77], v[94:95] op_sel_hi:[0,1,1] neg_lo:[1,0,0] neg_hi:[1,0,0]
	v_pk_fma_f32 v[82:83], v[54:55], v[78:79], v[82:83] op_sel_hi:[0,1,1] neg_lo:[1,0,0] neg_hi:[1,0,0]
	v_fma_f32 v84, -v54, v80, v84
	v_fma_f32 v4, -v54, v81, v4
	ds_read_b128 v[70:73], v21 offset:14624
	ds_read_b128 v[74:77], v21 offset:14640
	ds_read_b128 v[78:81], v21 offset:14656
	s_waitcnt lgkmcnt(0)
	v_fma_f32 v58, -v5, v58, v5
	v_fma_f32 v59, -v5, v59, v85
	v_mov_b32_e32 v202, v5
	v_pk_fma_f32 v[60:61], v[202:203], v[60:61], v[86:87] op_sel_hi:[0,1,1] neg_lo:[1,0,0] neg_hi:[1,0,0]
	v_pk_fma_f32 v[86:87], v[202:203], v[62:63], v[88:89] op_sel_hi:[0,1,1] neg_lo:[1,0,0] neg_hi:[1,0,0]
	v_pk_fma_f32 v[88:89], v[202:203], v[64:65], v[90:91] op_sel_hi:[0,1,1] neg_lo:[1,0,0] neg_hi:[1,0,0]
	v_pk_fma_f32 v[90:91], v[202:203], v[66:67], v[82:83] op_sel_hi:[0,1,1] neg_lo:[1,0,0] neg_hi:[1,0,0]
	v_fma_f32 v92, -v5, v68, v84
	v_fma_f32 v4, -v5, v69, v4
	ds_read_b128 v[62:65], v21 offset:14896
	ds_read_b128 v[66:69], v21 offset:14912
	ds_read_b128 v[82:85], v21 offset:14928
	v_fma_f32 v5, -v59, v70, v58
	v_fma_f32 v58, -v59, v71, v59
	v_fma_f32 v93, -v59, v72, v60
	v_fma_f32 v94, -v59, v73, v61
	v_mov_b32_e32 v202, v59
	v_pk_fma_f32 v[86:87], v[202:203], v[74:75], v[86:87] op_sel_hi:[0,1,1] neg_lo:[1,0,0] neg_hi:[1,0,0]
	v_pk_fma_f32 v[88:89], v[202:203], v[76:77], v[88:89] op_sel_hi:[0,1,1] neg_lo:[1,0,0] neg_hi:[1,0,0]
	v_pk_fma_f32 v[78:79], v[202:203], v[78:79], v[90:91] op_sel_hi:[0,1,1] neg_lo:[1,0,0] neg_hi:[1,0,0]
	v_fma_f32 v80, -v59, v80, v92
	v_fma_f32 v4, -v59, v81, v4
	ds_read_b128 v[70:73], v21 offset:15184
	ds_read_b128 v[74:77], v21 offset:15200
	s_waitcnt lgkmcnt(0)
	v_fma_f32 v61, -v93, v62, v5
	v_fma_f32 v60, -v93, v63, v58
	v_fma_f32 v59, -v93, v64, v93
	v_fma_f32 v58, -v93, v65, v94
	v_fma_f32 v5, -v93, v66, v86
	v_fma_f32 v81, -v93, v67, v87
	v_mov_b32_e32 v202, v93
	v_pk_fma_f32 v[86:87], v[202:203], v[68:69], v[88:89] op_sel_hi:[0,1,1] neg_lo:[1,0,0] neg_hi:[1,0,0]
	v_pk_fma_f32 v[78:79], v[202:203], v[82:83], v[78:79] op_sel_hi:[0,1,1] neg_lo:[1,0,0] neg_hi:[1,0,0]
	v_fma_f32 v80, -v93, v84, v80
	v_fma_f32 v4, -v93, v85, v4
	ds_read_b128 v[62:65], v21 offset:15456
	ds_read_b128 v[66:69], v21 offset:15472
	v_fma_f32 v5, -v58, v70, v5
	v_fma_f32 v81, -v58, v71, v81
	v_pk_fma_f32 v[82:83], v[58:59], v[72:73], v[86:87] op_sel_hi:[0,1,1] neg_lo:[1,0,0] neg_hi:[1,0,0]
	v_pk_fma_f32 v[78:79], v[58:59], v[74:75], v[78:79] op_sel_hi:[0,1,1] neg_lo:[1,0,0] neg_hi:[1,0,0]
	v_fma_f32 v80, -v58, v76, v80
	v_fma_f32 v4, -v58, v77, v4
	ds_read_b128 v[70:73], v21 offset:15728
	ds_read_b128 v[74:77], v21 offset:15744
	s_waitcnt lgkmcnt(0)
	v_mov_b32_e32 v202, v5
	v_pk_fma_f32 v[66:67], v[202:203], v[66:67], v[78:79] op_sel_hi:[0,1,1] neg_lo:[1,0,0] neg_hi:[1,0,0]
	v_fma_f32 v68, -v5, v68, v80
	v_fma_f32 v84, -v5, v62, v5
	v_fma_f32 v85, -v5, v63, v81
	v_pk_fma_f32 v[82:83], v[202:203], v[64:65], v[82:83] op_sel_hi:[0,1,1] neg_lo:[1,0,0] neg_hi:[1,0,0]
	v_fma_f32 v4, -v5, v69, v4
	ds_read_b128 v[62:65], v21 offset:16000
	ds_read_b128 v[78:81], v21 offset:16016
	v_fma_f32 v5, -v85, v70, v84
	v_fma_f32 v84, -v85, v71, v85
	v_mov_b32_e32 v202, v85
	v_pk_fma_f32 v[72:73], v[202:203], v[72:73], v[82:83] op_sel_hi:[0,1,1] neg_lo:[1,0,0] neg_hi:[1,0,0]
	v_pk_fma_f32 v[74:75], v[202:203], v[74:75], v[66:67] op_sel_hi:[0,1,1] neg_lo:[1,0,0] neg_hi:[1,0,0]
	v_fma_f32 v76, -v85, v76, v68
	v_fma_f32 v4, -v85, v77, v4
	ds_read_b128 v[68:71], v21 offset:16288
	s_waitcnt lgkmcnt(0)
	v_fma_f32 v67, -v72, v62, v5
	v_fma_f32 v66, -v72, v63, v84
	v_fma_f32 v63, -v72, v64, v72
	v_fma_f32 v62, -v72, v65, v73
	v_fma_f32 v64, -v72, v79, v75
	v_fma_f32 v65, -v72, v80, v76
	v_fma_f32 v5, -v72, v78, v74
	v_fma_f32 v4, -v72, v81, v4
	ds_read_b128 v[72:75], v21 offset:16560
	v_fma_f32 v64, -v62, v69, v64
	v_fma_f32 v65, -v62, v70, v65
	v_fma_f32 v5, -v62, v68, v5
	v_fma_f32 v4, -v62, v71, v4
	ds_read_b128 v[68:71], v21 offset:16832
	s_waitcnt lgkmcnt(0)
	v_fma_f32 v64, -v5, v73, v64
	v_fma_f32 v65, -v5, v74, v65
	v_fma_f32 v76, -v5, v72, v5
	v_fma_f32 v4, -v5, v75, v4
	ds_read_b128 v[72:75], v21 offset:17104
	v_fma_f32 v5, -v64, v68, v76
	v_fma_f32 v21, -v64, v69, v64
	v_fma_f32 v70, -v64, v70, v65
	v_fma_f32 v4, -v64, v71, v4
	s_waitcnt lgkmcnt(0)
	v_fma_f32 v69, -v70, v72, v5
	v_fma_f32 v68, -v70, v73, v21
	v_fma_f32 v65, -v70, v74, v70
	v_fma_f32 v64, -v70, v75, v4
	s_and_saveexec_b64 s[4:5], vcc
	s_xor_b64 s[4:5], exec, s[4:5]
	s_cbranch_execz .LBB0_375
	s_ashr_i32 s15, s14, 31
	s_lshl_b64 s[16:17], s[14:15], 10
	s_add_u32 s15, s12, s16
	s_addc_u32 s17, s13, s17
	s_lshl_b32 s16, s35, 1
	s_add_u32 s16, s15, s16
	s_addc_u32 s17, s17, 0
	v_mov_b32_e32 v21, v3
	v_lshl_add_u64 v[4:5], v[20:21], 1, s[16:17]
	s_mov_b32 s15, 0x439ff000
	v_add_co_u32_e32 v20, vcc, s15, v4
	v_cvt_pk_bf16_f32 v7, v7, s0
	s_nop 0
	v_addc_co_u32_e32 v21, vcc, 0, v5, vcc
	s_mov_b32 s15, 0x43a00000
	global_store_short v[20:21], v7, off offset:3840
	v_cvt_pk_bf16_f32 v20, v6, s0
	v_add_co_u32_e32 v6, vcc, s15, v4
	v_cvt_pk_bf16_f32 v1, v1, s0
	s_nop 0
	v_addc_co_u32_e32 v7, vcc, 0, v5, vcc
	v_cvt_pk_bf16_f32 v2, v2, s0
	global_store_short v[6:7], v1, off offset:2816
	v_cvt_pk_bf16_f32 v1, v11, s0
	s_mov_b32 s15, 0x43a01000
	global_store_short v[6:7], v20, off offset:768
	global_store_short v[6:7], v2, off offset:1792
	global_store_short v[6:7], v1, off offset:3840
	v_add_co_u32_e32 v6, vcc, s15, v4
	v_cvt_pk_bf16_f32 v1, v10, s0
	s_nop 0
	v_addc_co_u32_e32 v7, vcc, 0, v5, vcc
	global_store_short v[6:7], v1, off offset:768
	v_cvt_pk_bf16_f32 v1, v9, s0
	global_store_short v[6:7], v1, off offset:1792
	v_cvt_pk_bf16_f32 v1, v8, s0
	global_store_short v[6:7], v1, off offset:2816
	v_cvt_pk_bf16_f32 v1, v15, s0
	s_mov_b32 s15, 0x43a02000
	global_store_short v[6:7], v1, off offset:3840
	v_add_co_u32_e32 v6, vcc, s15, v4
	v_cvt_pk_bf16_f32 v1, v14, s0
	s_nop 0
	v_addc_co_u32_e32 v7, vcc, 0, v5, vcc
	global_store_short v[6:7], v1, off offset:768
	v_cvt_pk_bf16_f32 v1, v13, s0
	global_store_short v[6:7], v1, off offset:1792
	v_cvt_pk_bf16_f32 v1, v12, s0
	global_store_short v[6:7], v1, off offset:2816
	v_cvt_pk_bf16_f32 v1, v19, s0
	s_mov_b32 s15, 0x43a03000
	global_store_short v[6:7], v1, off offset:3840
	v_add_co_u32_e32 v6, vcc, s15, v4
	v_cvt_pk_bf16_f32 v1, v18, s0
	s_nop 0
	v_addc_co_u32_e32 v7, vcc, 0, v5, vcc
	global_store_short v[6:7], v1, off offset:768
	v_cvt_pk_bf16_f32 v1, v17, s0
	global_store_short v[6:7], v1, off offset:1792
	v_cvt_pk_bf16_f32 v1, v16, s0
	global_store_short v[6:7], v1, off offset:2816
	v_cvt_pk_bf16_f32 v1, v25, s0
	s_mov_b32 s15, 0x43a04000
	global_store_short v[6:7], v1, off offset:3840
	v_add_co_u32_e32 v6, vcc, s15, v4
	v_cvt_pk_bf16_f32 v1, v24, s0
	s_nop 0
	v_addc_co_u32_e32 v7, vcc, 0, v5, vcc
	global_store_short v[6:7], v1, off offset:768
	v_cvt_pk_bf16_f32 v1, v23, s0
	global_store_short v[6:7], v1, off offset:1792
	v_cvt_pk_bf16_f32 v1, v22, s0
	global_store_short v[6:7], v1, off offset:2816
	v_cvt_pk_bf16_f32 v1, v29, s0
	s_mov_b32 s15, 0x43a05000
	global_store_short v[6:7], v1, off offset:3840
	v_add_co_u32_e32 v6, vcc, s15, v4
	v_cvt_pk_bf16_f32 v1, v28, s0
	s_nop 0
	v_addc_co_u32_e32 v7, vcc, 0, v5, vcc
	global_store_short v[6:7], v1, off offset:768
	v_cvt_pk_bf16_f32 v1, v27, s0
	global_store_short v[6:7], v1, off offset:1792
	v_cvt_pk_bf16_f32 v1, v26, s0
	global_store_short v[6:7], v1, off offset:2816
	v_cvt_pk_bf16_f32 v1, v33, s0
	s_mov_b32 s15, 0x43a06000
	global_store_short v[6:7], v1, off offset:3840
	v_add_co_u32_e32 v6, vcc, s15, v4
	v_cvt_pk_bf16_f32 v1, v32, s0
	s_nop 0
	v_addc_co_u32_e32 v7, vcc, 0, v5, vcc
	global_store_short v[6:7], v1, off offset:768
	v_cvt_pk_bf16_f32 v1, v31, s0
	global_store_short v[6:7], v1, off offset:1792
	v_cvt_pk_bf16_f32 v1, v30, s0
	global_store_short v[6:7], v1, off offset:2816
	v_cvt_pk_bf16_f32 v1, v37, s0
	s_mov_b32 s15, 0x43a07000
	global_store_short v[6:7], v1, off offset:3840
	v_add_co_u32_e32 v6, vcc, s15, v4
	v_cvt_pk_bf16_f32 v1, v36, s0
	s_nop 0
	v_addc_co_u32_e32 v7, vcc, 0, v5, vcc
	global_store_short v[6:7], v1, off offset:768
	v_cvt_pk_bf16_f32 v1, v35, s0
	global_store_short v[6:7], v1, off offset:1792
	v_cvt_pk_bf16_f32 v1, v34, s0
	global_store_short v[6:7], v1, off offset:2816
	v_cvt_pk_bf16_f32 v1, v41, s0
	s_mov_b32 s15, 0x43a08000
	global_store_short v[6:7], v1, off offset:3840
	v_add_co_u32_e32 v6, vcc, s15, v4
	v_cvt_pk_bf16_f32 v1, v40, s0
	s_nop 0
	v_addc_co_u32_e32 v7, vcc, 0, v5, vcc
	global_store_short v[6:7], v1, off offset:768
	v_cvt_pk_bf16_f32 v1, v39, s0
	global_store_short v[6:7], v1, off offset:1792
	v_cvt_pk_bf16_f32 v1, v38, s0
	global_store_short v[6:7], v1, off offset:2816
	v_cvt_pk_bf16_f32 v1, v45, s0
	s_mov_b32 s15, 0x43a09000
	global_store_short v[6:7], v1, off offset:3840
	v_add_co_u32_e32 v6, vcc, s15, v4
	v_cvt_pk_bf16_f32 v1, v44, s0
	s_nop 0
	v_addc_co_u32_e32 v7, vcc, 0, v5, vcc
	global_store_short v[6:7], v1, off offset:768
	v_cvt_pk_bf16_f32 v1, v43, s0
	global_store_short v[6:7], v1, off offset:1792
	v_cvt_pk_bf16_f32 v1, v42, s0
	global_store_short v[6:7], v1, off offset:2816
	v_cvt_pk_bf16_f32 v1, v49, s0
	s_mov_b32 s15, 0x43a0a000
	global_store_short v[6:7], v1, off offset:3840
	v_add_co_u32_e32 v6, vcc, s15, v4
	v_cvt_pk_bf16_f32 v1, v48, s0
	s_nop 0
	v_addc_co_u32_e32 v7, vcc, 0, v5, vcc
	global_store_short v[6:7], v1, off offset:768
	v_cvt_pk_bf16_f32 v1, v47, s0
	global_store_short v[6:7], v1, off offset:1792
	v_cvt_pk_bf16_f32 v1, v46, s0
	global_store_short v[6:7], v1, off offset:2816
	v_cvt_pk_bf16_f32 v1, v53, s0
	s_mov_b32 s15, 0x43a0b000
	global_store_short v[6:7], v1, off offset:3840
	v_add_co_u32_e32 v6, vcc, s15, v4
	v_cvt_pk_bf16_f32 v1, v52, s0
	s_nop 0
	v_addc_co_u32_e32 v7, vcc, 0, v5, vcc
	global_store_short v[6:7], v1, off offset:768
	v_cvt_pk_bf16_f32 v1, v51, s0
	global_store_short v[6:7], v1, off offset:1792
	v_cvt_pk_bf16_f32 v1, v50, s0
	global_store_short v[6:7], v1, off offset:2816
	v_cvt_pk_bf16_f32 v1, v57, s0
	s_mov_b32 s15, 0x43a0c000
	global_store_short v[6:7], v1, off offset:3840
	v_add_co_u32_e32 v6, vcc, s15, v4
	v_cvt_pk_bf16_f32 v1, v56, s0
	s_nop 0
	v_addc_co_u32_e32 v7, vcc, 0, v5, vcc
	global_store_short v[6:7], v1, off offset:768
	v_cvt_pk_bf16_f32 v1, v55, s0
	global_store_short v[6:7], v1, off offset:1792
	v_cvt_pk_bf16_f32 v1, v54, s0
	global_store_short v[6:7], v1, off offset:2816
	v_cvt_pk_bf16_f32 v1, v61, s0
	s_mov_b32 s15, 0x43a0d000
	global_store_short v[6:7], v1, off offset:3840
	v_add_co_u32_e32 v6, vcc, s15, v4
	v_cvt_pk_bf16_f32 v1, v60, s0
	s_nop 0
	v_addc_co_u32_e32 v7, vcc, 0, v5, vcc
	global_store_short v[6:7], v1, off offset:768
	v_cvt_pk_bf16_f32 v1, v59, s0
	global_store_short v[6:7], v1, off offset:1792
	v_cvt_pk_bf16_f32 v1, v58, s0
	global_store_short v[6:7], v1, off offset:2816
	v_cvt_pk_bf16_f32 v1, v67, s0
	s_mov_b32 s15, 0x43a0e000
	global_store_short v[6:7], v1, off offset:3840
	v_add_co_u32_e32 v6, vcc, s15, v4
	v_cvt_pk_bf16_f32 v1, v66, s0
	s_nop 0
	v_addc_co_u32_e32 v7, vcc, 0, v5, vcc
	global_store_short v[6:7], v1, off offset:768
	v_cvt_pk_bf16_f32 v1, v63, s0
	global_store_short v[6:7], v1, off offset:1792
	v_cvt_pk_bf16_f32 v1, v62, s0
	global_store_short v[6:7], v1, off offset:2816
	v_cvt_pk_bf16_f32 v1, v69, s0
	v_add_co_u32_e32 v4, vcc, 0x43a0f000, v4
	global_store_short v[6:7], v1, off offset:3840
	v_cvt_pk_bf16_f32 v1, v68, s0
	v_addc_co_u32_e32 v5, vcc, 0, v5, vcc
	global_store_short v[4:5], v1, off offset:768
	v_cvt_pk_bf16_f32 v1, v65, s0
	global_store_short v[4:5], v1, off offset:1792
	v_cvt_pk_bf16_f32 v1, v64, s0
	global_store_short v[4:5], v1, off offset:2816
